# GEMM loops: no per-block setprio; waves 4-7 (trailing half) run the K-loop at static s_setprio 1
# speedup vs baseline: 1.0048x; 1.0048x over previous
.LBB0_260:
	s_ashr_i32 s69, s68, 31
	s_lshl_b64 s[26:27], s[68:69], 20
	v_readlane_b32 s8, v254, 56
	v_readlane_b32 s9, v254, 57
	s_add_u32 s70, s8, s26
	s_addc_u32 s71, s9, s27
	s_and_b64 s[26:27], s[0:1], exec
	s_cselect_b32 s69, s71, s83
	s_cselect_b32 s75, s70, s82
	s_ashr_i32 s57, s56, 31
	s_lshl_b64 s[26:27], s[56:57], 20
	s_add_u32 s72, s84, s26
	s_addc_u32 s73, s85, s27
	s_and_b64 s[26:27], s[0:1], exec
	s_cselect_b32 s57, s73, s81
	s_cselect_b32 s96, s72, s80
	s_add_u32 s97, s80, 0x10000
	s_addc_u32 vcc_lo, s81, 0
	s_add_u32 s80, s82, 0x80080
	v_mov_b32_e32 v2, 0
	s_addc_u32 s81, s83, 0
	s_mov_b32 vcc_hi, -2
	v_mov_b32_e32 v3, v2
	v_mov_b32_e32 v4, v2
	v_mov_b32_e32 v5, v2
	v_mov_b32_e32 v14, v2
	v_mov_b32_e32 v15, v2
	v_mov_b32_e32 v16, v2
	v_mov_b32_e32 v17, v2
	v_mov_b32_e32 v18, v2
	v_mov_b32_e32 v19, v2
	v_mov_b32_e32 v20, v2
	v_mov_b32_e32 v21, v2
	v_mov_b32_e32 v30, v2
	v_mov_b32_e32 v31, v2
	v_mov_b32_e32 v32, v2
	v_mov_b32_e32 v33, v2
	v_mov_b32_e32 v34, v2
	v_mov_b32_e32 v35, v2
	v_mov_b32_e32 v36, v2
	v_mov_b32_e32 v37, v2
	v_mov_b32_e32 v46, v2
	v_mov_b32_e32 v47, v2
	v_mov_b32_e32 v48, v2
	v_mov_b32_e32 v49, v2
	v_mov_b32_e32 v50, v2
	v_mov_b32_e32 v51, v2
	v_mov_b32_e32 v52, v2
	v_mov_b32_e32 v53, v2
	v_mov_b32_e32 v62, v2
	v_mov_b32_e32 v63, v2
	v_mov_b32_e32 v64, v2
	v_mov_b32_e32 v65, v2
	v_mov_b32_e32 v6, v2
	v_mov_b32_e32 v7, v2
	v_mov_b32_e32 v8, v2
	v_mov_b32_e32 v9, v2
	v_mov_b32_e32 v10, v2
	v_mov_b32_e32 v11, v2
	v_mov_b32_e32 v12, v2
	v_mov_b32_e32 v13, v2
	v_mov_b32_e32 v22, v2
	v_mov_b32_e32 v23, v2
	v_mov_b32_e32 v24, v2
	v_mov_b32_e32 v25, v2
	v_mov_b32_e32 v26, v2
	v_mov_b32_e32 v27, v2
	v_mov_b32_e32 v28, v2
	v_mov_b32_e32 v29, v2
	v_mov_b32_e32 v38, v2
	v_mov_b32_e32 v39, v2
	v_mov_b32_e32 v40, v2
	v_mov_b32_e32 v41, v2
	v_mov_b32_e32 v42, v2
	v_mov_b32_e32 v43, v2
	v_mov_b32_e32 v44, v2
	v_mov_b32_e32 v45, v2
	v_mov_b32_e32 v54, v2
	v_mov_b32_e32 v55, v2
	v_mov_b32_e32 v56, v2
	v_mov_b32_e32 v57, v2
	v_mov_b32_e32 v58, v2
	v_mov_b32_e32 v59, v2
	v_mov_b32_e32 v60, v2
	v_mov_b32_e32 v61, v2
	v_mov_b32_e32 v66, v2
	v_mov_b32_e32 v67, v2
	v_mov_b32_e32 v68, v2
	v_mov_b32_e32 v69, v2
	v_mov_b32_e32 v78, v2
	v_mov_b32_e32 v79, v2
	v_mov_b32_e32 v80, v2
	v_mov_b32_e32 v81, v2
	v_mov_b32_e32 v82, v2
	v_mov_b32_e32 v83, v2
	v_mov_b32_e32 v84, v2
	v_mov_b32_e32 v85, v2
	v_mov_b32_e32 v94, v2
	v_mov_b32_e32 v95, v2
	v_mov_b32_e32 v96, v2
	v_mov_b32_e32 v97, v2
	v_mov_b32_e32 v98, v2
	v_mov_b32_e32 v99, v2
	v_mov_b32_e32 v100, v2
	v_mov_b32_e32 v101, v2
	v_mov_b32_e32 v110, v2
	v_mov_b32_e32 v111, v2
	v_mov_b32_e32 v112, v2
	v_mov_b32_e32 v113, v2
	v_mov_b32_e32 v114, v2
	v_mov_b32_e32 v115, v2
	v_mov_b32_e32 v116, v2
	v_mov_b32_e32 v117, v2
	v_mov_b32_e32 v126, v2
	v_mov_b32_e32 v127, v2
	v_mov_b32_e32 v128, v2
	v_mov_b32_e32 v129, v2
	v_mov_b32_e32 v70, v2
	v_mov_b32_e32 v71, v2
	v_mov_b32_e32 v72, v2
	v_mov_b32_e32 v73, v2
	v_mov_b32_e32 v74, v2
	v_mov_b32_e32 v75, v2
	v_mov_b32_e32 v76, v2
	v_mov_b32_e32 v77, v2
	v_mov_b32_e32 v86, v2
	v_mov_b32_e32 v87, v2
	v_mov_b32_e32 v88, v2
	v_mov_b32_e32 v89, v2
	v_mov_b32_e32 v90, v2
	v_mov_b32_e32 v91, v2
	v_mov_b32_e32 v92, v2
	v_mov_b32_e32 v93, v2
	v_mov_b32_e32 v102, v2
	v_mov_b32_e32 v103, v2
	v_mov_b32_e32 v104, v2
	v_mov_b32_e32 v105, v2
	v_mov_b32_e32 v106, v2
	v_mov_b32_e32 v107, v2
	v_mov_b32_e32 v108, v2
	v_mov_b32_e32 v109, v2
	v_mov_b32_e32 v118, v2
	v_mov_b32_e32 v119, v2
	v_mov_b32_e32 v120, v2
	v_mov_b32_e32 v121, v2
	v_mov_b32_e32 v122, v2
	v_mov_b32_e32 v123, v2
	v_mov_b32_e32 v124, v2
	v_mov_b32_e32 v125, v2
	v_readfirstlane_b32 s98, v0
	s_lshr_b32 s98, s98, 8
	s_cmp_eq_u32 s98, 1
	s_cbranch_scc0 .Lprio_skip9
	s_setprio 1
.Lprio_skip9:
.LBB0_261:
	ds_read_b128 v[144:147], v170
	ds_read_b128 v[148:151], v170 offset:1024
	ds_read_b128 v[174:177], v170 offset:2048
	ds_read_b128 v[178:181], v170 offset:3072
	ds_read_b128 v[182:185], v171
	ds_read_b128 v[186:189], v171 offset:1024
	ds_read_b128 v[190:193], v171 offset:2048
	ds_read_b128 v[194:197], v171 offset:3072
	s_add_u32 s26, s80, 0xfff80080
	s_addc_u32 s27, s81, -1
	s_cmp_eq_u32 vcc_hi, 28
	s_cselect_b32 s83, s69, s27
	s_cselect_b32 s82, s75, s26
	s_cselect_b32 s27, s57, vcc_lo
	s_cselect_b32 s26, s96, s97
	v_lshl_add_u64 v[152:153], s[80:81], 0, v[134:135]
	s_add_i32 m0, s87, 0xc000
	ds_read_b128 v[198:201], v172
	ds_read_b128 v[202:205], v172 offset:1024
	ds_read_b128 v[206:209], v172 offset:2048
	ds_read_b128 v[210:213], v172 offset:3072
	ds_read_b128 v[214:217], v172 offset:4096
	ds_read_b128 v[220:223], v172 offset:5120
	ds_read_b128 v[224:227], v172 offset:6144
	ds_read_b128 v[228:231], v172 offset:7168
	global_load_lds_dwordx4 v[152:153], off
	v_lshl_add_u64 v[152:153], s[80:81], 0, v[138:139]
	s_add_i32 m0, s87, 0xe000
	s_nop 0
	global_load_lds_dwordx4 v[152:153], off
	s_waitcnt vmcnt(8)
	s_waitcnt lgkmcnt(0)
	s_barrier
	s_waitcnt lgkmcnt(0)
	v_mfma_f32_16x16x32_bf16 v[122:125], v[144:147], v[198:201], v[122:125]
	v_mfma_f32_16x16x32_bf16 v[118:121], v[174:177], v[198:201], v[118:121]
	v_mfma_f32_16x16x32_bf16 v[106:109], v[144:147], v[206:209], v[106:109]
	v_mfma_f32_16x16x32_bf16 v[102:105], v[174:177], v[206:209], v[102:105]
	v_mfma_f32_16x16x32_bf16 v[90:93], v[144:147], v[214:217], v[90:93]
	v_mfma_f32_16x16x32_bf16 v[86:89], v[174:177], v[214:217], v[86:89]
	v_mfma_f32_16x16x32_bf16 v[74:77], v[144:147], v[224:227], v[74:77]
	v_mfma_f32_16x16x32_bf16 v[70:73], v[174:177], v[224:227], v[70:73]
	v_mfma_f32_16x16x32_bf16 v[122:125], v[148:151], v[202:205], v[122:125]
	v_mfma_f32_16x16x32_bf16 v[118:121], v[178:181], v[202:205], v[118:121]
	v_mfma_f32_16x16x32_bf16 v[106:109], v[148:151], v[210:213], v[106:109]
	v_mfma_f32_16x16x32_bf16 v[102:105], v[178:181], v[210:213], v[102:105]
	v_mfma_f32_16x16x32_bf16 v[90:93], v[148:151], v[220:223], v[90:93]
	v_mfma_f32_16x16x32_bf16 v[86:89], v[178:181], v[220:223], v[86:89]
	v_mfma_f32_16x16x32_bf16 v[74:77], v[148:151], v[228:231], v[74:77]
	v_mfma_f32_16x16x32_bf16 v[70:73], v[178:181], v[228:231], v[70:73]
	v_mfma_f32_16x16x32_bf16 v[126:129], v[182:185], v[198:201], v[126:129]
	v_mfma_f32_16x16x32_bf16 v[114:117], v[190:193], v[198:201], v[114:117]
	v_mfma_f32_16x16x32_bf16 v[110:113], v[182:185], v[206:209], v[110:113]
	v_mfma_f32_16x16x32_bf16 v[98:101], v[190:193], v[206:209], v[98:101]
	v_mfma_f32_16x16x32_bf16 v[94:97], v[182:185], v[214:217], v[94:97]
	v_mfma_f32_16x16x32_bf16 v[82:85], v[190:193], v[214:217], v[82:85]
	v_mfma_f32_16x16x32_bf16 v[78:81], v[182:185], v[224:227], v[78:81]
	v_mfma_f32_16x16x32_bf16 v[66:69], v[190:193], v[224:227], v[66:69]
	v_mfma_f32_16x16x32_bf16 v[126:129], v[186:189], v[202:205], v[126:129]
	v_mfma_f32_16x16x32_bf16 v[114:117], v[194:197], v[202:205], v[114:117]
	v_mfma_f32_16x16x32_bf16 v[110:113], v[186:189], v[210:213], v[110:113]
	v_mfma_f32_16x16x32_bf16 v[98:101], v[194:197], v[210:213], v[98:101]
	v_mfma_f32_16x16x32_bf16 v[94:97], v[186:189], v[220:223], v[94:97]
	v_mfma_f32_16x16x32_bf16 v[82:85], v[194:197], v[220:223], v[82:85]
	v_mfma_f32_16x16x32_bf16 v[78:81], v[186:189], v[228:231], v[78:81]
	v_mfma_f32_16x16x32_bf16 v[66:69], v[194:197], v[228:231], v[66:69]
	s_barrier
	v_lshl_add_u64 v[152:153], s[26:27], 0, v[162:163]
	s_add_i32 s26, s94, s86
	s_mov_b32 m0, s26
	ds_read_b128 v[198:201], v172 offset:16384
	ds_read_b128 v[202:205], v172 offset:17408
	ds_read_b128 v[206:209], v172 offset:18432
	ds_read_b128 v[210:213], v172 offset:19456
	ds_read_b128 v[214:217], v172 offset:20480
	ds_read_b128 v[220:223], v172 offset:21504
	ds_read_b128 v[224:227], v172 offset:22528
	ds_read_b128 v[228:231], v172 offset:23552
	global_load_lds_dwordx4 v[152:153], off
	v_lshl_add_u64 v[232:233], v[152:153], 0, s[10:11]
	s_add_i32 m0, s26, 0x2000
	s_add_i32 s26, s95, s86
	global_load_lds_dwordx4 v[232:233], off
	v_lshl_add_u64 v[232:233], v[152:153], 0, s[12:13]
	s_mov_b32 m0, s26
	v_lshl_add_u64 v[234:235], s[82:83], 0, v[132:133]
	global_load_lds_dwordx4 v[232:233], off
	v_lshl_add_u64 v[232:233], v[152:153], 0, s[14:15]
	s_add_i32 m0, s26, 0x2000
	s_nop 0
	global_load_lds_dwordx4 v[232:233], off
	v_lshl_add_u64 v[232:233], s[82:83], 0, v[130:131]
	s_mov_b32 m0, s87
	s_nop 0
	global_load_lds_dwordx4 v[232:233], off
	s_mov_b32 m0, s88
	s_nop 0
	global_load_lds_dwordx4 v[234:235], off
	s_waitcnt vmcnt(8)
	s_waitcnt lgkmcnt(0)
	s_barrier
	s_waitcnt lgkmcnt(0)
	v_mfma_f32_16x16x32_bf16 v[58:61], v[144:147], v[198:201], v[58:61]
	v_mfma_f32_16x16x32_bf16 v[54:57], v[174:177], v[198:201], v[54:57]
	v_mfma_f32_16x16x32_bf16 v[42:45], v[144:147], v[206:209], v[42:45]
	v_mfma_f32_16x16x32_bf16 v[38:41], v[174:177], v[206:209], v[38:41]
	v_mfma_f32_16x16x32_bf16 v[26:29], v[144:147], v[214:217], v[26:29]
	v_mfma_f32_16x16x32_bf16 v[22:25], v[174:177], v[214:217], v[22:25]
	v_mfma_f32_16x16x32_bf16 v[10:13], v[144:147], v[224:227], v[10:13]
	v_mfma_f32_16x16x32_bf16 v[6:9], v[174:177], v[224:227], v[6:9]
	v_mfma_f32_16x16x32_bf16 v[58:61], v[148:151], v[202:205], v[58:61]
	v_mfma_f32_16x16x32_bf16 v[54:57], v[178:181], v[202:205], v[54:57]
	v_mfma_f32_16x16x32_bf16 v[42:45], v[148:151], v[210:213], v[42:45]
	v_mfma_f32_16x16x32_bf16 v[38:41], v[178:181], v[210:213], v[38:41]
	v_mfma_f32_16x16x32_bf16 v[26:29], v[148:151], v[220:223], v[26:29]
	v_mfma_f32_16x16x32_bf16 v[22:25], v[178:181], v[220:223], v[22:25]
	v_mfma_f32_16x16x32_bf16 v[10:13], v[148:151], v[228:231], v[10:13]
	v_mfma_f32_16x16x32_bf16 v[6:9], v[178:181], v[228:231], v[6:9]
	v_mfma_f32_16x16x32_bf16 v[62:65], v[182:185], v[198:201], v[62:65]
	v_mfma_f32_16x16x32_bf16 v[50:53], v[190:193], v[198:201], v[50:53]
	v_mfma_f32_16x16x32_bf16 v[46:49], v[182:185], v[206:209], v[46:49]
	v_mfma_f32_16x16x32_bf16 v[34:37], v[190:193], v[206:209], v[34:37]
	v_mfma_f32_16x16x32_bf16 v[30:33], v[182:185], v[214:217], v[30:33]
	v_mfma_f32_16x16x32_bf16 v[18:21], v[190:193], v[214:217], v[18:21]
	v_mfma_f32_16x16x32_bf16 v[14:17], v[182:185], v[224:227], v[14:17]
	v_mfma_f32_16x16x32_bf16 v[2:5], v[190:193], v[224:227], v[2:5]
	v_mfma_f32_16x16x32_bf16 v[62:65], v[186:189], v[202:205], v[62:65]
	v_mfma_f32_16x16x32_bf16 v[50:53], v[194:197], v[202:205], v[50:53]
	v_mfma_f32_16x16x32_bf16 v[46:49], v[186:189], v[210:213], v[46:49]
	v_mfma_f32_16x16x32_bf16 v[34:37], v[194:197], v[210:213], v[34:37]
	v_mfma_f32_16x16x32_bf16 v[30:33], v[186:189], v[220:223], v[30:33]
	v_mfma_f32_16x16x32_bf16 v[18:21], v[194:197], v[220:223], v[18:21]
	v_mfma_f32_16x16x32_bf16 v[14:17], v[186:189], v[228:231], v[14:17]
	v_mfma_f32_16x16x32_bf16 v[2:5], v[194:197], v[228:231], v[2:5]
	s_barrier
	s_add_i32 s33, 0, 0x18000
	v_add_u32_e32 v136, s33, v167
	s_add_i32 s8, 0, 0x1c000
	ds_read_b128 v[144:147], v136
	ds_read_b128 v[148:151], v136 offset:1024
	ds_read_b128 v[174:177], v136 offset:2048
	ds_read_b128 v[178:181], v136 offset:3072
	v_add_u32_e32 v136, s8, v167
	ds_read_b128 v[182:185], v136
	ds_read_b128 v[186:189], v136 offset:1024
	ds_read_b128 v[190:193], v136 offset:2048
	ds_read_b128 v[194:197], v136 offset:3072
	s_add_u32 s26, s82, 0x80000
	s_addc_u32 s27, s83, 0
	s_mov_b32 m0, s89
	v_lshl_add_u64 v[236:237], s[26:27], 0, v[130:131]
	ds_read_b128 v[198:201], v172 offset:32768
	ds_read_b128 v[202:205], v172 offset:33792
	ds_read_b128 v[206:209], v172 offset:34816
	ds_read_b128 v[210:213], v172 offset:35840
	ds_read_b128 v[214:217], v172 offset:36864
	ds_read_b128 v[220:223], v172 offset:37888
	ds_read_b128 v[224:227], v172 offset:38912
	ds_read_b128 v[228:231], v172 offset:39936
	global_load_lds_dwordx4 v[236:237], off
	v_lshl_add_u64 v[236:237], s[26:27], 0, v[132:133]
	s_mov_b32 m0, s90
	s_nop 0
	global_load_lds_dwordx4 v[236:237], off
	s_waitcnt vmcnt(8)
	s_waitcnt lgkmcnt(0)
	s_barrier
	s_waitcnt lgkmcnt(0)
	v_mfma_f32_16x16x32_bf16 v[122:125], v[144:147], v[198:201], v[122:125]
	v_mfma_f32_16x16x32_bf16 v[118:121], v[174:177], v[198:201], v[118:121]
	v_mfma_f32_16x16x32_bf16 v[106:109], v[144:147], v[206:209], v[106:109]
	v_mfma_f32_16x16x32_bf16 v[102:105], v[174:177], v[206:209], v[102:105]
	v_mfma_f32_16x16x32_bf16 v[90:93], v[144:147], v[214:217], v[90:93]
	v_mfma_f32_16x16x32_bf16 v[86:89], v[174:177], v[214:217], v[86:89]
	v_mfma_f32_16x16x32_bf16 v[74:77], v[144:147], v[224:227], v[74:77]
	v_mfma_f32_16x16x32_bf16 v[70:73], v[174:177], v[224:227], v[70:73]
	v_mfma_f32_16x16x32_bf16 v[122:125], v[148:151], v[202:205], v[122:125]
	v_mfma_f32_16x16x32_bf16 v[118:121], v[178:181], v[202:205], v[118:121]
	v_mfma_f32_16x16x32_bf16 v[106:109], v[148:151], v[210:213], v[106:109]
	v_mfma_f32_16x16x32_bf16 v[102:105], v[178:181], v[210:213], v[102:105]
	v_mfma_f32_16x16x32_bf16 v[90:93], v[148:151], v[220:223], v[90:93]
	v_mfma_f32_16x16x32_bf16 v[86:89], v[178:181], v[220:223], v[86:89]
	v_mfma_f32_16x16x32_bf16 v[74:77], v[148:151], v[228:231], v[74:77]
	v_mfma_f32_16x16x32_bf16 v[70:73], v[178:181], v[228:231], v[70:73]
	v_mfma_f32_16x16x32_bf16 v[126:129], v[182:185], v[198:201], v[126:129]
	v_mfma_f32_16x16x32_bf16 v[114:117], v[190:193], v[198:201], v[114:117]
	v_mfma_f32_16x16x32_bf16 v[110:113], v[182:185], v[206:209], v[110:113]
	v_mfma_f32_16x16x32_bf16 v[98:101], v[190:193], v[206:209], v[98:101]
	v_mfma_f32_16x16x32_bf16 v[94:97], v[182:185], v[214:217], v[94:97]
	v_mfma_f32_16x16x32_bf16 v[82:85], v[190:193], v[214:217], v[82:85]
	v_mfma_f32_16x16x32_bf16 v[78:81], v[182:185], v[224:227], v[78:81]
	v_mfma_f32_16x16x32_bf16 v[66:69], v[190:193], v[224:227], v[66:69]
	v_mfma_f32_16x16x32_bf16 v[126:129], v[186:189], v[202:205], v[126:129]
	v_mfma_f32_16x16x32_bf16 v[114:117], v[194:197], v[202:205], v[114:117]
	v_mfma_f32_16x16x32_bf16 v[110:113], v[186:189], v[210:213], v[110:113]
	v_mfma_f32_16x16x32_bf16 v[98:101], v[194:197], v[210:213], v[98:101]
	v_mfma_f32_16x16x32_bf16 v[94:97], v[186:189], v[220:223], v[94:97]
	v_mfma_f32_16x16x32_bf16 v[82:85], v[194:197], v[220:223], v[82:85]
	v_mfma_f32_16x16x32_bf16 v[78:81], v[186:189], v[228:231], v[78:81]
	v_mfma_f32_16x16x32_bf16 v[66:69], v[194:197], v[228:231], v[66:69]
	s_barrier
	s_add_i32 s9, s33, s86
	v_lshl_add_u64 v[236:237], v[152:153], 0, s[20:21]
	s_mov_b32 m0, s9
	ds_read_b128 v[198:201], v172 offset:49152
	ds_read_b128 v[202:205], v172 offset:50176
	ds_read_b128 v[206:209], v172 offset:51200
	ds_read_b128 v[210:213], v172 offset:52224
	ds_read_b128 v[214:217], v172 offset:53248
	ds_read_b128 v[220:223], v172 offset:54272
	ds_read_b128 v[224:227], v172 offset:55296
	ds_read_b128 v[228:231], v172 offset:56320
	global_load_lds_dwordx4 v[236:237], off
	v_lshl_add_u64 v[236:237], v[152:153], 0, s[22:23]
	s_add_i32 m0, s9, 0x2000
	s_add_i32 s8, s8, s86
	global_load_lds_dwordx4 v[236:237], off
	v_lshl_add_u64 v[236:237], v[152:153], 0, s[40:41]
	s_mov_b32 m0, s8
	v_lshl_add_u64 v[152:153], v[152:153], 0, s[44:45]
	global_load_lds_dwordx4 v[236:237], off
	s_add_i32 m0, s8, 0x2000
	s_nop 0
	global_load_lds_dwordx4 v[152:153], off
	v_lshl_add_u64 v[152:153], v[232:233], 0, s[24:25]
	s_mov_b32 m0, s91
	s_nop 0
	global_load_lds_dwordx4 v[152:153], off
	v_lshl_add_u64 v[152:153], v[234:235], 0, s[24:25]
	s_mov_b32 m0, s92
	s_nop 0
	global_load_lds_dwordx4 v[152:153], off
	s_waitcnt vmcnt(8)
	s_waitcnt lgkmcnt(0)
	s_barrier
	s_waitcnt lgkmcnt(0)
	v_mfma_f32_16x16x32_bf16 v[58:61], v[144:147], v[198:201], v[58:61]
	v_mfma_f32_16x16x32_bf16 v[54:57], v[174:177], v[198:201], v[54:57]
	v_mfma_f32_16x16x32_bf16 v[42:45], v[144:147], v[206:209], v[42:45]
	v_mfma_f32_16x16x32_bf16 v[38:41], v[174:177], v[206:209], v[38:41]
	v_mfma_f32_16x16x32_bf16 v[26:29], v[144:147], v[214:217], v[26:29]
	v_mfma_f32_16x16x32_bf16 v[22:25], v[174:177], v[214:217], v[22:25]
	v_mfma_f32_16x16x32_bf16 v[10:13], v[144:147], v[224:227], v[10:13]
	v_mfma_f32_16x16x32_bf16 v[6:9], v[174:177], v[224:227], v[6:9]
	v_mfma_f32_16x16x32_bf16 v[58:61], v[148:151], v[202:205], v[58:61]
	v_mfma_f32_16x16x32_bf16 v[54:57], v[178:181], v[202:205], v[54:57]
	v_mfma_f32_16x16x32_bf16 v[42:45], v[148:151], v[210:213], v[42:45]
	v_mfma_f32_16x16x32_bf16 v[38:41], v[178:181], v[210:213], v[38:41]
	v_mfma_f32_16x16x32_bf16 v[26:29], v[148:151], v[220:223], v[26:29]
	v_mfma_f32_16x16x32_bf16 v[22:25], v[178:181], v[220:223], v[22:25]
	v_mfma_f32_16x16x32_bf16 v[10:13], v[148:151], v[228:231], v[10:13]
	v_mfma_f32_16x16x32_bf16 v[6:9], v[178:181], v[228:231], v[6:9]
	v_mfma_f32_16x16x32_bf16 v[62:65], v[182:185], v[198:201], v[62:65]
	v_mfma_f32_16x16x32_bf16 v[50:53], v[190:193], v[198:201], v[50:53]
	v_mfma_f32_16x16x32_bf16 v[46:49], v[182:185], v[206:209], v[46:49]
	v_mfma_f32_16x16x32_bf16 v[34:37], v[190:193], v[206:209], v[34:37]
	v_mfma_f32_16x16x32_bf16 v[30:33], v[182:185], v[214:217], v[30:33]
	v_mfma_f32_16x16x32_bf16 v[18:21], v[190:193], v[214:217], v[18:21]
	v_mfma_f32_16x16x32_bf16 v[14:17], v[182:185], v[224:227], v[14:17]
	v_mfma_f32_16x16x32_bf16 v[2:5], v[190:193], v[224:227], v[2:5]
	v_mfma_f32_16x16x32_bf16 v[62:65], v[186:189], v[202:205], v[62:65]
	v_mfma_f32_16x16x32_bf16 v[50:53], v[194:197], v[202:205], v[50:53]
	v_mfma_f32_16x16x32_bf16 v[46:49], v[186:189], v[210:213], v[46:49]
	v_mfma_f32_16x16x32_bf16 v[34:37], v[194:197], v[210:213], v[34:37]
	v_mfma_f32_16x16x32_bf16 v[30:33], v[186:189], v[220:223], v[30:33]
	v_mfma_f32_16x16x32_bf16 v[18:21], v[194:197], v[220:223], v[18:21]
	v_mfma_f32_16x16x32_bf16 v[14:17], v[186:189], v[228:231], v[14:17]
	v_mfma_f32_16x16x32_bf16 v[2:5], v[194:197], v[228:231], v[2:5]
	s_barrier
	s_add_i32 vcc_hi, vcc_hi, 2
	s_add_u32 s97, s97, 0x10000
	s_addc_u32 vcc_lo, vcc_lo, 0
	s_add_u32 s80, s80, 0x100
	s_addc_u32 s81, s81, 0
	s_cmp_gt_u32 vcc_hi, 29
	s_cbranch_scc0 .LBB0_261
	s_setprio 0
	s_and_b64 vcc, exec, s[50:51]
	s_cbranch_vccz .LBB0_264
	s_barrier

.LBB0_284:
	s_ashr_i32 s51, s50, 31
	s_lshl_b64 s[26:27], s[50:51], 19
	v_readlane_b32 s54, v254, 58
	v_readlane_b32 s55, v254, 59
	s_add_u32 s54, s54, s26
	s_addc_u32 s55, s55, s27
	s_and_b64 s[26:27], s[0:1], exec
	s_cselect_b32 s51, s55, s73
	s_cselect_b32 s90, s54, s72
	s_ashr_i32 s45, s44, 31
	s_lshl_b64 s[26:27], s[44:45], 19
	s_add_u32 s56, s81, s26
	s_addc_u32 s57, s82, s27
	s_and_b64 s[26:27], s[0:1], exec
	s_cselect_b32 s45, s57, s71
	s_cselect_b32 s91, s56, s70
	s_add_u32 s92, s70, 0x10000
	s_addc_u32 s93, s71, 0
	s_add_u32 s70, s72, 0x40080
	v_mov_b32_e32 v34, 0
	s_addc_u32 s71, s73, 0
	s_mov_b32 s94, -2
	v_mov_b32_e32 v35, v34
	v_mov_b32_e32 v36, v34
	v_mov_b32_e32 v37, v34
	v_mov_b32_e32 v38, v34
	v_mov_b32_e32 v39, v34
	v_mov_b32_e32 v40, v34
	v_mov_b32_e32 v41, v34
	v_mov_b32_e32 v42, v34
	v_mov_b32_e32 v43, v34
	v_mov_b32_e32 v44, v34
	v_mov_b32_e32 v45, v34
	v_mov_b32_e32 v50, v34
	v_mov_b32_e32 v51, v34
	v_mov_b32_e32 v52, v34
	v_mov_b32_e32 v53, v34
	v_mov_b32_e32 v58, v34
	v_mov_b32_e32 v59, v34
	v_mov_b32_e32 v60, v34
	v_mov_b32_e32 v61, v34
	v_mov_b32_e32 v66, v34
	v_mov_b32_e32 v67, v34
	v_mov_b32_e32 v68, v34
	v_mov_b32_e32 v69, v34
	v_mov_b32_e32 v74, v34
	v_mov_b32_e32 v75, v34
	v_mov_b32_e32 v76, v34
	v_mov_b32_e32 v77, v34
	v_mov_b32_e32 v82, v34
	v_mov_b32_e32 v83, v34
	v_mov_b32_e32 v84, v34
	v_mov_b32_e32 v85, v34
	v_mov_b32_e32 v46, v34
	v_mov_b32_e32 v47, v34
	v_mov_b32_e32 v48, v34
	v_mov_b32_e32 v49, v34
	v_mov_b32_e32 v54, v34
	v_mov_b32_e32 v55, v34
	v_mov_b32_e32 v56, v34
	v_mov_b32_e32 v57, v34
	v_mov_b32_e32 v62, v34
	v_mov_b32_e32 v63, v34
	v_mov_b32_e32 v64, v34
	v_mov_b32_e32 v65, v34
	v_mov_b32_e32 v70, v34
	v_mov_b32_e32 v71, v34
	v_mov_b32_e32 v72, v34
	v_mov_b32_e32 v73, v34
	v_mov_b32_e32 v78, v34
	v_mov_b32_e32 v79, v34
	v_mov_b32_e32 v80, v34
	v_mov_b32_e32 v81, v34
	v_mov_b32_e32 v86, v34
	v_mov_b32_e32 v87, v34
	v_mov_b32_e32 v88, v34
	v_mov_b32_e32 v89, v34
	v_mov_b32_e32 v90, v34
	v_mov_b32_e32 v91, v34
	v_mov_b32_e32 v92, v34
	v_mov_b32_e32 v93, v34
	v_mov_b32_e32 v94, v34
	v_mov_b32_e32 v95, v34
	v_mov_b32_e32 v96, v34
	v_mov_b32_e32 v97, v34
	v_mov_b32_e32 v98, v34
	v_mov_b32_e32 v99, v34
	v_mov_b32_e32 v100, v34
	v_mov_b32_e32 v101, v34
	v_mov_b32_e32 v102, v34
	v_mov_b32_e32 v103, v34
	v_mov_b32_e32 v104, v34
	v_mov_b32_e32 v105, v34
	v_mov_b32_e32 v106, v34
	v_mov_b32_e32 v107, v34
	v_mov_b32_e32 v108, v34
	v_mov_b32_e32 v109, v34
	v_mov_b32_e32 v114, v34
	v_mov_b32_e32 v115, v34
	v_mov_b32_e32 v116, v34
	v_mov_b32_e32 v117, v34
	v_mov_b32_e32 v122, v34
	v_mov_b32_e32 v123, v34
	v_mov_b32_e32 v124, v34
	v_mov_b32_e32 v125, v34
	v_mov_b32_e32 v130, v34
	v_mov_b32_e32 v131, v34
	v_mov_b32_e32 v132, v34
	v_mov_b32_e32 v133, v34
	v_mov_b32_e32 v138, v34
	v_mov_b32_e32 v139, v34
	v_mov_b32_e32 v140, v34
	v_mov_b32_e32 v141, v34
	v_mov_b32_e32 v146, v34
	v_mov_b32_e32 v147, v34
	v_mov_b32_e32 v148, v34
	v_mov_b32_e32 v149, v34
	v_mov_b32_e32 v110, v34
	v_mov_b32_e32 v111, v34
	v_mov_b32_e32 v112, v34
	v_mov_b32_e32 v113, v34
	v_mov_b32_e32 v118, v34
	v_mov_b32_e32 v119, v34
	v_mov_b32_e32 v120, v34
	v_mov_b32_e32 v121, v34
	v_mov_b32_e32 v126, v34
	v_mov_b32_e32 v127, v34
	v_mov_b32_e32 v128, v34
	v_mov_b32_e32 v129, v34
	v_mov_b32_e32 v134, v34
	v_mov_b32_e32 v135, v34
	v_mov_b32_e32 v136, v34
	v_mov_b32_e32 v137, v34
	v_mov_b32_e32 v142, v34
	v_mov_b32_e32 v143, v34
	v_mov_b32_e32 v144, v34
	v_mov_b32_e32 v145, v34
	v_mov_b32_e32 v150, v34
	v_mov_b32_e32 v151, v34
	v_mov_b32_e32 v152, v34
	v_mov_b32_e32 v153, v34
	v_mov_b32_e32 v154, v34
	v_mov_b32_e32 v155, v34
	v_mov_b32_e32 v156, v34
	v_mov_b32_e32 v157, v34
	v_mov_b32_e32 v158, v34
	v_mov_b32_e32 v159, v34
	v_mov_b32_e32 v160, v34
	v_mov_b32_e32 v161, v34
	v_readfirstlane_b32 s98, v0
	s_lshr_b32 s98, s98, 8
	s_cmp_eq_u32 s98, 1
	s_cbranch_scc0 .Lprio_skip8
	s_setprio 1
.Lprio_skip8:
.LBB0_285:
	ds_read_b128 v[26:29], v1
	ds_read_b128 v[30:33], v1 offset:1024
	ds_read_b128 v[18:21], v1 offset:2048
	ds_read_b128 v[22:25], v1 offset:3072
	ds_read_b128 v[10:13], v185
	ds_read_b128 v[14:17], v185 offset:1024
	ds_read_b128 v[2:5], v185 offset:2048
	ds_read_b128 v[6:9], v185 offset:3072
	s_add_u32 s26, s70, 0xfffc0080
	s_addc_u32 s27, s71, -1
	s_cmp_eq_u32 s94, 12
	s_cselect_b32 s73, s51, s27
	s_cselect_b32 s72, s90, s26
	s_cselect_b32 s75, s45, s93
	s_cselect_b32 s74, s91, s92
	v_lshl_add_u64 v[176:177], s[70:71], 0, v[168:169]
	s_add_i32 m0, s33, 0xc000
	ds_read_b128 v[190:193], v186
	ds_read_b128 v[194:197], v186 offset:1024
	ds_read_b128 v[198:201], v186 offset:2048
	ds_read_b128 v[202:205], v186 offset:3072
	ds_read_b128 v[206:209], v186 offset:4096
	ds_read_b128 v[210:213], v186 offset:5120
	ds_read_b128 v[220:223], v186 offset:6144
	ds_read_b128 v[224:227], v186 offset:7168
	global_load_lds_dwordx4 v[176:177], off
	v_lshl_add_u64 v[176:177], s[70:71], 0, v[170:171]
	s_add_i32 m0, s33, 0xe000
	s_nop 0
	global_load_lds_dwordx4 v[176:177], off
	s_waitcnt vmcnt(8)
	s_waitcnt lgkmcnt(0)
	s_barrier
	s_waitcnt lgkmcnt(0)
	v_mfma_scale_f32_16x16x128_f8f6f4 v[158:161], v[26:33], v[190:197], v[158:161], v187, v188 op_sel_hi:[0,0,0]
	v_mfma_scale_f32_16x16x128_f8f6f4 v[154:157], v[18:25], v[190:197], v[154:157], v187, v188 op_sel_hi:[0,0,0]
	v_mfma_scale_f32_16x16x128_f8f6f4 v[150:153], v[26:33], v[198:205], v[150:153], v187, v188 op_sel_hi:[0,0,0]
	v_mfma_scale_f32_16x16x128_f8f6f4 v[142:145], v[18:25], v[198:205], v[142:145], v187, v188 op_sel_hi:[0,0,0]
	v_mfma_scale_f32_16x16x128_f8f6f4 v[134:137], v[26:33], v[206:213], v[134:137], v187, v188 op_sel_hi:[0,0,0]
	v_mfma_scale_f32_16x16x128_f8f6f4 v[126:129], v[18:25], v[206:213], v[126:129], v187, v188 op_sel_hi:[0,0,0]
	v_mfma_scale_f32_16x16x128_f8f6f4 v[118:121], v[26:33], v[220:227], v[118:121], v187, v188 op_sel_hi:[0,0,0]
	v_mfma_scale_f32_16x16x128_f8f6f4 v[110:113], v[18:25], v[220:227], v[110:113], v187, v188 op_sel_hi:[0,0,0]
	v_mfma_scale_f32_16x16x128_f8f6f4 v[146:149], v[10:17], v[190:197], v[146:149], v187, v188 op_sel_hi:[0,0,0]
	v_mfma_scale_f32_16x16x128_f8f6f4 v[138:141], v[2:9], v[190:197], v[138:141], v187, v188 op_sel_hi:[0,0,0]
	v_mfma_scale_f32_16x16x128_f8f6f4 v[130:133], v[10:17], v[198:205], v[130:133], v187, v188 op_sel_hi:[0,0,0]
	v_mfma_scale_f32_16x16x128_f8f6f4 v[122:125], v[2:9], v[198:205], v[122:125], v187, v188 op_sel_hi:[0,0,0]
	v_mfma_scale_f32_16x16x128_f8f6f4 v[114:117], v[10:17], v[206:213], v[114:117], v187, v188 op_sel_hi:[0,0,0]
	v_mfma_scale_f32_16x16x128_f8f6f4 v[106:109], v[2:9], v[206:213], v[106:109], v187, v188 op_sel_hi:[0,0,0]
	v_mfma_scale_f32_16x16x128_f8f6f4 v[102:105], v[10:17], v[220:227], v[102:105], v187, v188 op_sel_hi:[0,0,0]
	v_mfma_scale_f32_16x16x128_f8f6f4 v[98:101], v[2:9], v[220:227], v[98:101], v187, v188 op_sel_hi:[0,0,0]
	s_barrier
	s_add_i32 s26, s88, s80
	v_lshl_add_u64 v[176:177], s[74:75], 0, v[162:163]
	s_mov_b32 m0, s26
	ds_read_b128 v[190:193], v186 offset:16384
	ds_read_b128 v[194:197], v186 offset:17408
	ds_read_b128 v[198:201], v186 offset:18432
	ds_read_b128 v[202:205], v186 offset:19456
	ds_read_b128 v[206:209], v186 offset:20480
	ds_read_b128 v[210:213], v186 offset:21504
	ds_read_b128 v[220:223], v186 offset:22528
	ds_read_b128 v[224:227], v186 offset:23552
	global_load_lds_dwordx4 v[176:177], off
	v_lshl_add_u64 v[178:179], v[176:177], 0, s[8:9]
	s_add_i32 m0, s26, 0x2000
	s_add_i32 s26, s89, s80
	global_load_lds_dwordx4 v[178:179], off
	v_lshl_add_u64 v[178:179], v[176:177], 0, s[10:11]
	s_mov_b32 m0, s26
	v_lshl_add_u64 v[180:181], s[72:73], 0, v[166:167]
	global_load_lds_dwordx4 v[178:179], off
	v_lshl_add_u64 v[178:179], v[176:177], 0, s[12:13]
	s_add_i32 m0, s26, 0x2000
	s_nop 0
	global_load_lds_dwordx4 v[178:179], off
	v_lshl_add_u64 v[178:179], s[72:73], 0, v[164:165]
	s_mov_b32 m0, s33
	s_nop 0
	global_load_lds_dwordx4 v[178:179], off
	s_mov_b32 m0, s69
	s_nop 0
	global_load_lds_dwordx4 v[180:181], off
	s_waitcnt vmcnt(8)
	s_waitcnt lgkmcnt(0)
	s_barrier
	s_waitcnt lgkmcnt(0)
	v_mfma_scale_f32_16x16x128_f8f6f4 v[94:97], v[26:33], v[190:197], v[94:97], v187, v188 op_sel_hi:[0,0,0]
	v_mfma_scale_f32_16x16x128_f8f6f4 v[90:93], v[18:25], v[190:197], v[90:93], v187, v188 op_sel_hi:[0,0,0]
	v_mfma_scale_f32_16x16x128_f8f6f4 v[86:89], v[26:33], v[198:205], v[86:89], v187, v188 op_sel_hi:[0,0,0]
	v_mfma_scale_f32_16x16x128_f8f6f4 v[78:81], v[18:25], v[198:205], v[78:81], v187, v188 op_sel_hi:[0,0,0]
	v_mfma_scale_f32_16x16x128_f8f6f4 v[70:73], v[26:33], v[206:213], v[70:73], v187, v188 op_sel_hi:[0,0,0]
	v_mfma_scale_f32_16x16x128_f8f6f4 v[62:65], v[18:25], v[206:213], v[62:65], v187, v188 op_sel_hi:[0,0,0]
	v_mfma_scale_f32_16x16x128_f8f6f4 v[54:57], v[26:33], v[220:227], v[54:57], v187, v188 op_sel_hi:[0,0,0]
	v_mfma_scale_f32_16x16x128_f8f6f4 v[46:49], v[18:25], v[220:227], v[46:49], v187, v188 op_sel_hi:[0,0,0]
	v_mfma_scale_f32_16x16x128_f8f6f4 v[82:85], v[10:17], v[190:197], v[82:85], v187, v188 op_sel_hi:[0,0,0]
	v_mfma_scale_f32_16x16x128_f8f6f4 v[74:77], v[2:9], v[190:197], v[74:77], v187, v188 op_sel_hi:[0,0,0]
	v_mfma_scale_f32_16x16x128_f8f6f4 v[66:69], v[10:17], v[198:205], v[66:69], v187, v188 op_sel_hi:[0,0,0]
	v_mfma_scale_f32_16x16x128_f8f6f4 v[58:61], v[2:9], v[198:205], v[58:61], v187, v188 op_sel_hi:[0,0,0]
	v_mfma_scale_f32_16x16x128_f8f6f4 v[50:53], v[10:17], v[206:213], v[50:53], v187, v188 op_sel_hi:[0,0,0]
	v_mfma_scale_f32_16x16x128_f8f6f4 v[42:45], v[2:9], v[206:213], v[42:45], v187, v188 op_sel_hi:[0,0,0]
	v_mfma_scale_f32_16x16x128_f8f6f4 v[38:41], v[10:17], v[220:227], v[38:41], v187, v188 op_sel_hi:[0,0,0]
	v_mfma_scale_f32_16x16x128_f8f6f4 v[34:37], v[2:9], v[220:227], v[34:37], v187, v188 op_sel_hi:[0,0,0]
	s_barrier
	s_add_i32 s74, 0, 0x18000
	s_add_i32 s75, 0, 0x1c000
	v_add_u32_e32 v14, s74, v183
	v_add_u32_e32 v30, s75, v183
	ds_read_b128 v[2:5], v14
	ds_read_b128 v[6:9], v14 offset:1024
	ds_read_b128 v[10:13], v14 offset:2048
	ds_read_b128 v[14:17], v14 offset:3072
	ds_read_b128 v[18:21], v30
	ds_read_b128 v[22:25], v30 offset:1024
	ds_read_b128 v[26:29], v30 offset:2048
	ds_read_b128 v[30:33], v30 offset:3072
	s_add_u32 s26, s72, 0x40000
	s_addc_u32 s27, s73, 0
	s_mov_b32 m0, s83
	v_lshl_add_u64 v[214:215], s[26:27], 0, v[164:165]
	ds_read_b128 v[190:193], v186 offset:32768
	ds_read_b128 v[194:197], v186 offset:33792
	ds_read_b128 v[198:201], v186 offset:34816
	ds_read_b128 v[202:205], v186 offset:35840
	ds_read_b128 v[206:209], v186 offset:36864
	ds_read_b128 v[210:213], v186 offset:37888
	ds_read_b128 v[220:223], v186 offset:38912
	ds_read_b128 v[224:227], v186 offset:39936
	global_load_lds_dwordx4 v[214:215], off
	v_lshl_add_u64 v[214:215], s[26:27], 0, v[166:167]
	s_mov_b32 m0, s84
	s_nop 0
	global_load_lds_dwordx4 v[214:215], off
	s_waitcnt vmcnt(8)
	s_waitcnt lgkmcnt(0)
	s_barrier
	s_waitcnt lgkmcnt(0)
	v_mfma_scale_f32_16x16x128_f8f6f4 v[158:161], v[2:9], v[190:197], v[158:161], v187, v188 op_sel_hi:[0,0,0]
	v_mfma_scale_f32_16x16x128_f8f6f4 v[154:157], v[10:17], v[190:197], v[154:157], v187, v188 op_sel_hi:[0,0,0]
	v_mfma_scale_f32_16x16x128_f8f6f4 v[150:153], v[2:9], v[198:205], v[150:153], v187, v188 op_sel_hi:[0,0,0]
	v_mfma_scale_f32_16x16x128_f8f6f4 v[142:145], v[10:17], v[198:205], v[142:145], v187, v188 op_sel_hi:[0,0,0]
	v_mfma_scale_f32_16x16x128_f8f6f4 v[134:137], v[2:9], v[206:213], v[134:137], v187, v188 op_sel_hi:[0,0,0]
	v_mfma_scale_f32_16x16x128_f8f6f4 v[126:129], v[10:17], v[206:213], v[126:129], v187, v188 op_sel_hi:[0,0,0]
	v_mfma_scale_f32_16x16x128_f8f6f4 v[118:121], v[2:9], v[220:227], v[118:121], v187, v188 op_sel_hi:[0,0,0]
	v_mfma_scale_f32_16x16x128_f8f6f4 v[110:113], v[10:17], v[220:227], v[110:113], v187, v188 op_sel_hi:[0,0,0]
	v_mfma_scale_f32_16x16x128_f8f6f4 v[146:149], v[18:25], v[190:197], v[146:149], v187, v188 op_sel_hi:[0,0,0]
	v_mfma_scale_f32_16x16x128_f8f6f4 v[138:141], v[26:33], v[190:197], v[138:141], v187, v188 op_sel_hi:[0,0,0]
	v_mfma_scale_f32_16x16x128_f8f6f4 v[130:133], v[18:25], v[198:205], v[130:133], v187, v188 op_sel_hi:[0,0,0]
	v_mfma_scale_f32_16x16x128_f8f6f4 v[122:125], v[26:33], v[198:205], v[122:125], v187, v188 op_sel_hi:[0,0,0]
	v_mfma_scale_f32_16x16x128_f8f6f4 v[114:117], v[18:25], v[206:213], v[114:117], v187, v188 op_sel_hi:[0,0,0]
	v_mfma_scale_f32_16x16x128_f8f6f4 v[106:109], v[26:33], v[206:213], v[106:109], v187, v188 op_sel_hi:[0,0,0]
	v_mfma_scale_f32_16x16x128_f8f6f4 v[102:105], v[18:25], v[220:227], v[102:105], v187, v188 op_sel_hi:[0,0,0]
	v_mfma_scale_f32_16x16x128_f8f6f4 v[98:101], v[26:33], v[220:227], v[98:101], v187, v188 op_sel_hi:[0,0,0]
	s_barrier
	s_add_i32 s26, s74, s80
	v_lshl_add_u64 v[214:215], v[176:177], 0, s[16:17]
	s_mov_b32 m0, s26
	ds_read_b128 v[190:193], v186 offset:49152
	ds_read_b128 v[194:197], v186 offset:50176
	ds_read_b128 v[198:201], v186 offset:51200
	ds_read_b128 v[202:205], v186 offset:52224
	ds_read_b128 v[206:209], v186 offset:53248
	ds_read_b128 v[210:213], v186 offset:54272
	ds_read_b128 v[220:223], v186 offset:55296
	ds_read_b128 v[224:227], v186 offset:56320
	global_load_lds_dwordx4 v[214:215], off
	v_lshl_add_u64 v[214:215], v[176:177], 0, s[18:19]
	s_add_i32 m0, s26, 0x2000
	s_add_i32 s26, s75, s80
	global_load_lds_dwordx4 v[214:215], off
	v_lshl_add_u64 v[214:215], v[176:177], 0, s[22:23]
	s_mov_b32 m0, s26
	v_lshl_add_u64 v[176:177], v[176:177], 0, s[24:25]
	global_load_lds_dwordx4 v[214:215], off
	s_add_i32 m0, s26, 0x2000
	s_nop 0
	global_load_lds_dwordx4 v[176:177], off
	v_lshl_add_u64 v[176:177], v[178:179], 0, s[20:21]
	s_mov_b32 m0, s86
	s_nop 0
	global_load_lds_dwordx4 v[176:177], off
	v_lshl_add_u64 v[176:177], v[180:181], 0, s[20:21]
	s_mov_b32 m0, s87
	s_nop 0
	global_load_lds_dwordx4 v[176:177], off
	s_waitcnt vmcnt(8)
	s_waitcnt lgkmcnt(0)
	s_barrier
	s_waitcnt lgkmcnt(0)
	v_mfma_scale_f32_16x16x128_f8f6f4 v[94:97], v[2:9], v[190:197], v[94:97], v187, v188 op_sel_hi:[0,0,0]
	v_mfma_scale_f32_16x16x128_f8f6f4 v[90:93], v[10:17], v[190:197], v[90:93], v187, v188 op_sel_hi:[0,0,0]
	v_mfma_scale_f32_16x16x128_f8f6f4 v[86:89], v[2:9], v[198:205], v[86:89], v187, v188 op_sel_hi:[0,0,0]
	v_mfma_scale_f32_16x16x128_f8f6f4 v[78:81], v[10:17], v[198:205], v[78:81], v187, v188 op_sel_hi:[0,0,0]
	v_mfma_scale_f32_16x16x128_f8f6f4 v[70:73], v[2:9], v[206:213], v[70:73], v187, v188 op_sel_hi:[0,0,0]
	v_mfma_scale_f32_16x16x128_f8f6f4 v[62:65], v[10:17], v[206:213], v[62:65], v187, v188 op_sel_hi:[0,0,0]
	v_mfma_scale_f32_16x16x128_f8f6f4 v[54:57], v[2:9], v[220:227], v[54:57], v187, v188 op_sel_hi:[0,0,0]
	v_mfma_scale_f32_16x16x128_f8f6f4 v[46:49], v[10:17], v[220:227], v[46:49], v187, v188 op_sel_hi:[0,0,0]
	v_mfma_scale_f32_16x16x128_f8f6f4 v[82:85], v[18:25], v[190:197], v[82:85], v187, v188 op_sel_hi:[0,0,0]
	v_mfma_scale_f32_16x16x128_f8f6f4 v[74:77], v[26:33], v[190:197], v[74:77], v187, v188 op_sel_hi:[0,0,0]
	v_mfma_scale_f32_16x16x128_f8f6f4 v[66:69], v[18:25], v[198:205], v[66:69], v187, v188 op_sel_hi:[0,0,0]
	v_mfma_scale_f32_16x16x128_f8f6f4 v[58:61], v[26:33], v[198:205], v[58:61], v187, v188 op_sel_hi:[0,0,0]
	v_mfma_scale_f32_16x16x128_f8f6f4 v[50:53], v[18:25], v[206:213], v[50:53], v187, v188 op_sel_hi:[0,0,0]
	v_mfma_scale_f32_16x16x128_f8f6f4 v[42:45], v[26:33], v[206:213], v[42:45], v187, v188 op_sel_hi:[0,0,0]
	v_mfma_scale_f32_16x16x128_f8f6f4 v[38:41], v[18:25], v[220:227], v[38:41], v187, v188 op_sel_hi:[0,0,0]
	v_mfma_scale_f32_16x16x128_f8f6f4 v[34:37], v[26:33], v[220:227], v[34:37], v187, v188 op_sel_hi:[0,0,0]
	s_barrier
	s_add_i32 s94, s94, 2
	s_add_u32 s92, s92, 0x10000
	s_addc_u32 s93, s93, 0
	s_add_u32 s70, s70, 0x100
	s_addc_u32 s71, s71, 0
	s_cmp_gt_u32 s94, 13
	s_cbranch_scc0 .LBB0_285
	s_setprio 0
	s_and_b64 vcc, exec, s[40:41]
	s_cbranch_vccz .LBB0_288
	s_barrier

.LBB0_659:
	s_ashr_i32 s45, s44, 31
	s_lshl_b64 s[26:27], s[44:45], 20
	v_readlane_b32 s50, v254, 58
	v_readlane_b32 s51, v254, 59
	s_add_u32 s50, s50, s26
	s_addc_u32 s51, s51, s27
	s_and_b64 s[26:27], s[0:1], exec
	s_cselect_b32 s45, s51, s61
	s_cselect_b32 s72, s50, s60
	s_ashr_i32 s41, s40, 31
	s_lshl_b64 s[26:27], s[40:41], 20
	s_add_u32 s54, s3, s26
	s_addc_u32 s55, s33, s27
	s_and_b64 s[26:27], s[0:1], exec
	s_cselect_b32 s41, s55, s59
	s_cselect_b32 s73, s54, s58
	s_add_u32 s74, s58, 0x10000
	s_addc_u32 s75, s59, 0
	s_add_u32 s58, s60, 0x80080
	v_mov_b32_e32 v2, 0
	s_addc_u32 s59, s61, 0
	s_mov_b32 s80, -2
	v_mov_b32_e32 v3, v2
	v_mov_b32_e32 v4, v2
	v_mov_b32_e32 v5, v2
	v_mov_b32_e32 v6, v2
	v_mov_b32_e32 v7, v2
	v_mov_b32_e32 v8, v2
	v_mov_b32_e32 v9, v2
	v_mov_b32_e32 v14, v2
	v_mov_b32_e32 v15, v2
	v_mov_b32_e32 v16, v2
	v_mov_b32_e32 v17, v2
	v_mov_b32_e32 v18, v2
	v_mov_b32_e32 v19, v2
	v_mov_b32_e32 v20, v2
	v_mov_b32_e32 v21, v2
	v_mov_b32_e32 v22, v2
	v_mov_b32_e32 v23, v2
	v_mov_b32_e32 v24, v2
	v_mov_b32_e32 v25, v2
	v_mov_b32_e32 v26, v2
	v_mov_b32_e32 v27, v2
	v_mov_b32_e32 v28, v2
	v_mov_b32_e32 v29, v2
	v_mov_b32_e32 v34, v2
	v_mov_b32_e32 v35, v2
	v_mov_b32_e32 v36, v2
	v_mov_b32_e32 v37, v2
	v_mov_b32_e32 v42, v2
	v_mov_b32_e32 v43, v2
	v_mov_b32_e32 v44, v2
	v_mov_b32_e32 v45, v2
	v_mov_b32_e32 v10, v2
	v_mov_b32_e32 v11, v2
	v_mov_b32_e32 v12, v2
	v_mov_b32_e32 v13, v2
	v_mov_b32_e32 v30, v2
	v_mov_b32_e32 v31, v2
	v_mov_b32_e32 v32, v2
	v_mov_b32_e32 v33, v2
	v_mov_b32_e32 v38, v2
	v_mov_b32_e32 v39, v2
	v_mov_b32_e32 v40, v2
	v_mov_b32_e32 v41, v2
	v_mov_b32_e32 v46, v2
	v_mov_b32_e32 v47, v2
	v_mov_b32_e32 v48, v2
	v_mov_b32_e32 v49, v2
	v_mov_b32_e32 v50, v2
	v_mov_b32_e32 v51, v2
	v_mov_b32_e32 v52, v2
	v_mov_b32_e32 v53, v2
	v_mov_b32_e32 v54, v2
	v_mov_b32_e32 v55, v2
	v_mov_b32_e32 v56, v2
	v_mov_b32_e32 v57, v2
	v_mov_b32_e32 v58, v2
	v_mov_b32_e32 v59, v2
	v_mov_b32_e32 v60, v2
	v_mov_b32_e32 v61, v2
	v_mov_b32_e32 v62, v2
	v_mov_b32_e32 v63, v2
	v_mov_b32_e32 v64, v2
	v_mov_b32_e32 v65, v2
	v_mov_b32_e32 v66, v2
	v_mov_b32_e32 v67, v2
	v_mov_b32_e32 v68, v2
	v_mov_b32_e32 v69, v2
	v_mov_b32_e32 v70, v2
	v_mov_b32_e32 v71, v2
	v_mov_b32_e32 v72, v2
	v_mov_b32_e32 v73, v2
	v_mov_b32_e32 v78, v2
	v_mov_b32_e32 v79, v2
	v_mov_b32_e32 v80, v2
	v_mov_b32_e32 v81, v2
	v_mov_b32_e32 v82, v2
	v_mov_b32_e32 v83, v2
	v_mov_b32_e32 v84, v2
	v_mov_b32_e32 v85, v2
	v_mov_b32_e32 v86, v2
	v_mov_b32_e32 v87, v2
	v_mov_b32_e32 v88, v2
	v_mov_b32_e32 v89, v2
	v_mov_b32_e32 v90, v2
	v_mov_b32_e32 v91, v2
	v_mov_b32_e32 v92, v2
	v_mov_b32_e32 v93, v2
	v_mov_b32_e32 v98, v2
	v_mov_b32_e32 v99, v2
	v_mov_b32_e32 v100, v2
	v_mov_b32_e32 v101, v2
	v_mov_b32_e32 v106, v2
	v_mov_b32_e32 v107, v2
	v_mov_b32_e32 v108, v2
	v_mov_b32_e32 v109, v2
	v_mov_b32_e32 v74, v2
	v_mov_b32_e32 v75, v2
	v_mov_b32_e32 v76, v2
	v_mov_b32_e32 v77, v2
	v_mov_b32_e32 v94, v2
	v_mov_b32_e32 v95, v2
	v_mov_b32_e32 v96, v2
	v_mov_b32_e32 v97, v2
	v_mov_b32_e32 v102, v2
	v_mov_b32_e32 v103, v2
	v_mov_b32_e32 v104, v2
	v_mov_b32_e32 v105, v2
	v_mov_b32_e32 v110, v2
	v_mov_b32_e32 v111, v2
	v_mov_b32_e32 v112, v2
	v_mov_b32_e32 v113, v2
	v_mov_b32_e32 v114, v2
	v_mov_b32_e32 v115, v2
	v_mov_b32_e32 v116, v2
	v_mov_b32_e32 v117, v2
	v_mov_b32_e32 v118, v2
	v_mov_b32_e32 v119, v2
	v_mov_b32_e32 v120, v2
	v_mov_b32_e32 v121, v2
	v_mov_b32_e32 v122, v2
	v_mov_b32_e32 v123, v2
	v_mov_b32_e32 v124, v2
	v_mov_b32_e32 v125, v2
	v_mov_b32_e32 v126, v2
	v_mov_b32_e32 v127, v2
	v_mov_b32_e32 v128, v2
	v_mov_b32_e32 v129, v2
	v_readfirstlane_b32 s98, v0
	s_lshr_b32 s98, s98, 8
	s_cmp_eq_u32 s98, 1
	s_cbranch_scc0 .Lprio_skip7
	s_setprio 1
.Lprio_skip7:
.LBB0_660:
	ds_read_b128 v[130:133], v222
	ds_read_b128 v[134:137], v222 offset:1024
	ds_read_b128 v[138:141], v222 offset:2048
	ds_read_b128 v[142:145], v222 offset:3072
	ds_read_b128 v[146:149], v223
	ds_read_b128 v[150:153], v223 offset:1024
	ds_read_b128 v[154:157], v223 offset:2048
	ds_read_b128 v[158:161], v223 offset:3072
	s_add_u32 s26, s58, 0xfff80080
	s_addc_u32 s27, s59, -1
	s_cmp_eq_u32 s80, 28
	s_cselect_b32 s61, s45, s27
	s_cselect_b32 s60, s72, s26
	s_cselect_b32 s27, s41, s75
	s_cselect_b32 s26, s73, s74
	v_lshl_add_u64 v[208:209], s[58:59], 0, v[200:201]
	s_add_i32 m0, s57, 0xc000
	ds_read_b128 v[162:165], v224
	ds_read_b128 v[166:169], v224 offset:1024
	ds_read_b128 v[170:173], v224 offset:2048
	ds_read_b128 v[174:177], v224 offset:3072
	ds_read_b128 v[178:181], v224 offset:4096
	ds_read_b128 v[182:185], v224 offset:5120
	ds_read_b128 v[186:189], v224 offset:6144
	ds_read_b128 v[190:193], v224 offset:7168
	global_load_lds_dwordx4 v[208:209], off
	v_lshl_add_u64 v[208:209], s[58:59], 0, v[202:203]
	s_add_i32 m0, s57, 0xe000
	s_nop 0
	global_load_lds_dwordx4 v[208:209], off
	s_waitcnt vmcnt(8)
	s_waitcnt lgkmcnt(0)
	s_barrier
	s_waitcnt lgkmcnt(0)
	v_mfma_f32_16x16x32_bf16 v[126:129], v[130:133], v[162:165], v[126:129]
	v_mfma_f32_16x16x32_bf16 v[122:125], v[138:141], v[162:165], v[122:125]
	v_mfma_f32_16x16x32_bf16 v[118:121], v[130:133], v[170:173], v[118:121]
	v_mfma_f32_16x16x32_bf16 v[114:117], v[138:141], v[170:173], v[114:117]
	v_mfma_f32_16x16x32_bf16 v[110:113], v[130:133], v[178:181], v[110:113]
	v_mfma_f32_16x16x32_bf16 v[102:105], v[138:141], v[178:181], v[102:105]
	v_mfma_f32_16x16x32_bf16 v[94:97], v[130:133], v[186:189], v[94:97]
	v_mfma_f32_16x16x32_bf16 v[74:77], v[138:141], v[186:189], v[74:77]
	v_mfma_f32_16x16x32_bf16 v[126:129], v[134:137], v[166:169], v[126:129]
	v_mfma_f32_16x16x32_bf16 v[122:125], v[142:145], v[166:169], v[122:125]
	v_mfma_f32_16x16x32_bf16 v[118:121], v[134:137], v[174:177], v[118:121]
	v_mfma_f32_16x16x32_bf16 v[114:117], v[142:145], v[174:177], v[114:117]
	v_mfma_f32_16x16x32_bf16 v[110:113], v[134:137], v[182:185], v[110:113]
	v_mfma_f32_16x16x32_bf16 v[102:105], v[142:145], v[182:185], v[102:105]
	v_mfma_f32_16x16x32_bf16 v[94:97], v[134:137], v[190:193], v[94:97]
	v_mfma_f32_16x16x32_bf16 v[74:77], v[142:145], v[190:193], v[74:77]
	v_mfma_f32_16x16x32_bf16 v[106:109], v[146:149], v[162:165], v[106:109]
	v_mfma_f32_16x16x32_bf16 v[98:101], v[154:157], v[162:165], v[98:101]
	v_mfma_f32_16x16x32_bf16 v[90:93], v[146:149], v[170:173], v[90:93]
	v_mfma_f32_16x16x32_bf16 v[86:89], v[154:157], v[170:173], v[86:89]
	v_mfma_f32_16x16x32_bf16 v[82:85], v[146:149], v[178:181], v[82:85]
	v_mfma_f32_16x16x32_bf16 v[78:81], v[154:157], v[178:181], v[78:81]
	v_mfma_f32_16x16x32_bf16 v[70:73], v[146:149], v[186:189], v[70:73]
	v_mfma_f32_16x16x32_bf16 v[66:69], v[154:157], v[186:189], v[66:69]
	v_mfma_f32_16x16x32_bf16 v[106:109], v[150:153], v[166:169], v[106:109]
	v_mfma_f32_16x16x32_bf16 v[98:101], v[158:161], v[166:169], v[98:101]
	v_mfma_f32_16x16x32_bf16 v[90:93], v[150:153], v[174:177], v[90:93]
	v_mfma_f32_16x16x32_bf16 v[86:89], v[158:161], v[174:177], v[86:89]
	v_mfma_f32_16x16x32_bf16 v[82:85], v[150:153], v[182:185], v[82:85]
	v_mfma_f32_16x16x32_bf16 v[78:81], v[158:161], v[182:185], v[78:81]
	v_mfma_f32_16x16x32_bf16 v[70:73], v[150:153], v[190:193], v[70:73]
	v_mfma_f32_16x16x32_bf16 v[66:69], v[158:161], v[190:193], v[66:69]
	s_barrier
	v_lshl_add_u64 v[208:209], s[26:27], 0, v[194:195]
	s_add_i32 s26, s70, s35
	s_mov_b32 m0, s26
	ds_read_b128 v[162:165], v224 offset:16384
	ds_read_b128 v[166:169], v224 offset:17408
	ds_read_b128 v[170:173], v224 offset:18432
	ds_read_b128 v[174:177], v224 offset:19456
	ds_read_b128 v[178:181], v224 offset:20480
	ds_read_b128 v[182:185], v224 offset:21504
	ds_read_b128 v[186:189], v224 offset:22528
	ds_read_b128 v[190:193], v224 offset:23552
	global_load_lds_dwordx4 v[208:209], off
	v_lshl_add_u64 v[210:211], v[208:209], 0, s[6:7]
	s_add_i32 m0, s26, 0x2000
	s_add_i32 s26, s71, s35
	global_load_lds_dwordx4 v[210:211], off
	v_lshl_add_u64 v[210:211], v[208:209], 0, s[8:9]
	s_mov_b32 m0, s26
	v_lshl_add_u64 v[212:213], s[60:61], 0, v[198:199]
	global_load_lds_dwordx4 v[210:211], off
	v_lshl_add_u64 v[210:211], v[208:209], 0, s[10:11]
	s_add_i32 m0, s26, 0x2000
	s_nop 0
	global_load_lds_dwordx4 v[210:211], off
	v_lshl_add_u64 v[210:211], s[60:61], 0, v[196:197]
	s_mov_b32 m0, s57
	s_nop 0
	global_load_lds_dwordx4 v[210:211], off
	s_mov_b32 m0, s63
	s_nop 0
	global_load_lds_dwordx4 v[212:213], off
	s_waitcnt vmcnt(8)
	s_waitcnt lgkmcnt(0)
	s_barrier
	s_waitcnt lgkmcnt(0)
	v_mfma_f32_16x16x32_bf16 v[62:65], v[130:133], v[162:165], v[62:65]
	v_mfma_f32_16x16x32_bf16 v[58:61], v[138:141], v[162:165], v[58:61]
	v_mfma_f32_16x16x32_bf16 v[54:57], v[130:133], v[170:173], v[54:57]
	v_mfma_f32_16x16x32_bf16 v[50:53], v[138:141], v[170:173], v[50:53]
	v_mfma_f32_16x16x32_bf16 v[46:49], v[130:133], v[178:181], v[46:49]
	v_mfma_f32_16x16x32_bf16 v[38:41], v[138:141], v[178:181], v[38:41]
	v_mfma_f32_16x16x32_bf16 v[30:33], v[130:133], v[186:189], v[30:33]
	v_mfma_f32_16x16x32_bf16 v[10:13], v[138:141], v[186:189], v[10:13]
	v_mfma_f32_16x16x32_bf16 v[62:65], v[134:137], v[166:169], v[62:65]
	v_mfma_f32_16x16x32_bf16 v[58:61], v[142:145], v[166:169], v[58:61]
	v_mfma_f32_16x16x32_bf16 v[54:57], v[134:137], v[174:177], v[54:57]
	v_mfma_f32_16x16x32_bf16 v[50:53], v[142:145], v[174:177], v[50:53]
	v_mfma_f32_16x16x32_bf16 v[46:49], v[134:137], v[182:185], v[46:49]
	v_mfma_f32_16x16x32_bf16 v[38:41], v[142:145], v[182:185], v[38:41]
	v_mfma_f32_16x16x32_bf16 v[30:33], v[134:137], v[190:193], v[30:33]
	v_mfma_f32_16x16x32_bf16 v[10:13], v[142:145], v[190:193], v[10:13]
	v_mfma_f32_16x16x32_bf16 v[42:45], v[146:149], v[162:165], v[42:45]
	v_mfma_f32_16x16x32_bf16 v[34:37], v[154:157], v[162:165], v[34:37]
	v_mfma_f32_16x16x32_bf16 v[26:29], v[146:149], v[170:173], v[26:29]
	v_mfma_f32_16x16x32_bf16 v[22:25], v[154:157], v[170:173], v[22:25]
	v_mfma_f32_16x16x32_bf16 v[18:21], v[146:149], v[178:181], v[18:21]
	v_mfma_f32_16x16x32_bf16 v[14:17], v[154:157], v[178:181], v[14:17]
	v_mfma_f32_16x16x32_bf16 v[6:9], v[146:149], v[186:189], v[6:9]
	v_mfma_f32_16x16x32_bf16 v[2:5], v[154:157], v[186:189], v[2:5]
	v_mfma_f32_16x16x32_bf16 v[42:45], v[150:153], v[166:169], v[42:45]
	v_mfma_f32_16x16x32_bf16 v[34:37], v[158:161], v[166:169], v[34:37]
	v_mfma_f32_16x16x32_bf16 v[26:29], v[150:153], v[174:177], v[26:29]
	v_mfma_f32_16x16x32_bf16 v[22:25], v[158:161], v[174:177], v[22:25]
	v_mfma_f32_16x16x32_bf16 v[18:21], v[150:153], v[182:185], v[18:21]
	v_mfma_f32_16x16x32_bf16 v[14:17], v[158:161], v[182:185], v[14:17]
	v_mfma_f32_16x16x32_bf16 v[6:9], v[150:153], v[190:193], v[6:9]
	v_mfma_f32_16x16x32_bf16 v[2:5], v[158:161], v[190:193], v[2:5]
	s_barrier
	s_add_i32 s81, 0, 0x18000
	s_add_i32 s82, 0, 0x1c000
	v_add_u32_e32 v142, s81, v220
	v_add_u32_e32 v158, s82, v220
	ds_read_b128 v[130:133], v142
	ds_read_b128 v[134:137], v142 offset:1024
	ds_read_b128 v[138:141], v142 offset:2048
	ds_read_b128 v[142:145], v142 offset:3072
	ds_read_b128 v[146:149], v158
	ds_read_b128 v[150:153], v158 offset:1024
	ds_read_b128 v[154:157], v158 offset:2048
	ds_read_b128 v[158:161], v158 offset:3072
	s_add_u32 s26, s60, 0x80000
	s_addc_u32 s27, s61, 0
	s_mov_b32 m0, s64
	v_lshl_add_u64 v[214:215], s[26:27], 0, v[196:197]
	ds_read_b128 v[162:165], v224 offset:32768
	ds_read_b128 v[166:169], v224 offset:33792
	ds_read_b128 v[170:173], v224 offset:34816
	ds_read_b128 v[174:177], v224 offset:35840
	ds_read_b128 v[178:181], v224 offset:36864
	ds_read_b128 v[182:185], v224 offset:37888
	ds_read_b128 v[186:189], v224 offset:38912
	ds_read_b128 v[190:193], v224 offset:39936
	global_load_lds_dwordx4 v[214:215], off
	v_lshl_add_u64 v[214:215], s[26:27], 0, v[198:199]
	s_mov_b32 m0, s65
	s_nop 0
	global_load_lds_dwordx4 v[214:215], off
	s_waitcnt vmcnt(8)
	s_waitcnt lgkmcnt(0)
	s_barrier
	s_waitcnt lgkmcnt(0)
	v_mfma_f32_16x16x32_bf16 v[126:129], v[130:133], v[162:165], v[126:129]
	v_mfma_f32_16x16x32_bf16 v[122:125], v[138:141], v[162:165], v[122:125]
	v_mfma_f32_16x16x32_bf16 v[118:121], v[130:133], v[170:173], v[118:121]
	v_mfma_f32_16x16x32_bf16 v[114:117], v[138:141], v[170:173], v[114:117]
	v_mfma_f32_16x16x32_bf16 v[110:113], v[130:133], v[178:181], v[110:113]
	v_mfma_f32_16x16x32_bf16 v[102:105], v[138:141], v[178:181], v[102:105]
	v_mfma_f32_16x16x32_bf16 v[94:97], v[130:133], v[186:189], v[94:97]
	v_mfma_f32_16x16x32_bf16 v[74:77], v[138:141], v[186:189], v[74:77]
	v_mfma_f32_16x16x32_bf16 v[126:129], v[134:137], v[166:169], v[126:129]
	v_mfma_f32_16x16x32_bf16 v[122:125], v[142:145], v[166:169], v[122:125]
	v_mfma_f32_16x16x32_bf16 v[118:121], v[134:137], v[174:177], v[118:121]
	v_mfma_f32_16x16x32_bf16 v[114:117], v[142:145], v[174:177], v[114:117]
	v_mfma_f32_16x16x32_bf16 v[110:113], v[134:137], v[182:185], v[110:113]
	v_mfma_f32_16x16x32_bf16 v[102:105], v[142:145], v[182:185], v[102:105]
	v_mfma_f32_16x16x32_bf16 v[94:97], v[134:137], v[190:193], v[94:97]
	v_mfma_f32_16x16x32_bf16 v[74:77], v[142:145], v[190:193], v[74:77]
	v_mfma_f32_16x16x32_bf16 v[106:109], v[146:149], v[162:165], v[106:109]
	v_mfma_f32_16x16x32_bf16 v[98:101], v[154:157], v[162:165], v[98:101]
	v_mfma_f32_16x16x32_bf16 v[90:93], v[146:149], v[170:173], v[90:93]
	v_mfma_f32_16x16x32_bf16 v[86:89], v[154:157], v[170:173], v[86:89]
	v_mfma_f32_16x16x32_bf16 v[82:85], v[146:149], v[178:181], v[82:85]
	v_mfma_f32_16x16x32_bf16 v[78:81], v[154:157], v[178:181], v[78:81]
	v_mfma_f32_16x16x32_bf16 v[70:73], v[146:149], v[186:189], v[70:73]
	v_mfma_f32_16x16x32_bf16 v[66:69], v[154:157], v[186:189], v[66:69]
	v_mfma_f32_16x16x32_bf16 v[106:109], v[150:153], v[166:169], v[106:109]
	v_mfma_f32_16x16x32_bf16 v[98:101], v[158:161], v[166:169], v[98:101]
	v_mfma_f32_16x16x32_bf16 v[90:93], v[150:153], v[174:177], v[90:93]
	v_mfma_f32_16x16x32_bf16 v[86:89], v[158:161], v[174:177], v[86:89]
	v_mfma_f32_16x16x32_bf16 v[82:85], v[150:153], v[182:185], v[82:85]
	v_mfma_f32_16x16x32_bf16 v[78:81], v[158:161], v[182:185], v[78:81]
	v_mfma_f32_16x16x32_bf16 v[70:73], v[150:153], v[190:193], v[70:73]
	v_mfma_f32_16x16x32_bf16 v[66:69], v[158:161], v[190:193], v[66:69]
	s_barrier
	s_add_i32 s26, s81, s35
	v_lshl_add_u64 v[214:215], v[208:209], 0, s[14:15]
	s_mov_b32 m0, s26
	ds_read_b128 v[162:165], v224 offset:49152
	ds_read_b128 v[166:169], v224 offset:50176
	ds_read_b128 v[170:173], v224 offset:51200
	ds_read_b128 v[174:177], v224 offset:52224
	ds_read_b128 v[178:181], v224 offset:53248
	ds_read_b128 v[182:185], v224 offset:54272
	ds_read_b128 v[186:189], v224 offset:55296
	ds_read_b128 v[190:193], v224 offset:56320
	global_load_lds_dwordx4 v[214:215], off
	v_lshl_add_u64 v[214:215], v[208:209], 0, s[16:17]
	s_add_i32 m0, s26, 0x2000
	s_add_i32 s26, s82, s35
	global_load_lds_dwordx4 v[214:215], off
	v_lshl_add_u64 v[214:215], v[208:209], 0, s[20:21]
	s_mov_b32 m0, s26
	v_lshl_add_u64 v[208:209], v[208:209], 0, s[22:23]
	global_load_lds_dwordx4 v[214:215], off
	s_add_i32 m0, s26, 0x2000
	s_nop 0
	global_load_lds_dwordx4 v[208:209], off
	v_lshl_add_u64 v[208:209], v[210:211], 0, s[18:19]
	s_mov_b32 m0, s67
	s_nop 0
	global_load_lds_dwordx4 v[208:209], off
	v_lshl_add_u64 v[208:209], v[212:213], 0, s[18:19]
	s_mov_b32 m0, s68
	s_nop 0
	global_load_lds_dwordx4 v[208:209], off
	s_waitcnt vmcnt(8)
	s_waitcnt lgkmcnt(0)
	s_barrier
	s_waitcnt lgkmcnt(0)
	v_mfma_f32_16x16x32_bf16 v[62:65], v[130:133], v[162:165], v[62:65]
	v_mfma_f32_16x16x32_bf16 v[58:61], v[138:141], v[162:165], v[58:61]
	v_mfma_f32_16x16x32_bf16 v[54:57], v[130:133], v[170:173], v[54:57]
	v_mfma_f32_16x16x32_bf16 v[50:53], v[138:141], v[170:173], v[50:53]
	v_mfma_f32_16x16x32_bf16 v[46:49], v[130:133], v[178:181], v[46:49]
	v_mfma_f32_16x16x32_bf16 v[38:41], v[138:141], v[178:181], v[38:41]
	v_mfma_f32_16x16x32_bf16 v[30:33], v[130:133], v[186:189], v[30:33]
	v_mfma_f32_16x16x32_bf16 v[10:13], v[138:141], v[186:189], v[10:13]
	v_mfma_f32_16x16x32_bf16 v[62:65], v[134:137], v[166:169], v[62:65]
	v_mfma_f32_16x16x32_bf16 v[58:61], v[142:145], v[166:169], v[58:61]
	v_mfma_f32_16x16x32_bf16 v[54:57], v[134:137], v[174:177], v[54:57]
	v_mfma_f32_16x16x32_bf16 v[50:53], v[142:145], v[174:177], v[50:53]
	v_mfma_f32_16x16x32_bf16 v[46:49], v[134:137], v[182:185], v[46:49]
	v_mfma_f32_16x16x32_bf16 v[38:41], v[142:145], v[182:185], v[38:41]
	v_mfma_f32_16x16x32_bf16 v[30:33], v[134:137], v[190:193], v[30:33]
	v_mfma_f32_16x16x32_bf16 v[10:13], v[142:145], v[190:193], v[10:13]
	v_mfma_f32_16x16x32_bf16 v[42:45], v[146:149], v[162:165], v[42:45]
	v_mfma_f32_16x16x32_bf16 v[34:37], v[154:157], v[162:165], v[34:37]
	v_mfma_f32_16x16x32_bf16 v[26:29], v[146:149], v[170:173], v[26:29]
	v_mfma_f32_16x16x32_bf16 v[22:25], v[154:157], v[170:173], v[22:25]
	v_mfma_f32_16x16x32_bf16 v[18:21], v[146:149], v[178:181], v[18:21]
	v_mfma_f32_16x16x32_bf16 v[14:17], v[154:157], v[178:181], v[14:17]
	v_mfma_f32_16x16x32_bf16 v[6:9], v[146:149], v[186:189], v[6:9]
	v_mfma_f32_16x16x32_bf16 v[2:5], v[154:157], v[186:189], v[2:5]
	v_mfma_f32_16x16x32_bf16 v[42:45], v[150:153], v[166:169], v[42:45]
	v_mfma_f32_16x16x32_bf16 v[34:37], v[158:161], v[166:169], v[34:37]
	v_mfma_f32_16x16x32_bf16 v[26:29], v[150:153], v[174:177], v[26:29]
	v_mfma_f32_16x16x32_bf16 v[22:25], v[158:161], v[174:177], v[22:25]
	v_mfma_f32_16x16x32_bf16 v[18:21], v[150:153], v[182:185], v[18:21]
	v_mfma_f32_16x16x32_bf16 v[14:17], v[158:161], v[182:185], v[14:17]
	v_mfma_f32_16x16x32_bf16 v[6:9], v[150:153], v[190:193], v[6:9]
	v_mfma_f32_16x16x32_bf16 v[2:5], v[158:161], v[190:193], v[2:5]
	s_barrier
	s_add_i32 s80, s80, 2
	s_add_u32 s74, s74, 0x10000
	s_addc_u32 s75, s75, 0
	s_add_u32 s58, s58, 0x100
	s_addc_u32 s59, s59, 0
	s_cmp_gt_u32 s80, 29
	s_cbranch_scc0 .LBB0_660
	s_setprio 0
	s_and_b64 vcc, exec, s[24:25]
	s_cbranch_vccz .LBB0_663
	s_barrier

.LBB0_782:
	s_ashr_i32 s55, s54, 31
	s_lshl_b64 s[26:27], s[54:55], 20
	v_readlane_b32 s56, v254, 56
	v_readlane_b32 s57, v254, 57
	s_add_u32 s56, s56, s26
	s_addc_u32 s57, s57, s27
	s_and_b64 s[26:27], s[0:1], exec
	s_cselect_b32 s55, s57, s65
	s_cselect_b32 s81, s56, s64
	s_ashr_i32 s53, s52, 31
	s_lshl_b64 s[26:27], s[52:53], 20
	s_add_u32 s58, s3, s26
	s_addc_u32 s59, s33, s27
	s_and_b64 s[26:27], s[0:1], exec
	s_cselect_b32 s53, s59, s63
	s_cselect_b32 s82, s58, s62
	s_add_u32 s83, s62, 0x10000
	s_addc_u32 s84, s63, 0
	s_add_u32 s62, s64, 0x80080
	v_mov_b32_e32 v2, 0
	s_addc_u32 s63, s65, 0
	s_mov_b32 s85, -2
	v_mov_b32_e32 v3, v2
	v_mov_b32_e32 v4, v2
	v_mov_b32_e32 v5, v2
	v_mov_b32_e32 v10, v2
	v_mov_b32_e32 v11, v2
	v_mov_b32_e32 v12, v2
	v_mov_b32_e32 v13, v2
	v_mov_b32_e32 v18, v2
	v_mov_b32_e32 v19, v2
	v_mov_b32_e32 v20, v2
	v_mov_b32_e32 v21, v2
	v_mov_b32_e32 v26, v2
	v_mov_b32_e32 v27, v2
	v_mov_b32_e32 v28, v2
	v_mov_b32_e32 v29, v2
	v_mov_b32_e32 v34, v2
	v_mov_b32_e32 v35, v2
	v_mov_b32_e32 v36, v2
	v_mov_b32_e32 v37, v2
	v_mov_b32_e32 v42, v2
	v_mov_b32_e32 v43, v2
	v_mov_b32_e32 v44, v2
	v_mov_b32_e32 v45, v2
	v_mov_b32_e32 v50, v2
	v_mov_b32_e32 v51, v2
	v_mov_b32_e32 v52, v2
	v_mov_b32_e32 v53, v2
	v_mov_b32_e32 v58, v2
	v_mov_b32_e32 v59, v2
	v_mov_b32_e32 v60, v2
	v_mov_b32_e32 v61, v2
	v_mov_b32_e32 v6, v2
	v_mov_b32_e32 v7, v2
	v_mov_b32_e32 v8, v2
	v_mov_b32_e32 v9, v2
	v_mov_b32_e32 v14, v2
	v_mov_b32_e32 v15, v2
	v_mov_b32_e32 v16, v2
	v_mov_b32_e32 v17, v2
	v_mov_b32_e32 v22, v2
	v_mov_b32_e32 v23, v2
	v_mov_b32_e32 v24, v2
	v_mov_b32_e32 v25, v2
	v_mov_b32_e32 v30, v2
	v_mov_b32_e32 v31, v2
	v_mov_b32_e32 v32, v2
	v_mov_b32_e32 v33, v2
	v_mov_b32_e32 v38, v2
	v_mov_b32_e32 v39, v2
	v_mov_b32_e32 v40, v2
	v_mov_b32_e32 v41, v2
	v_mov_b32_e32 v46, v2
	v_mov_b32_e32 v47, v2
	v_mov_b32_e32 v48, v2
	v_mov_b32_e32 v49, v2
	v_mov_b32_e32 v54, v2
	v_mov_b32_e32 v55, v2
	v_mov_b32_e32 v56, v2
	v_mov_b32_e32 v57, v2
	v_mov_b32_e32 v62, v2
	v_mov_b32_e32 v63, v2
	v_mov_b32_e32 v64, v2
	v_mov_b32_e32 v65, v2
	v_mov_b32_e32 v66, v2
	v_mov_b32_e32 v67, v2
	v_mov_b32_e32 v68, v2
	v_mov_b32_e32 v69, v2
	v_mov_b32_e32 v74, v2
	v_mov_b32_e32 v75, v2
	v_mov_b32_e32 v76, v2
	v_mov_b32_e32 v77, v2
	v_mov_b32_e32 v82, v2
	v_mov_b32_e32 v83, v2
	v_mov_b32_e32 v84, v2
	v_mov_b32_e32 v85, v2
	v_mov_b32_e32 v90, v2
	v_mov_b32_e32 v91, v2
	v_mov_b32_e32 v92, v2
	v_mov_b32_e32 v93, v2
	v_mov_b32_e32 v98, v2
	v_mov_b32_e32 v99, v2
	v_mov_b32_e32 v100, v2
	v_mov_b32_e32 v101, v2
	v_mov_b32_e32 v106, v2
	v_mov_b32_e32 v107, v2
	v_mov_b32_e32 v108, v2
	v_mov_b32_e32 v109, v2
	v_mov_b32_e32 v114, v2
	v_mov_b32_e32 v115, v2
	v_mov_b32_e32 v116, v2
	v_mov_b32_e32 v117, v2
	v_mov_b32_e32 v122, v2
	v_mov_b32_e32 v123, v2
	v_mov_b32_e32 v124, v2
	v_mov_b32_e32 v125, v2
	v_mov_b32_e32 v70, v2
	v_mov_b32_e32 v71, v2
	v_mov_b32_e32 v72, v2
	v_mov_b32_e32 v73, v2
	v_mov_b32_e32 v78, v2
	v_mov_b32_e32 v79, v2
	v_mov_b32_e32 v80, v2
	v_mov_b32_e32 v81, v2
	v_mov_b32_e32 v86, v2
	v_mov_b32_e32 v87, v2
	v_mov_b32_e32 v88, v2
	v_mov_b32_e32 v89, v2
	v_mov_b32_e32 v94, v2
	v_mov_b32_e32 v95, v2
	v_mov_b32_e32 v96, v2
	v_mov_b32_e32 v97, v2
	v_mov_b32_e32 v102, v2
	v_mov_b32_e32 v103, v2
	v_mov_b32_e32 v104, v2
	v_mov_b32_e32 v105, v2
	v_mov_b32_e32 v110, v2
	v_mov_b32_e32 v111, v2
	v_mov_b32_e32 v112, v2
	v_mov_b32_e32 v113, v2
	v_mov_b32_e32 v118, v2
	v_mov_b32_e32 v119, v2
	v_mov_b32_e32 v120, v2
	v_mov_b32_e32 v121, v2
	v_mov_b32_e32 v126, v2
	v_mov_b32_e32 v127, v2
	v_mov_b32_e32 v128, v2
	v_mov_b32_e32 v129, v2
	v_readfirstlane_b32 s98, v0
	s_lshr_b32 s98, s98, 8
	s_cmp_eq_u32 s98, 1
	s_cbranch_scc0 .Lprio_skip6
	s_setprio 1
.Lprio_skip6:
.LBB0_783:
	ds_read_b128 v[144:147], v151
	ds_read_b128 v[156:159], v151 offset:1024
	ds_read_b128 v[160:163], v151 offset:2048
	ds_read_b128 v[164:167], v151 offset:3072
	ds_read_b128 v[168:171], v152
	ds_read_b128 v[172:175], v152 offset:1024
	ds_read_b128 v[176:179], v152 offset:2048
	ds_read_b128 v[180:183], v152 offset:3072
	s_add_u32 s26, s62, 0xfff80080
	s_addc_u32 s27, s63, -1
	s_cmp_eq_u32 s85, 28
	s_cselect_b32 s65, s55, s27
	s_cselect_b32 s64, s81, s26
	s_cselect_b32 s27, s53, s84
	s_cselect_b32 s26, s82, s83
	v_lshl_add_u64 v[216:217], s[62:63], 0, v[136:137]
	s_add_i32 m0, s61, 0xc000
	ds_read_b128 v[184:187], v153
	ds_read_b128 v[188:191], v153 offset:1024
	ds_read_b128 v[192:195], v153 offset:2048
	ds_read_b128 v[196:199], v153 offset:3072
	ds_read_b128 v[200:203], v153 offset:4096
	ds_read_b128 v[204:207], v153 offset:5120
	ds_read_b128 v[208:211], v153 offset:6144
	ds_read_b128 v[212:215], v153 offset:7168
	global_load_lds_dwordx4 v[216:217], off
	v_lshl_add_u64 v[216:217], s[62:63], 0, v[138:139]
	s_add_i32 m0, s61, 0xe000
	s_nop 0
	global_load_lds_dwordx4 v[216:217], off
	s_waitcnt vmcnt(8)
	s_waitcnt lgkmcnt(0)
	s_barrier
	s_waitcnt lgkmcnt(0)
	v_mfma_f32_16x16x32_bf16 v[126:129], v[144:147], v[184:187], v[126:129]
	v_mfma_f32_16x16x32_bf16 v[118:121], v[160:163], v[184:187], v[118:121]
	v_mfma_f32_16x16x32_bf16 v[110:113], v[144:147], v[192:195], v[110:113]
	v_mfma_f32_16x16x32_bf16 v[102:105], v[160:163], v[192:195], v[102:105]
	v_mfma_f32_16x16x32_bf16 v[94:97], v[144:147], v[200:203], v[94:97]
	v_mfma_f32_16x16x32_bf16 v[86:89], v[160:163], v[200:203], v[86:89]
	v_mfma_f32_16x16x32_bf16 v[78:81], v[144:147], v[208:211], v[78:81]
	v_mfma_f32_16x16x32_bf16 v[70:73], v[160:163], v[208:211], v[70:73]
	v_mfma_f32_16x16x32_bf16 v[126:129], v[156:159], v[188:191], v[126:129]
	v_mfma_f32_16x16x32_bf16 v[118:121], v[164:167], v[188:191], v[118:121]
	v_mfma_f32_16x16x32_bf16 v[110:113], v[156:159], v[196:199], v[110:113]
	v_mfma_f32_16x16x32_bf16 v[102:105], v[164:167], v[196:199], v[102:105]
	v_mfma_f32_16x16x32_bf16 v[94:97], v[156:159], v[204:207], v[94:97]
	v_mfma_f32_16x16x32_bf16 v[86:89], v[164:167], v[204:207], v[86:89]
	v_mfma_f32_16x16x32_bf16 v[78:81], v[156:159], v[212:215], v[78:81]
	v_mfma_f32_16x16x32_bf16 v[70:73], v[164:167], v[212:215], v[70:73]
	v_mfma_f32_16x16x32_bf16 v[122:125], v[168:171], v[184:187], v[122:125]
	v_mfma_f32_16x16x32_bf16 v[114:117], v[176:179], v[184:187], v[114:117]
	v_mfma_f32_16x16x32_bf16 v[106:109], v[168:171], v[192:195], v[106:109]
	v_mfma_f32_16x16x32_bf16 v[98:101], v[176:179], v[192:195], v[98:101]
	v_mfma_f32_16x16x32_bf16 v[90:93], v[168:171], v[200:203], v[90:93]
	v_mfma_f32_16x16x32_bf16 v[82:85], v[176:179], v[200:203], v[82:85]
	v_mfma_f32_16x16x32_bf16 v[74:77], v[168:171], v[208:211], v[74:77]
	v_mfma_f32_16x16x32_bf16 v[66:69], v[176:179], v[208:211], v[66:69]
	v_mfma_f32_16x16x32_bf16 v[122:125], v[172:175], v[188:191], v[122:125]
	v_mfma_f32_16x16x32_bf16 v[114:117], v[180:183], v[188:191], v[114:117]
	v_mfma_f32_16x16x32_bf16 v[106:109], v[172:175], v[196:199], v[106:109]
	v_mfma_f32_16x16x32_bf16 v[98:101], v[180:183], v[196:199], v[98:101]
	v_mfma_f32_16x16x32_bf16 v[90:93], v[172:175], v[204:207], v[90:93]
	v_mfma_f32_16x16x32_bf16 v[82:85], v[180:183], v[204:207], v[82:85]
	v_mfma_f32_16x16x32_bf16 v[74:77], v[172:175], v[212:215], v[74:77]
	v_mfma_f32_16x16x32_bf16 v[66:69], v[180:183], v[212:215], v[66:69]
	s_barrier
	v_lshl_add_u64 v[216:217], s[26:27], 0, v[130:131]
	s_add_i32 s26, s73, s35
	s_mov_b32 m0, s26
	ds_read_b128 v[184:187], v153 offset:16384
	ds_read_b128 v[188:191], v153 offset:17408
	ds_read_b128 v[192:195], v153 offset:18432
	ds_read_b128 v[196:199], v153 offset:19456
	ds_read_b128 v[200:203], v153 offset:20480
	ds_read_b128 v[204:207], v153 offset:21504
	ds_read_b128 v[208:211], v153 offset:22528
	ds_read_b128 v[212:215], v153 offset:23552
	global_load_lds_dwordx4 v[216:217], off
	v_lshl_add_u64 v[220:221], v[216:217], 0, s[6:7]
	s_add_i32 m0, s26, 0x2000
	s_add_i32 s26, s74, s35
	global_load_lds_dwordx4 v[220:221], off
	v_lshl_add_u64 v[220:221], v[216:217], 0, s[8:9]
	s_mov_b32 m0, s26
	v_lshl_add_u64 v[222:223], s[64:65], 0, v[134:135]
	global_load_lds_dwordx4 v[220:221], off
	v_lshl_add_u64 v[220:221], v[216:217], 0, s[10:11]
	s_add_i32 m0, s26, 0x2000
	s_nop 0
	global_load_lds_dwordx4 v[220:221], off
	v_lshl_add_u64 v[220:221], s[64:65], 0, v[132:133]
	s_mov_b32 m0, s61
	s_nop 0
	global_load_lds_dwordx4 v[220:221], off
	s_mov_b32 m0, s66
	s_nop 0
	global_load_lds_dwordx4 v[222:223], off
	s_waitcnt vmcnt(8)
	s_waitcnt lgkmcnt(0)
	s_barrier
	s_waitcnt lgkmcnt(0)
	v_mfma_f32_16x16x32_bf16 v[62:65], v[144:147], v[184:187], v[62:65]
	v_mfma_f32_16x16x32_bf16 v[54:57], v[160:163], v[184:187], v[54:57]
	v_mfma_f32_16x16x32_bf16 v[46:49], v[144:147], v[192:195], v[46:49]
	v_mfma_f32_16x16x32_bf16 v[38:41], v[160:163], v[192:195], v[38:41]
	v_mfma_f32_16x16x32_bf16 v[30:33], v[144:147], v[200:203], v[30:33]
	v_mfma_f32_16x16x32_bf16 v[22:25], v[160:163], v[200:203], v[22:25]
	v_mfma_f32_16x16x32_bf16 v[14:17], v[144:147], v[208:211], v[14:17]
	v_mfma_f32_16x16x32_bf16 v[6:9], v[160:163], v[208:211], v[6:9]
	v_mfma_f32_16x16x32_bf16 v[62:65], v[156:159], v[188:191], v[62:65]
	v_mfma_f32_16x16x32_bf16 v[54:57], v[164:167], v[188:191], v[54:57]
	v_mfma_f32_16x16x32_bf16 v[46:49], v[156:159], v[196:199], v[46:49]
	v_mfma_f32_16x16x32_bf16 v[38:41], v[164:167], v[196:199], v[38:41]
	v_mfma_f32_16x16x32_bf16 v[30:33], v[156:159], v[204:207], v[30:33]
	v_mfma_f32_16x16x32_bf16 v[22:25], v[164:167], v[204:207], v[22:25]
	v_mfma_f32_16x16x32_bf16 v[14:17], v[156:159], v[212:215], v[14:17]
	v_mfma_f32_16x16x32_bf16 v[6:9], v[164:167], v[212:215], v[6:9]
	v_mfma_f32_16x16x32_bf16 v[58:61], v[168:171], v[184:187], v[58:61]
	v_mfma_f32_16x16x32_bf16 v[50:53], v[176:179], v[184:187], v[50:53]
	v_mfma_f32_16x16x32_bf16 v[42:45], v[168:171], v[192:195], v[42:45]
	v_mfma_f32_16x16x32_bf16 v[34:37], v[176:179], v[192:195], v[34:37]
	v_mfma_f32_16x16x32_bf16 v[26:29], v[168:171], v[200:203], v[26:29]
	v_mfma_f32_16x16x32_bf16 v[18:21], v[176:179], v[200:203], v[18:21]
	v_mfma_f32_16x16x32_bf16 v[10:13], v[168:171], v[208:211], v[10:13]
	v_mfma_f32_16x16x32_bf16 v[2:5], v[176:179], v[208:211], v[2:5]
	v_mfma_f32_16x16x32_bf16 v[58:61], v[172:175], v[188:191], v[58:61]
	v_mfma_f32_16x16x32_bf16 v[50:53], v[180:183], v[188:191], v[50:53]
	v_mfma_f32_16x16x32_bf16 v[42:45], v[172:175], v[196:199], v[42:45]
	v_mfma_f32_16x16x32_bf16 v[34:37], v[180:183], v[196:199], v[34:37]
	v_mfma_f32_16x16x32_bf16 v[26:29], v[172:175], v[204:207], v[26:29]
	v_mfma_f32_16x16x32_bf16 v[18:21], v[180:183], v[204:207], v[18:21]
	v_mfma_f32_16x16x32_bf16 v[10:13], v[172:175], v[212:215], v[10:13]
	v_mfma_f32_16x16x32_bf16 v[2:5], v[180:183], v[212:215], v[2:5]
	s_barrier
	s_add_i32 s86, 0, 0x18000
	v_add_u32_e32 v155, s86, v149
	s_add_i32 s87, 0, 0x1c000
	ds_read_b128 v[144:147], v155
	ds_read_b128 v[156:159], v155 offset:1024
	ds_read_b128 v[160:163], v155 offset:2048
	ds_read_b128 v[164:167], v155 offset:3072
	v_add_u32_e32 v155, s87, v149
	ds_read_b128 v[168:171], v155
	ds_read_b128 v[172:175], v155 offset:1024
	ds_read_b128 v[176:179], v155 offset:2048
	ds_read_b128 v[180:183], v155 offset:3072
	s_add_u32 s26, s64, 0x80000
	s_addc_u32 s27, s65, 0
	s_mov_b32 m0, s67
	v_lshl_add_u64 v[224:225], s[26:27], 0, v[132:133]
	ds_read_b128 v[184:187], v153 offset:32768
	ds_read_b128 v[188:191], v153 offset:33792
	ds_read_b128 v[192:195], v153 offset:34816
	ds_read_b128 v[196:199], v153 offset:35840
	ds_read_b128 v[200:203], v153 offset:36864
	ds_read_b128 v[204:207], v153 offset:37888
	ds_read_b128 v[208:211], v153 offset:38912
	ds_read_b128 v[212:215], v153 offset:39936
	global_load_lds_dwordx4 v[224:225], off
	v_lshl_add_u64 v[224:225], s[26:27], 0, v[134:135]
	s_mov_b32 m0, s68
	s_nop 0
	global_load_lds_dwordx4 v[224:225], off
	s_waitcnt vmcnt(8)
	s_waitcnt lgkmcnt(0)
	s_barrier
	s_waitcnt lgkmcnt(0)
	v_mfma_f32_16x16x32_bf16 v[126:129], v[144:147], v[184:187], v[126:129]
	v_mfma_f32_16x16x32_bf16 v[118:121], v[160:163], v[184:187], v[118:121]
	v_mfma_f32_16x16x32_bf16 v[110:113], v[144:147], v[192:195], v[110:113]
	v_mfma_f32_16x16x32_bf16 v[102:105], v[160:163], v[192:195], v[102:105]
	v_mfma_f32_16x16x32_bf16 v[94:97], v[144:147], v[200:203], v[94:97]
	v_mfma_f32_16x16x32_bf16 v[86:89], v[160:163], v[200:203], v[86:89]
	v_mfma_f32_16x16x32_bf16 v[78:81], v[144:147], v[208:211], v[78:81]
	v_mfma_f32_16x16x32_bf16 v[70:73], v[160:163], v[208:211], v[70:73]
	v_mfma_f32_16x16x32_bf16 v[126:129], v[156:159], v[188:191], v[126:129]
	v_mfma_f32_16x16x32_bf16 v[118:121], v[164:167], v[188:191], v[118:121]
	v_mfma_f32_16x16x32_bf16 v[110:113], v[156:159], v[196:199], v[110:113]
	v_mfma_f32_16x16x32_bf16 v[102:105], v[164:167], v[196:199], v[102:105]
	v_mfma_f32_16x16x32_bf16 v[94:97], v[156:159], v[204:207], v[94:97]
	v_mfma_f32_16x16x32_bf16 v[86:89], v[164:167], v[204:207], v[86:89]
	v_mfma_f32_16x16x32_bf16 v[78:81], v[156:159], v[212:215], v[78:81]
	v_mfma_f32_16x16x32_bf16 v[70:73], v[164:167], v[212:215], v[70:73]
	v_mfma_f32_16x16x32_bf16 v[122:125], v[168:171], v[184:187], v[122:125]
	v_mfma_f32_16x16x32_bf16 v[114:117], v[176:179], v[184:187], v[114:117]
	v_mfma_f32_16x16x32_bf16 v[106:109], v[168:171], v[192:195], v[106:109]
	v_mfma_f32_16x16x32_bf16 v[98:101], v[176:179], v[192:195], v[98:101]
	v_mfma_f32_16x16x32_bf16 v[90:93], v[168:171], v[200:203], v[90:93]
	v_mfma_f32_16x16x32_bf16 v[82:85], v[176:179], v[200:203], v[82:85]
	v_mfma_f32_16x16x32_bf16 v[74:77], v[168:171], v[208:211], v[74:77]
	v_mfma_f32_16x16x32_bf16 v[66:69], v[176:179], v[208:211], v[66:69]
	v_mfma_f32_16x16x32_bf16 v[122:125], v[172:175], v[188:191], v[122:125]
	v_mfma_f32_16x16x32_bf16 v[114:117], v[180:183], v[188:191], v[114:117]
	v_mfma_f32_16x16x32_bf16 v[106:109], v[172:175], v[196:199], v[106:109]
	v_mfma_f32_16x16x32_bf16 v[98:101], v[180:183], v[196:199], v[98:101]
	v_mfma_f32_16x16x32_bf16 v[90:93], v[172:175], v[204:207], v[90:93]
	v_mfma_f32_16x16x32_bf16 v[82:85], v[180:183], v[204:207], v[82:85]
	v_mfma_f32_16x16x32_bf16 v[74:77], v[172:175], v[212:215], v[74:77]
	v_mfma_f32_16x16x32_bf16 v[66:69], v[180:183], v[212:215], v[66:69]
	s_barrier
	s_add_i32 s26, s86, s35
	v_lshl_add_u64 v[224:225], v[216:217], 0, s[16:17]
	s_mov_b32 m0, s26
	ds_read_b128 v[184:187], v153 offset:49152
	ds_read_b128 v[188:191], v153 offset:50176
	ds_read_b128 v[192:195], v153 offset:51200
	ds_read_b128 v[196:199], v153 offset:52224
	ds_read_b128 v[200:203], v153 offset:53248
	ds_read_b128 v[204:207], v153 offset:54272
	ds_read_b128 v[208:211], v153 offset:55296
	ds_read_b128 v[212:215], v153 offset:56320
	global_load_lds_dwordx4 v[224:225], off
	v_lshl_add_u64 v[224:225], v[216:217], 0, s[18:19]
	s_add_i32 m0, s26, 0x2000
	s_add_i32 s26, s87, s35
	global_load_lds_dwordx4 v[224:225], off
	v_lshl_add_u64 v[224:225], v[216:217], 0, s[22:23]
	s_mov_b32 m0, s26
	v_lshl_add_u64 v[216:217], v[216:217], 0, s[24:25]
	global_load_lds_dwordx4 v[224:225], off
	s_add_i32 m0, s26, 0x2000
	s_nop 0
	global_load_lds_dwordx4 v[216:217], off
	v_lshl_add_u64 v[216:217], v[220:221], 0, s[20:21]
	s_mov_b32 m0, s70
	s_nop 0
	global_load_lds_dwordx4 v[216:217], off
	v_lshl_add_u64 v[216:217], v[222:223], 0, s[20:21]
	s_mov_b32 m0, s71
	s_nop 0
	global_load_lds_dwordx4 v[216:217], off
	s_waitcnt vmcnt(8)
	s_waitcnt lgkmcnt(0)
	s_barrier
	s_waitcnt lgkmcnt(0)
	v_mfma_f32_16x16x32_bf16 v[62:65], v[144:147], v[184:187], v[62:65]
	v_mfma_f32_16x16x32_bf16 v[54:57], v[160:163], v[184:187], v[54:57]
	v_mfma_f32_16x16x32_bf16 v[46:49], v[144:147], v[192:195], v[46:49]
	v_mfma_f32_16x16x32_bf16 v[38:41], v[160:163], v[192:195], v[38:41]
	v_mfma_f32_16x16x32_bf16 v[30:33], v[144:147], v[200:203], v[30:33]
	v_mfma_f32_16x16x32_bf16 v[22:25], v[160:163], v[200:203], v[22:25]
	v_mfma_f32_16x16x32_bf16 v[14:17], v[144:147], v[208:211], v[14:17]
	v_mfma_f32_16x16x32_bf16 v[6:9], v[160:163], v[208:211], v[6:9]
	v_mfma_f32_16x16x32_bf16 v[62:65], v[156:159], v[188:191], v[62:65]
	v_mfma_f32_16x16x32_bf16 v[54:57], v[164:167], v[188:191], v[54:57]
	v_mfma_f32_16x16x32_bf16 v[46:49], v[156:159], v[196:199], v[46:49]
	v_mfma_f32_16x16x32_bf16 v[38:41], v[164:167], v[196:199], v[38:41]
	v_mfma_f32_16x16x32_bf16 v[30:33], v[156:159], v[204:207], v[30:33]
	v_mfma_f32_16x16x32_bf16 v[22:25], v[164:167], v[204:207], v[22:25]
	v_mfma_f32_16x16x32_bf16 v[14:17], v[156:159], v[212:215], v[14:17]
	v_mfma_f32_16x16x32_bf16 v[6:9], v[164:167], v[212:215], v[6:9]
	v_mfma_f32_16x16x32_bf16 v[58:61], v[168:171], v[184:187], v[58:61]
	v_mfma_f32_16x16x32_bf16 v[50:53], v[176:179], v[184:187], v[50:53]
	v_mfma_f32_16x16x32_bf16 v[42:45], v[168:171], v[192:195], v[42:45]
	v_mfma_f32_16x16x32_bf16 v[34:37], v[176:179], v[192:195], v[34:37]
	v_mfma_f32_16x16x32_bf16 v[26:29], v[168:171], v[200:203], v[26:29]
	v_mfma_f32_16x16x32_bf16 v[18:21], v[176:179], v[200:203], v[18:21]
	v_mfma_f32_16x16x32_bf16 v[10:13], v[168:171], v[208:211], v[10:13]
	v_mfma_f32_16x16x32_bf16 v[2:5], v[176:179], v[208:211], v[2:5]
	v_mfma_f32_16x16x32_bf16 v[58:61], v[172:175], v[188:191], v[58:61]
	v_mfma_f32_16x16x32_bf16 v[50:53], v[180:183], v[188:191], v[50:53]
	v_mfma_f32_16x16x32_bf16 v[42:45], v[172:175], v[196:199], v[42:45]
	v_mfma_f32_16x16x32_bf16 v[34:37], v[180:183], v[196:199], v[34:37]
	v_mfma_f32_16x16x32_bf16 v[26:29], v[172:175], v[204:207], v[26:29]
	v_mfma_f32_16x16x32_bf16 v[18:21], v[180:183], v[204:207], v[18:21]
	v_mfma_f32_16x16x32_bf16 v[10:13], v[172:175], v[212:215], v[10:13]
	v_mfma_f32_16x16x32_bf16 v[2:5], v[180:183], v[212:215], v[2:5]
	s_barrier
	s_add_i32 s85, s85, 2
	s_add_u32 s83, s83, 0x10000
	s_addc_u32 s84, s84, 0
	s_add_u32 s62, s62, 0x100
	s_addc_u32 s63, s63, 0
	s_cmp_gt_u32 s85, 29
	s_cbranch_scc0 .LBB0_783
	s_setprio 0
	s_and_b64 vcc, exec, s[40:41]
	s_cbranch_vccz .LBB0_786
	s_barrier

.LBB0_857:
	s_add_u32 s72, s50, 0x10000
	s_addc_u32 s73, s51, 0
	s_add_u32 s50, s52, 0xb0080
	v_mov_b32_e32 v34, 0
	s_addc_u32 s51, s53, 0
	s_mov_b32 s74, -2
	v_mov_b32_e32 v35, v34
	v_mov_b32_e32 v36, v34
	v_mov_b32_e32 v37, v34
	v_mov_b32_e32 v38, v34
	v_mov_b32_e32 v39, v34
	v_mov_b32_e32 v40, v34
	v_mov_b32_e32 v41, v34
	v_mov_b32_e32 v42, v34
	v_mov_b32_e32 v43, v34
	v_mov_b32_e32 v44, v34
	v_mov_b32_e32 v45, v34
	v_mov_b32_e32 v50, v34
	v_mov_b32_e32 v51, v34
	v_mov_b32_e32 v52, v34
	v_mov_b32_e32 v53, v34
	v_mov_b32_e32 v58, v34
	v_mov_b32_e32 v59, v34
	v_mov_b32_e32 v60, v34
	v_mov_b32_e32 v61, v34
	v_mov_b32_e32 v66, v34
	v_mov_b32_e32 v67, v34
	v_mov_b32_e32 v68, v34
	v_mov_b32_e32 v69, v34
	v_mov_b32_e32 v74, v34
	v_mov_b32_e32 v75, v34
	v_mov_b32_e32 v76, v34
	v_mov_b32_e32 v77, v34
	v_mov_b32_e32 v82, v34
	v_mov_b32_e32 v83, v34
	v_mov_b32_e32 v84, v34
	v_mov_b32_e32 v85, v34
	v_mov_b32_e32 v46, v34
	v_mov_b32_e32 v47, v34
	v_mov_b32_e32 v48, v34
	v_mov_b32_e32 v49, v34
	v_mov_b32_e32 v54, v34
	v_mov_b32_e32 v55, v34
	v_mov_b32_e32 v56, v34
	v_mov_b32_e32 v57, v34
	v_mov_b32_e32 v62, v34
	v_mov_b32_e32 v63, v34
	v_mov_b32_e32 v64, v34
	v_mov_b32_e32 v65, v34
	v_mov_b32_e32 v70, v34
	v_mov_b32_e32 v71, v34
	v_mov_b32_e32 v72, v34
	v_mov_b32_e32 v73, v34
	v_mov_b32_e32 v78, v34
	v_mov_b32_e32 v79, v34
	v_mov_b32_e32 v80, v34
	v_mov_b32_e32 v81, v34
	v_mov_b32_e32 v86, v34
	v_mov_b32_e32 v87, v34
	v_mov_b32_e32 v88, v34
	v_mov_b32_e32 v89, v34
	v_mov_b32_e32 v90, v34
	v_mov_b32_e32 v91, v34
	v_mov_b32_e32 v92, v34
	v_mov_b32_e32 v93, v34
	v_mov_b32_e32 v94, v34
	v_mov_b32_e32 v95, v34
	v_mov_b32_e32 v96, v34
	v_mov_b32_e32 v97, v34
	v_mov_b32_e32 v98, v34
	v_mov_b32_e32 v99, v34
	v_mov_b32_e32 v100, v34
	v_mov_b32_e32 v101, v34
	v_mov_b32_e32 v102, v34
	v_mov_b32_e32 v103, v34
	v_mov_b32_e32 v104, v34
	v_mov_b32_e32 v105, v34
	v_mov_b32_e32 v106, v34
	v_mov_b32_e32 v107, v34
	v_mov_b32_e32 v108, v34
	v_mov_b32_e32 v109, v34
	v_mov_b32_e32 v110, v34
	v_mov_b32_e32 v111, v34
	v_mov_b32_e32 v112, v34
	v_mov_b32_e32 v113, v34
	v_mov_b32_e32 v118, v34
	v_mov_b32_e32 v119, v34
	v_mov_b32_e32 v120, v34
	v_mov_b32_e32 v121, v34
	v_mov_b32_e32 v126, v34
	v_mov_b32_e32 v127, v34
	v_mov_b32_e32 v128, v34
	v_mov_b32_e32 v129, v34
	v_mov_b32_e32 v134, v34
	v_mov_b32_e32 v135, v34
	v_mov_b32_e32 v136, v34
	v_mov_b32_e32 v137, v34
	v_mov_b32_e32 v142, v34
	v_mov_b32_e32 v143, v34
	v_mov_b32_e32 v144, v34
	v_mov_b32_e32 v145, v34
	v_mov_b32_e32 v114, v34
	v_mov_b32_e32 v115, v34
	v_mov_b32_e32 v116, v34
	v_mov_b32_e32 v117, v34
	v_mov_b32_e32 v122, v34
	v_mov_b32_e32 v123, v34
	v_mov_b32_e32 v124, v34
	v_mov_b32_e32 v125, v34
	v_mov_b32_e32 v130, v34
	v_mov_b32_e32 v131, v34
	v_mov_b32_e32 v132, v34
	v_mov_b32_e32 v133, v34
	v_mov_b32_e32 v138, v34
	v_mov_b32_e32 v139, v34
	v_mov_b32_e32 v140, v34
	v_mov_b32_e32 v141, v34
	v_mov_b32_e32 v146, v34
	v_mov_b32_e32 v147, v34
	v_mov_b32_e32 v148, v34
	v_mov_b32_e32 v149, v34
	v_mov_b32_e32 v150, v34
	v_mov_b32_e32 v151, v34
	v_mov_b32_e32 v152, v34
	v_mov_b32_e32 v153, v34
	v_mov_b32_e32 v154, v34
	v_mov_b32_e32 v155, v34
	v_mov_b32_e32 v156, v34
	v_mov_b32_e32 v157, v34
	v_mov_b32_e32 v158, v34
	v_mov_b32_e32 v159, v34
	v_mov_b32_e32 v160, v34
	v_mov_b32_e32 v161, v34
	v_readfirstlane_b32 s98, v0
	s_lshr_b32 s98, s98, 8
	s_cmp_eq_u32 s98, 1
	s_cbranch_scc0 .Lprio_skip5
	s_setprio 1
.Lprio_skip5:
.LBB0_858:
	ds_read_b128 v[26:29], v185
	ds_read_b128 v[30:33], v185 offset:1024
	ds_read_b128 v[18:21], v185 offset:2048
	ds_read_b128 v[22:25], v185 offset:3072
	ds_read_b128 v[10:13], v186
	ds_read_b128 v[14:17], v186 offset:1024
	ds_read_b128 v[2:5], v186 offset:2048
	ds_read_b128 v[6:9], v186 offset:3072
	s_add_u32 s26, s50, 0xfff50080
	s_addc_u32 s27, s51, -1
	s_cmp_eq_u32 s74, 40
	s_cselect_b32 s53, s5, s27
	s_cselect_b32 s52, s4, s26
	s_cselect_b32 s55, s45, s73
	s_cselect_b32 s54, s44, s72
	v_lshl_add_u64 v[176:177], s[50:51], 0, v[168:169]
	s_add_i32 m0, s59, 0xc000
	ds_read_b128 v[190:193], v187
	ds_read_b128 v[194:197], v187 offset:1024
	ds_read_b128 v[198:201], v187 offset:2048
	ds_read_b128 v[202:205], v187 offset:3072
	ds_read_b128 v[206:209], v187 offset:4096
	ds_read_b128 v[210:213], v187 offset:5120
	ds_read_b128 v[220:223], v187 offset:6144
	ds_read_b128 v[224:227], v187 offset:7168
	global_load_lds_dwordx4 v[176:177], off
	v_lshl_add_u64 v[176:177], s[50:51], 0, v[170:171]
	s_add_i32 m0, s59, 0xe000
	s_nop 0
	global_load_lds_dwordx4 v[176:177], off
	s_waitcnt vmcnt(8)
	s_waitcnt lgkmcnt(0)
	s_barrier
	s_waitcnt lgkmcnt(0)
	v_mfma_scale_f32_16x16x128_f8f6f4 v[158:161], v[26:33], v[190:197], v[158:161], v188, v189 op_sel_hi:[0,0,0]
	v_mfma_scale_f32_16x16x128_f8f6f4 v[154:157], v[18:25], v[190:197], v[154:157], v188, v189 op_sel_hi:[0,0,0]
	v_mfma_scale_f32_16x16x128_f8f6f4 v[150:153], v[26:33], v[198:205], v[150:153], v188, v189 op_sel_hi:[0,0,0]
	v_mfma_scale_f32_16x16x128_f8f6f4 v[146:149], v[18:25], v[198:205], v[146:149], v188, v189 op_sel_hi:[0,0,0]
	v_mfma_scale_f32_16x16x128_f8f6f4 v[138:141], v[26:33], v[206:213], v[138:141], v188, v189 op_sel_hi:[0,0,0]
	v_mfma_scale_f32_16x16x128_f8f6f4 v[130:133], v[18:25], v[206:213], v[130:133], v188, v189 op_sel_hi:[0,0,0]
	v_mfma_scale_f32_16x16x128_f8f6f4 v[122:125], v[26:33], v[220:227], v[122:125], v188, v189 op_sel_hi:[0,0,0]
	v_mfma_scale_f32_16x16x128_f8f6f4 v[114:117], v[18:25], v[220:227], v[114:117], v188, v189 op_sel_hi:[0,0,0]
	v_mfma_scale_f32_16x16x128_f8f6f4 v[142:145], v[10:17], v[190:197], v[142:145], v188, v189 op_sel_hi:[0,0,0]
	v_mfma_scale_f32_16x16x128_f8f6f4 v[134:137], v[2:9], v[190:197], v[134:137], v188, v189 op_sel_hi:[0,0,0]
	v_mfma_scale_f32_16x16x128_f8f6f4 v[126:129], v[10:17], v[198:205], v[126:129], v188, v189 op_sel_hi:[0,0,0]
	v_mfma_scale_f32_16x16x128_f8f6f4 v[118:121], v[2:9], v[198:205], v[118:121], v188, v189 op_sel_hi:[0,0,0]
	v_mfma_scale_f32_16x16x128_f8f6f4 v[110:113], v[10:17], v[206:213], v[110:113], v188, v189 op_sel_hi:[0,0,0]
	v_mfma_scale_f32_16x16x128_f8f6f4 v[106:109], v[2:9], v[206:213], v[106:109], v188, v189 op_sel_hi:[0,0,0]
	v_mfma_scale_f32_16x16x128_f8f6f4 v[102:105], v[10:17], v[220:227], v[102:105], v188, v189 op_sel_hi:[0,0,0]
	v_mfma_scale_f32_16x16x128_f8f6f4 v[98:101], v[2:9], v[220:227], v[98:101], v188, v189 op_sel_hi:[0,0,0]
	s_barrier
	s_add_i32 s26, s67, s57
	v_lshl_add_u64 v[176:177], s[54:55], 0, v[162:163]
	s_mov_b32 m0, s26
	ds_read_b128 v[190:193], v187 offset:16384
	ds_read_b128 v[194:197], v187 offset:17408
	ds_read_b128 v[198:201], v187 offset:18432
	ds_read_b128 v[202:205], v187 offset:19456
	ds_read_b128 v[206:209], v187 offset:20480
	ds_read_b128 v[210:213], v187 offset:21504
	ds_read_b128 v[220:223], v187 offset:22528
	ds_read_b128 v[224:227], v187 offset:23552
	global_load_lds_dwordx4 v[176:177], off
	v_lshl_add_u64 v[178:179], v[176:177], 0, s[8:9]
	s_add_i32 m0, s26, 0x2000
	s_add_i32 s26, s68, s57
	global_load_lds_dwordx4 v[178:179], off
	v_lshl_add_u64 v[178:179], v[176:177], 0, s[10:11]
	s_mov_b32 m0, s26
	v_lshl_add_u64 v[180:181], s[52:53], 0, v[166:167]
	global_load_lds_dwordx4 v[178:179], off
	v_lshl_add_u64 v[178:179], v[176:177], 0, s[12:13]
	s_add_i32 m0, s26, 0x2000
	s_nop 0
	global_load_lds_dwordx4 v[178:179], off
	v_lshl_add_u64 v[178:179], s[52:53], 0, v[164:165]
	s_mov_b32 m0, s59
	s_nop 0
	global_load_lds_dwordx4 v[178:179], off
	s_mov_b32 m0, s60
	s_nop 0
	global_load_lds_dwordx4 v[180:181], off
	s_waitcnt vmcnt(8)
	s_waitcnt lgkmcnt(0)
	s_barrier
	s_waitcnt lgkmcnt(0)
	v_mfma_scale_f32_16x16x128_f8f6f4 v[94:97], v[26:33], v[190:197], v[94:97], v188, v189 op_sel_hi:[0,0,0]
	v_mfma_scale_f32_16x16x128_f8f6f4 v[90:93], v[18:25], v[190:197], v[90:93], v188, v189 op_sel_hi:[0,0,0]
	v_mfma_scale_f32_16x16x128_f8f6f4 v[86:89], v[26:33], v[198:205], v[86:89], v188, v189 op_sel_hi:[0,0,0]
	v_mfma_scale_f32_16x16x128_f8f6f4 v[78:81], v[18:25], v[198:205], v[78:81], v188, v189 op_sel_hi:[0,0,0]
	v_mfma_scale_f32_16x16x128_f8f6f4 v[70:73], v[26:33], v[206:213], v[70:73], v188, v189 op_sel_hi:[0,0,0]
	v_mfma_scale_f32_16x16x128_f8f6f4 v[62:65], v[18:25], v[206:213], v[62:65], v188, v189 op_sel_hi:[0,0,0]
	v_mfma_scale_f32_16x16x128_f8f6f4 v[54:57], v[26:33], v[220:227], v[54:57], v188, v189 op_sel_hi:[0,0,0]
	v_mfma_scale_f32_16x16x128_f8f6f4 v[46:49], v[18:25], v[220:227], v[46:49], v188, v189 op_sel_hi:[0,0,0]
	v_mfma_scale_f32_16x16x128_f8f6f4 v[82:85], v[10:17], v[190:197], v[82:85], v188, v189 op_sel_hi:[0,0,0]
	v_mfma_scale_f32_16x16x128_f8f6f4 v[74:77], v[2:9], v[190:197], v[74:77], v188, v189 op_sel_hi:[0,0,0]
	v_mfma_scale_f32_16x16x128_f8f6f4 v[66:69], v[10:17], v[198:205], v[66:69], v188, v189 op_sel_hi:[0,0,0]
	v_mfma_scale_f32_16x16x128_f8f6f4 v[58:61], v[2:9], v[198:205], v[58:61], v188, v189 op_sel_hi:[0,0,0]
	v_mfma_scale_f32_16x16x128_f8f6f4 v[50:53], v[10:17], v[206:213], v[50:53], v188, v189 op_sel_hi:[0,0,0]
	v_mfma_scale_f32_16x16x128_f8f6f4 v[42:45], v[2:9], v[206:213], v[42:45], v188, v189 op_sel_hi:[0,0,0]
	v_mfma_scale_f32_16x16x128_f8f6f4 v[38:41], v[10:17], v[220:227], v[38:41], v188, v189 op_sel_hi:[0,0,0]
	v_mfma_scale_f32_16x16x128_f8f6f4 v[34:37], v[2:9], v[220:227], v[34:37], v188, v189 op_sel_hi:[0,0,0]
	s_barrier
	s_add_i32 s54, 0, 0x18000
	s_add_i32 s55, 0, 0x1c000
	v_add_u32_e32 v14, s54, v183
	v_add_u32_e32 v30, s55, v183
	ds_read_b128 v[2:5], v14
	ds_read_b128 v[6:9], v14 offset:1024
	ds_read_b128 v[10:13], v14 offset:2048
	ds_read_b128 v[14:17], v14 offset:3072
	ds_read_b128 v[18:21], v30
	ds_read_b128 v[22:25], v30 offset:1024
	ds_read_b128 v[26:29], v30 offset:2048
	ds_read_b128 v[30:33], v30 offset:3072
	s_add_u32 s26, s52, 0xb0000
	s_addc_u32 s27, s53, 0
	s_mov_b32 m0, s61
	v_lshl_add_u64 v[214:215], s[26:27], 0, v[164:165]
	ds_read_b128 v[190:193], v187 offset:32768
	ds_read_b128 v[194:197], v187 offset:33792
	ds_read_b128 v[198:201], v187 offset:34816
	ds_read_b128 v[202:205], v187 offset:35840
	ds_read_b128 v[206:209], v187 offset:36864
	ds_read_b128 v[210:213], v187 offset:37888
	ds_read_b128 v[220:223], v187 offset:38912
	ds_read_b128 v[224:227], v187 offset:39936
	global_load_lds_dwordx4 v[214:215], off
	v_lshl_add_u64 v[214:215], s[26:27], 0, v[166:167]
	s_mov_b32 m0, s62
	s_nop 0
	global_load_lds_dwordx4 v[214:215], off
	s_waitcnt vmcnt(8)
	s_waitcnt lgkmcnt(0)
	s_barrier
	s_waitcnt lgkmcnt(0)
	v_mfma_scale_f32_16x16x128_f8f6f4 v[158:161], v[2:9], v[190:197], v[158:161], v188, v189 op_sel_hi:[0,0,0]
	v_mfma_scale_f32_16x16x128_f8f6f4 v[154:157], v[10:17], v[190:197], v[154:157], v188, v189 op_sel_hi:[0,0,0]
	v_mfma_scale_f32_16x16x128_f8f6f4 v[150:153], v[2:9], v[198:205], v[150:153], v188, v189 op_sel_hi:[0,0,0]
	v_mfma_scale_f32_16x16x128_f8f6f4 v[146:149], v[10:17], v[198:205], v[146:149], v188, v189 op_sel_hi:[0,0,0]
	v_mfma_scale_f32_16x16x128_f8f6f4 v[138:141], v[2:9], v[206:213], v[138:141], v188, v189 op_sel_hi:[0,0,0]
	v_mfma_scale_f32_16x16x128_f8f6f4 v[130:133], v[10:17], v[206:213], v[130:133], v188, v189 op_sel_hi:[0,0,0]
	v_mfma_scale_f32_16x16x128_f8f6f4 v[122:125], v[2:9], v[220:227], v[122:125], v188, v189 op_sel_hi:[0,0,0]
	v_mfma_scale_f32_16x16x128_f8f6f4 v[114:117], v[10:17], v[220:227], v[114:117], v188, v189 op_sel_hi:[0,0,0]
	v_mfma_scale_f32_16x16x128_f8f6f4 v[142:145], v[18:25], v[190:197], v[142:145], v188, v189 op_sel_hi:[0,0,0]
	v_mfma_scale_f32_16x16x128_f8f6f4 v[134:137], v[26:33], v[190:197], v[134:137], v188, v189 op_sel_hi:[0,0,0]
	v_mfma_scale_f32_16x16x128_f8f6f4 v[126:129], v[18:25], v[198:205], v[126:129], v188, v189 op_sel_hi:[0,0,0]
	v_mfma_scale_f32_16x16x128_f8f6f4 v[118:121], v[26:33], v[198:205], v[118:121], v188, v189 op_sel_hi:[0,0,0]
	v_mfma_scale_f32_16x16x128_f8f6f4 v[110:113], v[18:25], v[206:213], v[110:113], v188, v189 op_sel_hi:[0,0,0]
	v_mfma_scale_f32_16x16x128_f8f6f4 v[106:109], v[26:33], v[206:213], v[106:109], v188, v189 op_sel_hi:[0,0,0]
	v_mfma_scale_f32_16x16x128_f8f6f4 v[102:105], v[18:25], v[220:227], v[102:105], v188, v189 op_sel_hi:[0,0,0]
	v_mfma_scale_f32_16x16x128_f8f6f4 v[98:101], v[26:33], v[220:227], v[98:101], v188, v189 op_sel_hi:[0,0,0]
	s_barrier
	s_add_i32 s26, s54, s57
	v_lshl_add_u64 v[214:215], v[176:177], 0, s[16:17]
	s_mov_b32 m0, s26
	ds_read_b128 v[190:193], v187 offset:49152
	ds_read_b128 v[194:197], v187 offset:50176
	ds_read_b128 v[198:201], v187 offset:51200
	ds_read_b128 v[202:205], v187 offset:52224
	ds_read_b128 v[206:209], v187 offset:53248
	ds_read_b128 v[210:213], v187 offset:54272
	ds_read_b128 v[220:223], v187 offset:55296
	ds_read_b128 v[224:227], v187 offset:56320
	global_load_lds_dwordx4 v[214:215], off
	v_lshl_add_u64 v[214:215], v[176:177], 0, s[18:19]
	s_add_i32 m0, s26, 0x2000
	s_add_i32 s26, s55, s57
	global_load_lds_dwordx4 v[214:215], off
	v_lshl_add_u64 v[214:215], v[176:177], 0, s[22:23]
	s_mov_b32 m0, s26
	v_lshl_add_u64 v[176:177], v[176:177], 0, s[24:25]
	global_load_lds_dwordx4 v[214:215], off
	s_add_i32 m0, s26, 0x2000
	s_nop 0
	global_load_lds_dwordx4 v[176:177], off
	v_lshl_add_u64 v[176:177], v[178:179], 0, s[20:21]
	s_mov_b32 m0, s64
	s_nop 0
	global_load_lds_dwordx4 v[176:177], off
	v_lshl_add_u64 v[176:177], v[180:181], 0, s[20:21]
	s_mov_b32 m0, s65
	s_nop 0
	global_load_lds_dwordx4 v[176:177], off
	s_waitcnt vmcnt(8)
	s_waitcnt lgkmcnt(0)
	s_barrier
	s_waitcnt lgkmcnt(0)
	v_mfma_scale_f32_16x16x128_f8f6f4 v[94:97], v[2:9], v[190:197], v[94:97], v188, v189 op_sel_hi:[0,0,0]
	v_mfma_scale_f32_16x16x128_f8f6f4 v[90:93], v[10:17], v[190:197], v[90:93], v188, v189 op_sel_hi:[0,0,0]
	v_mfma_scale_f32_16x16x128_f8f6f4 v[86:89], v[2:9], v[198:205], v[86:89], v188, v189 op_sel_hi:[0,0,0]
	v_mfma_scale_f32_16x16x128_f8f6f4 v[78:81], v[10:17], v[198:205], v[78:81], v188, v189 op_sel_hi:[0,0,0]
	v_mfma_scale_f32_16x16x128_f8f6f4 v[70:73], v[2:9], v[206:213], v[70:73], v188, v189 op_sel_hi:[0,0,0]
	v_mfma_scale_f32_16x16x128_f8f6f4 v[62:65], v[10:17], v[206:213], v[62:65], v188, v189 op_sel_hi:[0,0,0]
	v_mfma_scale_f32_16x16x128_f8f6f4 v[54:57], v[2:9], v[220:227], v[54:57], v188, v189 op_sel_hi:[0,0,0]
	v_mfma_scale_f32_16x16x128_f8f6f4 v[46:49], v[10:17], v[220:227], v[46:49], v188, v189 op_sel_hi:[0,0,0]
	v_mfma_scale_f32_16x16x128_f8f6f4 v[82:85], v[18:25], v[190:197], v[82:85], v188, v189 op_sel_hi:[0,0,0]
	v_mfma_scale_f32_16x16x128_f8f6f4 v[74:77], v[26:33], v[190:197], v[74:77], v188, v189 op_sel_hi:[0,0,0]
	v_mfma_scale_f32_16x16x128_f8f6f4 v[66:69], v[18:25], v[198:205], v[66:69], v188, v189 op_sel_hi:[0,0,0]
	v_mfma_scale_f32_16x16x128_f8f6f4 v[58:61], v[26:33], v[198:205], v[58:61], v188, v189 op_sel_hi:[0,0,0]
	v_mfma_scale_f32_16x16x128_f8f6f4 v[50:53], v[18:25], v[206:213], v[50:53], v188, v189 op_sel_hi:[0,0,0]
	v_mfma_scale_f32_16x16x128_f8f6f4 v[42:45], v[26:33], v[206:213], v[42:45], v188, v189 op_sel_hi:[0,0,0]
	v_mfma_scale_f32_16x16x128_f8f6f4 v[38:41], v[18:25], v[220:227], v[38:41], v188, v189 op_sel_hi:[0,0,0]
	v_mfma_scale_f32_16x16x128_f8f6f4 v[34:37], v[26:33], v[220:227], v[34:37], v188, v189 op_sel_hi:[0,0,0]
	s_barrier
	s_add_i32 s74, s74, 2
	s_add_u32 s72, s72, 0x10000
	s_addc_u32 s73, s73, 0
	s_add_u32 s50, s50, 0x100
	s_addc_u32 s51, s51, 0
	s_cmp_gt_u32 s74, 41
	s_cbranch_scc0 .LBB0_858
	s_setprio 0
	s_and_b64 vcc, exec, s[40:41]
	s_cbranch_vccz .LBB0_861
	s_barrier

.LBB0_984:
	s_ashr_i32 s45, s44, 31
	s_lshl_b64 s[26:27], s[44:45], 19
	v_readlane_b32 s50, v254, 56
	v_readlane_b32 s51, v254, 57
	s_add_u32 s50, s50, s26
	s_addc_u32 s51, s51, s27
	s_and_b64 s[26:27], s[0:1], exec
	s_cselect_b32 s45, s51, s59
	s_cselect_b32 s72, s50, s58
	s_ashr_i32 s41, s40, 31
	s_lshl_b64 s[26:27], s[40:41], 19
	s_add_u32 s52, s3, s26
	s_addc_u32 s53, s33, s27
	s_and_b64 s[26:27], s[0:1], exec
	s_cselect_b32 s41, s53, s57
	s_cselect_b32 s73, s52, s56
	s_add_u32 s74, s56, 0x10000
	s_addc_u32 s75, s57, 0
	s_add_u32 s56, s58, 0x40080
	v_mov_b32_e32 v34, 0
	s_addc_u32 s57, s59, 0
	s_mov_b32 s80, -2
	v_mov_b32_e32 v35, v34
	v_mov_b32_e32 v36, v34
	v_mov_b32_e32 v37, v34
	v_mov_b32_e32 v38, v34
	v_mov_b32_e32 v39, v34
	v_mov_b32_e32 v40, v34
	v_mov_b32_e32 v41, v34
	v_mov_b32_e32 v46, v34
	v_mov_b32_e32 v47, v34
	v_mov_b32_e32 v48, v34
	v_mov_b32_e32 v49, v34
	v_mov_b32_e32 v54, v34
	v_mov_b32_e32 v55, v34
	v_mov_b32_e32 v56, v34
	v_mov_b32_e32 v57, v34
	v_mov_b32_e32 v62, v34
	v_mov_b32_e32 v63, v34
	v_mov_b32_e32 v64, v34
	v_mov_b32_e32 v65, v34
	v_mov_b32_e32 v70, v34
	v_mov_b32_e32 v71, v34
	v_mov_b32_e32 v72, v34
	v_mov_b32_e32 v73, v34
	v_mov_b32_e32 v78, v34
	v_mov_b32_e32 v79, v34
	v_mov_b32_e32 v80, v34
	v_mov_b32_e32 v81, v34
	v_mov_b32_e32 v86, v34
	v_mov_b32_e32 v87, v34
	v_mov_b32_e32 v88, v34
	v_mov_b32_e32 v89, v34
	v_mov_b32_e32 v42, v34
	v_mov_b32_e32 v43, v34
	v_mov_b32_e32 v44, v34
	v_mov_b32_e32 v45, v34
	v_mov_b32_e32 v50, v34
	v_mov_b32_e32 v51, v34
	v_mov_b32_e32 v52, v34
	v_mov_b32_e32 v53, v34
	v_mov_b32_e32 v58, v34
	v_mov_b32_e32 v59, v34
	v_mov_b32_e32 v60, v34
	v_mov_b32_e32 v61, v34
	v_mov_b32_e32 v66, v34
	v_mov_b32_e32 v67, v34
	v_mov_b32_e32 v68, v34
	v_mov_b32_e32 v69, v34
	v_mov_b32_e32 v74, v34
	v_mov_b32_e32 v75, v34
	v_mov_b32_e32 v76, v34
	v_mov_b32_e32 v77, v34
	v_mov_b32_e32 v82, v34
	v_mov_b32_e32 v83, v34
	v_mov_b32_e32 v84, v34
	v_mov_b32_e32 v85, v34
	v_mov_b32_e32 v90, v34
	v_mov_b32_e32 v91, v34
	v_mov_b32_e32 v92, v34
	v_mov_b32_e32 v93, v34
	v_mov_b32_e32 v94, v34
	v_mov_b32_e32 v95, v34
	v_mov_b32_e32 v96, v34
	v_mov_b32_e32 v97, v34
	v_mov_b32_e32 v98, v34
	v_mov_b32_e32 v99, v34
	v_mov_b32_e32 v100, v34
	v_mov_b32_e32 v101, v34
	v_mov_b32_e32 v102, v34
	v_mov_b32_e32 v103, v34
	v_mov_b32_e32 v104, v34
	v_mov_b32_e32 v105, v34
	v_mov_b32_e32 v110, v34
	v_mov_b32_e32 v111, v34
	v_mov_b32_e32 v112, v34
	v_mov_b32_e32 v113, v34
	v_mov_b32_e32 v118, v34
	v_mov_b32_e32 v119, v34
	v_mov_b32_e32 v120, v34
	v_mov_b32_e32 v121, v34
	v_mov_b32_e32 v126, v34
	v_mov_b32_e32 v127, v34
	v_mov_b32_e32 v128, v34
	v_mov_b32_e32 v129, v34
	v_mov_b32_e32 v134, v34
	v_mov_b32_e32 v135, v34
	v_mov_b32_e32 v136, v34
	v_mov_b32_e32 v137, v34
	v_mov_b32_e32 v142, v34
	v_mov_b32_e32 v143, v34
	v_mov_b32_e32 v144, v34
	v_mov_b32_e32 v145, v34
	v_mov_b32_e32 v150, v34
	v_mov_b32_e32 v151, v34
	v_mov_b32_e32 v152, v34
	v_mov_b32_e32 v153, v34
	v_mov_b32_e32 v106, v34
	v_mov_b32_e32 v107, v34
	v_mov_b32_e32 v108, v34
	v_mov_b32_e32 v109, v34
	v_mov_b32_e32 v114, v34
	v_mov_b32_e32 v115, v34
	v_mov_b32_e32 v116, v34
	v_mov_b32_e32 v117, v34
	v_mov_b32_e32 v122, v34
	v_mov_b32_e32 v123, v34
	v_mov_b32_e32 v124, v34
	v_mov_b32_e32 v125, v34
	v_mov_b32_e32 v130, v34
	v_mov_b32_e32 v131, v34
	v_mov_b32_e32 v132, v34
	v_mov_b32_e32 v133, v34
	v_mov_b32_e32 v138, v34
	v_mov_b32_e32 v139, v34
	v_mov_b32_e32 v140, v34
	v_mov_b32_e32 v141, v34
	v_mov_b32_e32 v146, v34
	v_mov_b32_e32 v147, v34
	v_mov_b32_e32 v148, v34
	v_mov_b32_e32 v149, v34
	v_mov_b32_e32 v154, v34
	v_mov_b32_e32 v155, v34
	v_mov_b32_e32 v156, v34
	v_mov_b32_e32 v157, v34
	v_mov_b32_e32 v158, v34
	v_mov_b32_e32 v159, v34
	v_mov_b32_e32 v160, v34
	v_mov_b32_e32 v161, v34
	v_readfirstlane_b32 s98, v0
	s_lshr_b32 s98, s98, 8
	s_cmp_eq_u32 s98, 1
	s_cbranch_scc0 .Lprio_skip4
	s_setprio 1
.Lprio_skip4:
.LBB0_985:
	ds_read_b128 v[26:29], v185
	ds_read_b128 v[30:33], v185 offset:1024
	ds_read_b128 v[18:21], v185 offset:2048
	ds_read_b128 v[22:25], v185 offset:3072
	ds_read_b128 v[10:13], v186
	ds_read_b128 v[14:17], v186 offset:1024
	ds_read_b128 v[2:5], v186 offset:2048
	ds_read_b128 v[6:9], v186 offset:3072
	s_add_u32 s26, s56, 0xfffc0080
	s_addc_u32 s27, s57, -1
	s_cmp_eq_u32 s80, 12
	s_cselect_b32 s59, s45, s27
	s_cselect_b32 s58, s72, s26
	s_cselect_b32 s61, s41, s75
	s_cselect_b32 s60, s73, s74
	v_lshl_add_u64 v[176:177], s[56:57], 0, v[168:169]
	s_add_i32 m0, s55, 0xc000
	ds_read_b128 v[192:195], v187
	ds_read_b128 v[196:199], v187 offset:1024
	ds_read_b128 v[200:203], v187 offset:2048
	ds_read_b128 v[204:207], v187 offset:3072
	ds_read_b128 v[208:211], v187 offset:4096
	ds_read_b128 v[212:215], v187 offset:5120
	ds_read_b128 v[220:223], v187 offset:6144
	ds_read_b128 v[224:227], v187 offset:7168
	global_load_lds_dwordx4 v[176:177], off
	v_lshl_add_u64 v[176:177], s[56:57], 0, v[170:171]
	s_add_i32 m0, s55, 0xe000
	s_nop 0
	global_load_lds_dwordx4 v[176:177], off
	s_waitcnt vmcnt(8)
	s_waitcnt lgkmcnt(0)
	s_barrier
	s_waitcnt lgkmcnt(0)
	v_mfma_scale_f32_16x16x128_f8f6f4 v[158:161], v[26:33], v[192:199], v[158:161], v188, v189 op_sel_hi:[0,0,0]
	v_mfma_scale_f32_16x16x128_f8f6f4 v[154:157], v[18:25], v[192:199], v[154:157], v188, v189 op_sel_hi:[0,0,0]
	v_mfma_scale_f32_16x16x128_f8f6f4 v[146:149], v[26:33], v[200:207], v[146:149], v188, v189 op_sel_hi:[0,0,0]
	v_mfma_scale_f32_16x16x128_f8f6f4 v[138:141], v[18:25], v[200:207], v[138:141], v188, v189 op_sel_hi:[0,0,0]
	v_mfma_scale_f32_16x16x128_f8f6f4 v[130:133], v[26:33], v[208:215], v[130:133], v188, v189 op_sel_hi:[0,0,0]
	v_mfma_scale_f32_16x16x128_f8f6f4 v[122:125], v[18:25], v[208:215], v[122:125], v188, v189 op_sel_hi:[0,0,0]
	v_mfma_scale_f32_16x16x128_f8f6f4 v[114:117], v[26:33], v[220:227], v[114:117], v188, v189 op_sel_hi:[0,0,0]
	v_mfma_scale_f32_16x16x128_f8f6f4 v[106:109], v[18:25], v[220:227], v[106:109], v188, v189 op_sel_hi:[0,0,0]
	v_mfma_scale_f32_16x16x128_f8f6f4 v[150:153], v[10:17], v[192:199], v[150:153], v188, v189 op_sel_hi:[0,0,0]
	v_mfma_scale_f32_16x16x128_f8f6f4 v[142:145], v[2:9], v[192:199], v[142:145], v188, v189 op_sel_hi:[0,0,0]
	v_mfma_scale_f32_16x16x128_f8f6f4 v[134:137], v[10:17], v[200:207], v[134:137], v188, v189 op_sel_hi:[0,0,0]
	v_mfma_scale_f32_16x16x128_f8f6f4 v[126:129], v[2:9], v[200:207], v[126:129], v188, v189 op_sel_hi:[0,0,0]
	v_mfma_scale_f32_16x16x128_f8f6f4 v[118:121], v[10:17], v[208:215], v[118:121], v188, v189 op_sel_hi:[0,0,0]
	v_mfma_scale_f32_16x16x128_f8f6f4 v[110:113], v[2:9], v[208:215], v[110:113], v188, v189 op_sel_hi:[0,0,0]
	v_mfma_scale_f32_16x16x128_f8f6f4 v[102:105], v[10:17], v[220:227], v[102:105], v188, v189 op_sel_hi:[0,0,0]
	v_mfma_scale_f32_16x16x128_f8f6f4 v[98:101], v[2:9], v[220:227], v[98:101], v188, v189 op_sel_hi:[0,0,0]
	s_barrier
	s_add_i32 s26, s70, s35
	v_lshl_add_u64 v[176:177], s[60:61], 0, v[162:163]
	s_mov_b32 m0, s26
	ds_read_b128 v[192:195], v187 offset:16384
	ds_read_b128 v[196:199], v187 offset:17408
	ds_read_b128 v[200:203], v187 offset:18432
	ds_read_b128 v[204:207], v187 offset:19456
	ds_read_b128 v[208:211], v187 offset:20480
	ds_read_b128 v[212:215], v187 offset:21504
	ds_read_b128 v[220:223], v187 offset:22528
	ds_read_b128 v[224:227], v187 offset:23552
	global_load_lds_dwordx4 v[176:177], off
	v_lshl_add_u64 v[178:179], v[176:177], 0, s[6:7]
	s_add_i32 m0, s26, 0x2000
	s_add_i32 s26, s71, s35
	global_load_lds_dwordx4 v[178:179], off
	v_lshl_add_u64 v[178:179], v[176:177], 0, s[8:9]
	s_mov_b32 m0, s26
	v_lshl_add_u64 v[180:181], s[58:59], 0, v[166:167]
	global_load_lds_dwordx4 v[178:179], off
	v_lshl_add_u64 v[178:179], v[176:177], 0, s[10:11]
	s_add_i32 m0, s26, 0x2000
	s_nop 0
	global_load_lds_dwordx4 v[178:179], off
	v_lshl_add_u64 v[178:179], s[58:59], 0, v[164:165]
	s_mov_b32 m0, s55
	s_nop 0
	global_load_lds_dwordx4 v[178:179], off
	s_mov_b32 m0, s63
	s_nop 0
	global_load_lds_dwordx4 v[180:181], off
	s_waitcnt vmcnt(8)
	s_waitcnt lgkmcnt(0)
	s_barrier
	s_waitcnt lgkmcnt(0)
	v_mfma_scale_f32_16x16x128_f8f6f4 v[94:97], v[26:33], v[192:199], v[94:97], v188, v189 op_sel_hi:[0,0,0]
	v_mfma_scale_f32_16x16x128_f8f6f4 v[90:93], v[18:25], v[192:199], v[90:93], v188, v189 op_sel_hi:[0,0,0]
	v_mfma_scale_f32_16x16x128_f8f6f4 v[82:85], v[26:33], v[200:207], v[82:85], v188, v189 op_sel_hi:[0,0,0]
	v_mfma_scale_f32_16x16x128_f8f6f4 v[74:77], v[18:25], v[200:207], v[74:77], v188, v189 op_sel_hi:[0,0,0]
	v_mfma_scale_f32_16x16x128_f8f6f4 v[66:69], v[26:33], v[208:215], v[66:69], v188, v189 op_sel_hi:[0,0,0]
	v_mfma_scale_f32_16x16x128_f8f6f4 v[58:61], v[18:25], v[208:215], v[58:61], v188, v189 op_sel_hi:[0,0,0]
	v_mfma_scale_f32_16x16x128_f8f6f4 v[50:53], v[26:33], v[220:227], v[50:53], v188, v189 op_sel_hi:[0,0,0]
	v_mfma_scale_f32_16x16x128_f8f6f4 v[42:45], v[18:25], v[220:227], v[42:45], v188, v189 op_sel_hi:[0,0,0]
	v_mfma_scale_f32_16x16x128_f8f6f4 v[86:89], v[10:17], v[192:199], v[86:89], v188, v189 op_sel_hi:[0,0,0]
	v_mfma_scale_f32_16x16x128_f8f6f4 v[78:81], v[2:9], v[192:199], v[78:81], v188, v189 op_sel_hi:[0,0,0]
	v_mfma_scale_f32_16x16x128_f8f6f4 v[70:73], v[10:17], v[200:207], v[70:73], v188, v189 op_sel_hi:[0,0,0]
	v_mfma_scale_f32_16x16x128_f8f6f4 v[62:65], v[2:9], v[200:207], v[62:65], v188, v189 op_sel_hi:[0,0,0]
	v_mfma_scale_f32_16x16x128_f8f6f4 v[54:57], v[10:17], v[208:215], v[54:57], v188, v189 op_sel_hi:[0,0,0]
	v_mfma_scale_f32_16x16x128_f8f6f4 v[46:49], v[2:9], v[208:215], v[46:49], v188, v189 op_sel_hi:[0,0,0]
	v_mfma_scale_f32_16x16x128_f8f6f4 v[38:41], v[10:17], v[220:227], v[38:41], v188, v189 op_sel_hi:[0,0,0]
	v_mfma_scale_f32_16x16x128_f8f6f4 v[34:37], v[2:9], v[220:227], v[34:37], v188, v189 op_sel_hi:[0,0,0]
	s_barrier
	s_add_i32 s60, 0, 0x18000
	s_add_i32 s61, 0, 0x1c000
	v_add_u32_e32 v14, s60, v183
	v_add_u32_e32 v30, s61, v183
	ds_read_b128 v[2:5], v14
	ds_read_b128 v[6:9], v14 offset:1024
	ds_read_b128 v[10:13], v14 offset:2048
	ds_read_b128 v[14:17], v14 offset:3072
	ds_read_b128 v[18:21], v30
	ds_read_b128 v[22:25], v30 offset:1024
	ds_read_b128 v[26:29], v30 offset:2048
	ds_read_b128 v[30:33], v30 offset:3072
	s_add_u32 s26, s58, 0x40000
	s_addc_u32 s27, s59, 0
	s_mov_b32 m0, s64
	v_lshl_add_u64 v[216:217], s[26:27], 0, v[164:165]
	ds_read_b128 v[192:195], v187 offset:32768
	ds_read_b128 v[196:199], v187 offset:33792
	ds_read_b128 v[200:203], v187 offset:34816
	ds_read_b128 v[204:207], v187 offset:35840
	ds_read_b128 v[208:211], v187 offset:36864
	ds_read_b128 v[212:215], v187 offset:37888
	ds_read_b128 v[220:223], v187 offset:38912
	ds_read_b128 v[224:227], v187 offset:39936
	global_load_lds_dwordx4 v[216:217], off
	v_lshl_add_u64 v[216:217], s[26:27], 0, v[166:167]
	s_mov_b32 m0, s65
	s_nop 0
	global_load_lds_dwordx4 v[216:217], off
	s_waitcnt vmcnt(8)
	s_waitcnt lgkmcnt(0)
	s_barrier
	s_waitcnt lgkmcnt(0)
	v_mfma_scale_f32_16x16x128_f8f6f4 v[158:161], v[2:9], v[192:199], v[158:161], v188, v189 op_sel_hi:[0,0,0]
	v_mfma_scale_f32_16x16x128_f8f6f4 v[154:157], v[10:17], v[192:199], v[154:157], v188, v189 op_sel_hi:[0,0,0]
	v_mfma_scale_f32_16x16x128_f8f6f4 v[146:149], v[2:9], v[200:207], v[146:149], v188, v189 op_sel_hi:[0,0,0]
	v_mfma_scale_f32_16x16x128_f8f6f4 v[138:141], v[10:17], v[200:207], v[138:141], v188, v189 op_sel_hi:[0,0,0]
	v_mfma_scale_f32_16x16x128_f8f6f4 v[130:133], v[2:9], v[208:215], v[130:133], v188, v189 op_sel_hi:[0,0,0]
	v_mfma_scale_f32_16x16x128_f8f6f4 v[122:125], v[10:17], v[208:215], v[122:125], v188, v189 op_sel_hi:[0,0,0]
	v_mfma_scale_f32_16x16x128_f8f6f4 v[114:117], v[2:9], v[220:227], v[114:117], v188, v189 op_sel_hi:[0,0,0]
	v_mfma_scale_f32_16x16x128_f8f6f4 v[106:109], v[10:17], v[220:227], v[106:109], v188, v189 op_sel_hi:[0,0,0]
	v_mfma_scale_f32_16x16x128_f8f6f4 v[150:153], v[18:25], v[192:199], v[150:153], v188, v189 op_sel_hi:[0,0,0]
	v_mfma_scale_f32_16x16x128_f8f6f4 v[142:145], v[26:33], v[192:199], v[142:145], v188, v189 op_sel_hi:[0,0,0]
	v_mfma_scale_f32_16x16x128_f8f6f4 v[134:137], v[18:25], v[200:207], v[134:137], v188, v189 op_sel_hi:[0,0,0]
	v_mfma_scale_f32_16x16x128_f8f6f4 v[126:129], v[26:33], v[200:207], v[126:129], v188, v189 op_sel_hi:[0,0,0]
	v_mfma_scale_f32_16x16x128_f8f6f4 v[118:121], v[18:25], v[208:215], v[118:121], v188, v189 op_sel_hi:[0,0,0]
	v_mfma_scale_f32_16x16x128_f8f6f4 v[110:113], v[26:33], v[208:215], v[110:113], v188, v189 op_sel_hi:[0,0,0]
	v_mfma_scale_f32_16x16x128_f8f6f4 v[102:105], v[18:25], v[220:227], v[102:105], v188, v189 op_sel_hi:[0,0,0]
	v_mfma_scale_f32_16x16x128_f8f6f4 v[98:101], v[26:33], v[220:227], v[98:101], v188, v189 op_sel_hi:[0,0,0]
	s_barrier
	s_add_i32 s26, s60, s35
	v_lshl_add_u64 v[216:217], v[176:177], 0, s[14:15]
	s_mov_b32 m0, s26
	ds_read_b128 v[192:195], v187 offset:49152
	ds_read_b128 v[196:199], v187 offset:50176
	ds_read_b128 v[200:203], v187 offset:51200
	ds_read_b128 v[204:207], v187 offset:52224
	ds_read_b128 v[208:211], v187 offset:53248
	ds_read_b128 v[212:215], v187 offset:54272
	ds_read_b128 v[220:223], v187 offset:55296
	ds_read_b128 v[224:227], v187 offset:56320
	global_load_lds_dwordx4 v[216:217], off
	v_lshl_add_u64 v[216:217], v[176:177], 0, s[16:17]
	s_add_i32 m0, s26, 0x2000
	s_add_i32 s26, s61, s35
	global_load_lds_dwordx4 v[216:217], off
	v_lshl_add_u64 v[216:217], v[176:177], 0, s[20:21]
	s_mov_b32 m0, s26
	v_lshl_add_u64 v[176:177], v[176:177], 0, s[22:23]
	global_load_lds_dwordx4 v[216:217], off
	s_add_i32 m0, s26, 0x2000
	s_nop 0
	global_load_lds_dwordx4 v[176:177], off
	v_lshl_add_u64 v[176:177], v[178:179], 0, s[18:19]
	s_mov_b32 m0, s67
	s_nop 0
	global_load_lds_dwordx4 v[176:177], off
	v_lshl_add_u64 v[176:177], v[180:181], 0, s[18:19]
	s_mov_b32 m0, s68
	s_nop 0
	global_load_lds_dwordx4 v[176:177], off
	s_waitcnt vmcnt(8)
	s_waitcnt lgkmcnt(0)
	s_barrier
	s_waitcnt lgkmcnt(0)
	v_mfma_scale_f32_16x16x128_f8f6f4 v[94:97], v[2:9], v[192:199], v[94:97], v188, v189 op_sel_hi:[0,0,0]
	v_mfma_scale_f32_16x16x128_f8f6f4 v[90:93], v[10:17], v[192:199], v[90:93], v188, v189 op_sel_hi:[0,0,0]
	v_mfma_scale_f32_16x16x128_f8f6f4 v[82:85], v[2:9], v[200:207], v[82:85], v188, v189 op_sel_hi:[0,0,0]
	v_mfma_scale_f32_16x16x128_f8f6f4 v[74:77], v[10:17], v[200:207], v[74:77], v188, v189 op_sel_hi:[0,0,0]
	v_mfma_scale_f32_16x16x128_f8f6f4 v[66:69], v[2:9], v[208:215], v[66:69], v188, v189 op_sel_hi:[0,0,0]
	v_mfma_scale_f32_16x16x128_f8f6f4 v[58:61], v[10:17], v[208:215], v[58:61], v188, v189 op_sel_hi:[0,0,0]
	v_mfma_scale_f32_16x16x128_f8f6f4 v[50:53], v[2:9], v[220:227], v[50:53], v188, v189 op_sel_hi:[0,0,0]
	v_mfma_scale_f32_16x16x128_f8f6f4 v[42:45], v[10:17], v[220:227], v[42:45], v188, v189 op_sel_hi:[0,0,0]
	v_mfma_scale_f32_16x16x128_f8f6f4 v[86:89], v[18:25], v[192:199], v[86:89], v188, v189 op_sel_hi:[0,0,0]
	v_mfma_scale_f32_16x16x128_f8f6f4 v[78:81], v[26:33], v[192:199], v[78:81], v188, v189 op_sel_hi:[0,0,0]
	v_mfma_scale_f32_16x16x128_f8f6f4 v[70:73], v[18:25], v[200:207], v[70:73], v188, v189 op_sel_hi:[0,0,0]
	v_mfma_scale_f32_16x16x128_f8f6f4 v[62:65], v[26:33], v[200:207], v[62:65], v188, v189 op_sel_hi:[0,0,0]
	v_mfma_scale_f32_16x16x128_f8f6f4 v[54:57], v[18:25], v[208:215], v[54:57], v188, v189 op_sel_hi:[0,0,0]
	v_mfma_scale_f32_16x16x128_f8f6f4 v[46:49], v[26:33], v[208:215], v[46:49], v188, v189 op_sel_hi:[0,0,0]
	v_mfma_scale_f32_16x16x128_f8f6f4 v[38:41], v[18:25], v[220:227], v[38:41], v188, v189 op_sel_hi:[0,0,0]
	v_mfma_scale_f32_16x16x128_f8f6f4 v[34:37], v[26:33], v[220:227], v[34:37], v188, v189 op_sel_hi:[0,0,0]
	s_barrier
	s_add_i32 s80, s80, 2
	s_add_u32 s74, s74, 0x10000
	s_addc_u32 s75, s75, 0
	s_add_u32 s56, s56, 0x100
	s_addc_u32 s57, s57, 0
	s_cmp_gt_u32 s80, 13
	s_cbranch_scc0 .LBB0_985
	s_setprio 0
	s_and_b64 vcc, exec, s[24:25]
	s_cbranch_vccz .LBB0_988
	s_barrier

.LBB0_1191:
	s_ashr_i32 s45, s44, 31
	s_lshl_b64 s[26:27], s[44:45], 19
	s_add_u32 s50, s4, s26
	s_addc_u32 s51, s5, s27
	s_and_b64 s[26:27], s[0:1], exec
	s_cselect_b32 s45, s51, s59
	s_cselect_b32 s69, s50, s58
	s_ashr_i32 s41, s40, 31
	s_lshl_b64 s[26:27], s[40:41], 19
	s_add_u32 s52, s3, s26
	s_addc_u32 s53, s33, s27
	s_and_b64 s[26:27], s[0:1], exec
	s_cselect_b32 s41, s53, s57
	s_cselect_b32 s70, s52, s56
	s_add_u32 s71, s56, 0x10000
	s_addc_u32 s72, s57, 0
	s_add_u32 s56, s58, 0x40080
	v_mov_b32_e32 v2, 0
	s_addc_u32 s57, s59, 0
	s_mov_b32 s73, -2
	v_mov_b32_e32 v3, v2
	v_mov_b32_e32 v4, v2
	v_mov_b32_e32 v5, v2
	v_mov_b32_e32 v6, v2
	v_mov_b32_e32 v7, v2
	v_mov_b32_e32 v8, v2
	v_mov_b32_e32 v9, v2
	v_mov_b32_e32 v18, v2
	v_mov_b32_e32 v19, v2
	v_mov_b32_e32 v20, v2
	v_mov_b32_e32 v21, v2
	v_mov_b32_e32 v22, v2
	v_mov_b32_e32 v23, v2
	v_mov_b32_e32 v24, v2
	v_mov_b32_e32 v25, v2
	v_mov_b32_e32 v34, v2
	v_mov_b32_e32 v35, v2
	v_mov_b32_e32 v36, v2
	v_mov_b32_e32 v37, v2
	v_mov_b32_e32 v38, v2
	v_mov_b32_e32 v39, v2
	v_mov_b32_e32 v40, v2
	v_mov_b32_e32 v41, v2
	v_mov_b32_e32 v50, v2
	v_mov_b32_e32 v51, v2
	v_mov_b32_e32 v52, v2
	v_mov_b32_e32 v53, v2
	v_mov_b32_e32 v54, v2
	v_mov_b32_e32 v55, v2
	v_mov_b32_e32 v56, v2
	v_mov_b32_e32 v57, v2
	v_mov_b32_e32 v10, v2
	v_mov_b32_e32 v11, v2
	v_mov_b32_e32 v12, v2
	v_mov_b32_e32 v13, v2
	v_mov_b32_e32 v14, v2
	v_mov_b32_e32 v15, v2
	v_mov_b32_e32 v16, v2
	v_mov_b32_e32 v17, v2
	v_mov_b32_e32 v26, v2
	v_mov_b32_e32 v27, v2
	v_mov_b32_e32 v28, v2
	v_mov_b32_e32 v29, v2
	v_mov_b32_e32 v30, v2
	v_mov_b32_e32 v31, v2
	v_mov_b32_e32 v32, v2
	v_mov_b32_e32 v33, v2
	v_mov_b32_e32 v42, v2
	v_mov_b32_e32 v43, v2
	v_mov_b32_e32 v44, v2
	v_mov_b32_e32 v45, v2
	v_mov_b32_e32 v46, v2
	v_mov_b32_e32 v47, v2
	v_mov_b32_e32 v48, v2
	v_mov_b32_e32 v49, v2
	v_mov_b32_e32 v58, v2
	v_mov_b32_e32 v59, v2
	v_mov_b32_e32 v60, v2
	v_mov_b32_e32 v61, v2
	v_mov_b32_e32 v62, v2
	v_mov_b32_e32 v63, v2
	v_mov_b32_e32 v64, v2
	v_mov_b32_e32 v65, v2
	v_mov_b32_e32 v74, v2
	v_mov_b32_e32 v75, v2
	v_mov_b32_e32 v76, v2
	v_mov_b32_e32 v77, v2
	v_mov_b32_e32 v78, v2
	v_mov_b32_e32 v79, v2
	v_mov_b32_e32 v80, v2
	v_mov_b32_e32 v81, v2
	v_mov_b32_e32 v98, v2
	v_mov_b32_e32 v99, v2
	v_mov_b32_e32 v100, v2
	v_mov_b32_e32 v101, v2
	v_mov_b32_e32 v102, v2
	v_mov_b32_e32 v103, v2
	v_mov_b32_e32 v104, v2
	v_mov_b32_e32 v105, v2
	v_mov_b32_e32 v114, v2
	v_mov_b32_e32 v115, v2
	v_mov_b32_e32 v116, v2
	v_mov_b32_e32 v117, v2
	v_mov_b32_e32 v118, v2
	v_mov_b32_e32 v119, v2
	v_mov_b32_e32 v120, v2
	v_mov_b32_e32 v121, v2
	v_mov_b32_e32 v130, v2
	v_mov_b32_e32 v131, v2
	v_mov_b32_e32 v132, v2
	v_mov_b32_e32 v133, v2
	v_mov_b32_e32 v134, v2
	v_mov_b32_e32 v135, v2
	v_mov_b32_e32 v136, v2
	v_mov_b32_e32 v137, v2
	v_mov_b32_e32 v90, v2
	v_mov_b32_e32 v91, v2
	v_mov_b32_e32 v92, v2
	v_mov_b32_e32 v93, v2
	v_mov_b32_e32 v94, v2
	v_mov_b32_e32 v95, v2
	v_mov_b32_e32 v96, v2
	v_mov_b32_e32 v97, v2
	v_mov_b32_e32 v106, v2
	v_mov_b32_e32 v107, v2
	v_mov_b32_e32 v108, v2
	v_mov_b32_e32 v109, v2
	v_mov_b32_e32 v110, v2
	v_mov_b32_e32 v111, v2
	v_mov_b32_e32 v112, v2
	v_mov_b32_e32 v113, v2
	v_mov_b32_e32 v122, v2
	v_mov_b32_e32 v123, v2
	v_mov_b32_e32 v124, v2
	v_mov_b32_e32 v125, v2
	v_mov_b32_e32 v126, v2
	v_mov_b32_e32 v127, v2
	v_mov_b32_e32 v128, v2
	v_mov_b32_e32 v129, v2
	v_mov_b32_e32 v138, v2
	v_mov_b32_e32 v139, v2
	v_mov_b32_e32 v140, v2
	v_mov_b32_e32 v141, v2
	v_mov_b32_e32 v142, v2
	v_mov_b32_e32 v143, v2
	v_mov_b32_e32 v144, v2
	v_mov_b32_e32 v145, v2
	v_readfirstlane_b32 s98, v0
	s_lshr_b32 s98, s98, 8
	s_cmp_eq_u32 s98, 1
	s_cbranch_scc0 .Lprio_skip3
	s_setprio 1
.Lprio_skip3:
.LBB0_1192:
	ds_read_b128 v[66:69], v199
	ds_read_b128 v[70:73], v199 offset:1024
	ds_read_b128 v[82:85], v199 offset:2048
	ds_read_b128 v[86:89], v199 offset:3072
	ds_read_b128 v[146:149], v200
	ds_read_b128 v[150:153], v200 offset:1024
	ds_read_b128 v[154:157], v200 offset:2048
	ds_read_b128 v[158:161], v200 offset:3072
	s_add_u32 s26, s56, 0xfffc0080
	s_addc_u32 s27, s57, -1
	s_cmp_eq_u32 s73, 12
	s_cselect_b32 s59, s45, s27
	s_cselect_b32 s58, s69, s26
	s_cselect_b32 s27, s41, s72
	s_cselect_b32 s26, s70, s71
	v_lshl_add_u64 v[214:215], s[56:57], 0, v[176:177]
	s_add_i32 m0, s55, 0xc000
	ds_read_b128 v[162:165], v201
	ds_read_b128 v[166:169], v201 offset:1024
	ds_read_b128 v[184:187], v201 offset:2048
	ds_read_b128 v[188:191], v201 offset:3072
	ds_read_b128 v[192:195], v201 offset:4096
	ds_read_b128 v[202:205], v201 offset:5120
	ds_read_b128 v[206:209], v201 offset:6144
	ds_read_b128 v[210:213], v201 offset:7168
	global_load_lds_dwordx4 v[214:215], off
	v_lshl_add_u64 v[214:215], s[56:57], 0, v[178:179]
	s_add_i32 m0, s55, 0xe000
	s_nop 0
	global_load_lds_dwordx4 v[214:215], off
	s_waitcnt vmcnt(8)
	s_waitcnt lgkmcnt(0)
	s_barrier
	s_waitcnt lgkmcnt(0)
	v_mfma_f32_16x16x32_bf16 v[142:145], v[66:69], v[162:165], v[142:145]
	v_mfma_f32_16x16x32_bf16 v[138:141], v[82:85], v[162:165], v[138:141]
	v_mfma_f32_16x16x32_bf16 v[126:129], v[66:69], v[184:187], v[126:129]
	v_mfma_f32_16x16x32_bf16 v[122:125], v[82:85], v[184:187], v[122:125]
	v_mfma_f32_16x16x32_bf16 v[110:113], v[66:69], v[192:195], v[110:113]
	v_mfma_f32_16x16x32_bf16 v[106:109], v[82:85], v[192:195], v[106:109]
	v_mfma_f32_16x16x32_bf16 v[94:97], v[66:69], v[206:209], v[94:97]
	v_mfma_f32_16x16x32_bf16 v[90:93], v[82:85], v[206:209], v[90:93]
	v_mfma_f32_16x16x32_bf16 v[142:145], v[70:73], v[166:169], v[142:145]
	v_mfma_f32_16x16x32_bf16 v[138:141], v[86:89], v[166:169], v[138:141]
	v_mfma_f32_16x16x32_bf16 v[126:129], v[70:73], v[188:191], v[126:129]
	v_mfma_f32_16x16x32_bf16 v[122:125], v[86:89], v[188:191], v[122:125]
	v_mfma_f32_16x16x32_bf16 v[110:113], v[70:73], v[202:205], v[110:113]
	v_mfma_f32_16x16x32_bf16 v[106:109], v[86:89], v[202:205], v[106:109]
	v_mfma_f32_16x16x32_bf16 v[94:97], v[70:73], v[210:213], v[94:97]
	v_mfma_f32_16x16x32_bf16 v[90:93], v[86:89], v[210:213], v[90:93]
	v_mfma_f32_16x16x32_bf16 v[134:137], v[146:149], v[162:165], v[134:137]
	v_mfma_f32_16x16x32_bf16 v[130:133], v[154:157], v[162:165], v[130:133]
	v_mfma_f32_16x16x32_bf16 v[118:121], v[146:149], v[184:187], v[118:121]
	v_mfma_f32_16x16x32_bf16 v[114:117], v[154:157], v[184:187], v[114:117]
	v_mfma_f32_16x16x32_bf16 v[102:105], v[146:149], v[192:195], v[102:105]
	v_mfma_f32_16x16x32_bf16 v[98:101], v[154:157], v[192:195], v[98:101]
	v_mfma_f32_16x16x32_bf16 v[78:81], v[146:149], v[206:209], v[78:81]
	v_mfma_f32_16x16x32_bf16 v[74:77], v[154:157], v[206:209], v[74:77]
	v_mfma_f32_16x16x32_bf16 v[134:137], v[150:153], v[166:169], v[134:137]
	v_mfma_f32_16x16x32_bf16 v[130:133], v[158:161], v[166:169], v[130:133]
	v_mfma_f32_16x16x32_bf16 v[118:121], v[150:153], v[188:191], v[118:121]
	v_mfma_f32_16x16x32_bf16 v[114:117], v[158:161], v[188:191], v[114:117]
	v_mfma_f32_16x16x32_bf16 v[102:105], v[150:153], v[202:205], v[102:105]
	v_mfma_f32_16x16x32_bf16 v[98:101], v[158:161], v[202:205], v[98:101]
	v_mfma_f32_16x16x32_bf16 v[78:81], v[150:153], v[210:213], v[78:81]
	v_mfma_f32_16x16x32_bf16 v[74:77], v[158:161], v[210:213], v[74:77]
	s_barrier
	v_lshl_add_u64 v[214:215], s[26:27], 0, v[170:171]
	s_add_i32 s26, s67, s35
	s_mov_b32 m0, s26
	ds_read_b128 v[162:165], v201 offset:16384
	ds_read_b128 v[166:169], v201 offset:17408
	ds_read_b128 v[184:187], v201 offset:18432
	ds_read_b128 v[188:191], v201 offset:19456
	ds_read_b128 v[192:195], v201 offset:20480
	ds_read_b128 v[202:205], v201 offset:21504
	ds_read_b128 v[206:209], v201 offset:22528
	ds_read_b128 v[210:213], v201 offset:23552
	global_load_lds_dwordx4 v[214:215], off
	v_lshl_add_u64 v[216:217], v[214:215], 0, s[6:7]
	s_add_i32 m0, s26, 0x2000
	s_add_i32 s26, s68, s35
	global_load_lds_dwordx4 v[216:217], off
	v_lshl_add_u64 v[216:217], v[214:215], 0, s[10:11]
	s_mov_b32 m0, s26
	v_lshl_add_u64 v[220:221], s[58:59], 0, v[174:175]
	global_load_lds_dwordx4 v[216:217], off
	v_lshl_add_u64 v[216:217], v[214:215], 0, s[12:13]
	s_add_i32 m0, s26, 0x2000
	s_nop 0
	global_load_lds_dwordx4 v[216:217], off
	v_lshl_add_u64 v[216:217], s[58:59], 0, v[172:173]
	s_mov_b32 m0, s55
	s_nop 0
	global_load_lds_dwordx4 v[216:217], off
	s_mov_b32 m0, s60
	s_nop 0
	global_load_lds_dwordx4 v[220:221], off
	s_waitcnt vmcnt(8)
	s_waitcnt lgkmcnt(0)
	s_barrier
	s_waitcnt lgkmcnt(0)
	v_mfma_f32_16x16x32_bf16 v[62:65], v[66:69], v[162:165], v[62:65]
	v_mfma_f32_16x16x32_bf16 v[58:61], v[82:85], v[162:165], v[58:61]
	v_mfma_f32_16x16x32_bf16 v[46:49], v[66:69], v[184:187], v[46:49]
	v_mfma_f32_16x16x32_bf16 v[42:45], v[82:85], v[184:187], v[42:45]
	v_mfma_f32_16x16x32_bf16 v[30:33], v[66:69], v[192:195], v[30:33]
	v_mfma_f32_16x16x32_bf16 v[26:29], v[82:85], v[192:195], v[26:29]
	v_mfma_f32_16x16x32_bf16 v[14:17], v[66:69], v[206:209], v[14:17]
	v_mfma_f32_16x16x32_bf16 v[10:13], v[82:85], v[206:209], v[10:13]
	v_mfma_f32_16x16x32_bf16 v[62:65], v[70:73], v[166:169], v[62:65]
	v_mfma_f32_16x16x32_bf16 v[58:61], v[86:89], v[166:169], v[58:61]
	v_mfma_f32_16x16x32_bf16 v[46:49], v[70:73], v[188:191], v[46:49]
	v_mfma_f32_16x16x32_bf16 v[42:45], v[86:89], v[188:191], v[42:45]
	v_mfma_f32_16x16x32_bf16 v[30:33], v[70:73], v[202:205], v[30:33]
	v_mfma_f32_16x16x32_bf16 v[26:29], v[86:89], v[202:205], v[26:29]
	v_mfma_f32_16x16x32_bf16 v[14:17], v[70:73], v[210:213], v[14:17]
	v_mfma_f32_16x16x32_bf16 v[10:13], v[86:89], v[210:213], v[10:13]
	v_mfma_f32_16x16x32_bf16 v[54:57], v[146:149], v[162:165], v[54:57]
	v_mfma_f32_16x16x32_bf16 v[50:53], v[154:157], v[162:165], v[50:53]
	v_mfma_f32_16x16x32_bf16 v[38:41], v[146:149], v[184:187], v[38:41]
	v_mfma_f32_16x16x32_bf16 v[34:37], v[154:157], v[184:187], v[34:37]
	v_mfma_f32_16x16x32_bf16 v[22:25], v[146:149], v[192:195], v[22:25]
	v_mfma_f32_16x16x32_bf16 v[18:21], v[154:157], v[192:195], v[18:21]
	v_mfma_f32_16x16x32_bf16 v[6:9], v[146:149], v[206:209], v[6:9]
	v_mfma_f32_16x16x32_bf16 v[2:5], v[154:157], v[206:209], v[2:5]
	v_mfma_f32_16x16x32_bf16 v[54:57], v[150:153], v[166:169], v[54:57]
	v_mfma_f32_16x16x32_bf16 v[50:53], v[158:161], v[166:169], v[50:53]
	v_mfma_f32_16x16x32_bf16 v[38:41], v[150:153], v[188:191], v[38:41]
	v_mfma_f32_16x16x32_bf16 v[34:37], v[158:161], v[188:191], v[34:37]
	v_mfma_f32_16x16x32_bf16 v[22:25], v[150:153], v[202:205], v[22:25]
	v_mfma_f32_16x16x32_bf16 v[18:21], v[158:161], v[202:205], v[18:21]
	v_mfma_f32_16x16x32_bf16 v[6:9], v[150:153], v[210:213], v[6:9]
	v_mfma_f32_16x16x32_bf16 v[2:5], v[158:161], v[210:213], v[2:5]
	s_barrier
	s_add_i32 s74, 0, 0x18000
	s_add_i32 s75, 0, 0x1c000
	v_add_u32_e32 v86, s74, v197
	v_add_u32_e32 v158, s75, v197
	ds_read_b128 v[66:69], v86
	ds_read_b128 v[70:73], v86 offset:1024
	ds_read_b128 v[82:85], v86 offset:2048
	ds_read_b128 v[86:89], v86 offset:3072
	ds_read_b128 v[146:149], v158
	ds_read_b128 v[150:153], v158 offset:1024
	ds_read_b128 v[154:157], v158 offset:2048
	ds_read_b128 v[158:161], v158 offset:3072
	s_add_u32 s26, s58, 0x40000
	s_addc_u32 s27, s59, 0
	s_mov_b32 m0, s61
	v_lshl_add_u64 v[222:223], s[26:27], 0, v[172:173]
	ds_read_b128 v[162:165], v201 offset:32768
	ds_read_b128 v[166:169], v201 offset:33792
	ds_read_b128 v[184:187], v201 offset:34816
	ds_read_b128 v[188:191], v201 offset:35840
	ds_read_b128 v[192:195], v201 offset:36864
	ds_read_b128 v[202:205], v201 offset:37888
	ds_read_b128 v[206:209], v201 offset:38912
	ds_read_b128 v[210:213], v201 offset:39936
	global_load_lds_dwordx4 v[222:223], off
	v_lshl_add_u64 v[222:223], s[26:27], 0, v[174:175]
	s_mov_b32 m0, s62
	s_nop 0
	global_load_lds_dwordx4 v[222:223], off
	s_waitcnt vmcnt(8)
	s_waitcnt lgkmcnt(0)
	s_barrier
	s_waitcnt lgkmcnt(0)
	v_mfma_f32_16x16x32_bf16 v[142:145], v[66:69], v[162:165], v[142:145]
	v_mfma_f32_16x16x32_bf16 v[138:141], v[82:85], v[162:165], v[138:141]
	v_mfma_f32_16x16x32_bf16 v[126:129], v[66:69], v[184:187], v[126:129]
	v_mfma_f32_16x16x32_bf16 v[122:125], v[82:85], v[184:187], v[122:125]
	v_mfma_f32_16x16x32_bf16 v[110:113], v[66:69], v[192:195], v[110:113]
	v_mfma_f32_16x16x32_bf16 v[106:109], v[82:85], v[192:195], v[106:109]
	v_mfma_f32_16x16x32_bf16 v[94:97], v[66:69], v[206:209], v[94:97]
	v_mfma_f32_16x16x32_bf16 v[90:93], v[82:85], v[206:209], v[90:93]
	v_mfma_f32_16x16x32_bf16 v[142:145], v[70:73], v[166:169], v[142:145]
	v_mfma_f32_16x16x32_bf16 v[138:141], v[86:89], v[166:169], v[138:141]
	v_mfma_f32_16x16x32_bf16 v[126:129], v[70:73], v[188:191], v[126:129]
	v_mfma_f32_16x16x32_bf16 v[122:125], v[86:89], v[188:191], v[122:125]
	v_mfma_f32_16x16x32_bf16 v[110:113], v[70:73], v[202:205], v[110:113]
	v_mfma_f32_16x16x32_bf16 v[106:109], v[86:89], v[202:205], v[106:109]
	v_mfma_f32_16x16x32_bf16 v[94:97], v[70:73], v[210:213], v[94:97]
	v_mfma_f32_16x16x32_bf16 v[90:93], v[86:89], v[210:213], v[90:93]
	v_mfma_f32_16x16x32_bf16 v[134:137], v[146:149], v[162:165], v[134:137]
	v_mfma_f32_16x16x32_bf16 v[130:133], v[154:157], v[162:165], v[130:133]
	v_mfma_f32_16x16x32_bf16 v[118:121], v[146:149], v[184:187], v[118:121]
	v_mfma_f32_16x16x32_bf16 v[114:117], v[154:157], v[184:187], v[114:117]
	v_mfma_f32_16x16x32_bf16 v[102:105], v[146:149], v[192:195], v[102:105]
	v_mfma_f32_16x16x32_bf16 v[98:101], v[154:157], v[192:195], v[98:101]
	v_mfma_f32_16x16x32_bf16 v[78:81], v[146:149], v[206:209], v[78:81]
	v_mfma_f32_16x16x32_bf16 v[74:77], v[154:157], v[206:209], v[74:77]
	v_mfma_f32_16x16x32_bf16 v[134:137], v[150:153], v[166:169], v[134:137]
	v_mfma_f32_16x16x32_bf16 v[130:133], v[158:161], v[166:169], v[130:133]
	v_mfma_f32_16x16x32_bf16 v[118:121], v[150:153], v[188:191], v[118:121]
	v_mfma_f32_16x16x32_bf16 v[114:117], v[158:161], v[188:191], v[114:117]
	v_mfma_f32_16x16x32_bf16 v[102:105], v[150:153], v[202:205], v[102:105]
	v_mfma_f32_16x16x32_bf16 v[98:101], v[158:161], v[202:205], v[98:101]
	v_mfma_f32_16x16x32_bf16 v[78:81], v[150:153], v[210:213], v[78:81]
	v_mfma_f32_16x16x32_bf16 v[74:77], v[158:161], v[210:213], v[74:77]
	s_barrier
	s_add_i32 s26, s74, s35
	v_lshl_add_u64 v[222:223], v[214:215], 0, s[16:17]
	s_mov_b32 m0, s26
	ds_read_b128 v[162:165], v201 offset:49152
	ds_read_b128 v[166:169], v201 offset:50176
	ds_read_b128 v[184:187], v201 offset:51200
	ds_read_b128 v[188:191], v201 offset:52224
	ds_read_b128 v[192:195], v201 offset:53248
	ds_read_b128 v[202:205], v201 offset:54272
	ds_read_b128 v[206:209], v201 offset:55296
	ds_read_b128 v[210:213], v201 offset:56320
	global_load_lds_dwordx4 v[222:223], off
	v_lshl_add_u64 v[222:223], v[214:215], 0, s[18:19]
	s_add_i32 m0, s26, 0x2000
	s_add_i32 s26, s75, s35
	global_load_lds_dwordx4 v[222:223], off
	v_lshl_add_u64 v[222:223], v[214:215], 0, s[22:23]
	s_mov_b32 m0, s26
	v_lshl_add_u64 v[214:215], v[214:215], 0, s[24:25]
	global_load_lds_dwordx4 v[222:223], off
	s_add_i32 m0, s26, 0x2000
	s_nop 0
	global_load_lds_dwordx4 v[214:215], off
	v_lshl_add_u64 v[214:215], v[216:217], 0, s[20:21]
	s_mov_b32 m0, s64
	s_nop 0
	global_load_lds_dwordx4 v[214:215], off
	v_lshl_add_u64 v[214:215], v[220:221], 0, s[20:21]
	s_mov_b32 m0, s65
	s_nop 0
	global_load_lds_dwordx4 v[214:215], off
	s_waitcnt vmcnt(8)
	s_waitcnt lgkmcnt(0)
	s_barrier
	s_waitcnt lgkmcnt(0)
	v_mfma_f32_16x16x32_bf16 v[62:65], v[66:69], v[162:165], v[62:65]
	v_mfma_f32_16x16x32_bf16 v[58:61], v[82:85], v[162:165], v[58:61]
	v_mfma_f32_16x16x32_bf16 v[46:49], v[66:69], v[184:187], v[46:49]
	v_mfma_f32_16x16x32_bf16 v[42:45], v[82:85], v[184:187], v[42:45]
	v_mfma_f32_16x16x32_bf16 v[30:33], v[66:69], v[192:195], v[30:33]
	v_mfma_f32_16x16x32_bf16 v[26:29], v[82:85], v[192:195], v[26:29]
	v_mfma_f32_16x16x32_bf16 v[14:17], v[66:69], v[206:209], v[14:17]
	v_mfma_f32_16x16x32_bf16 v[10:13], v[82:85], v[206:209], v[10:13]
	v_mfma_f32_16x16x32_bf16 v[62:65], v[70:73], v[166:169], v[62:65]
	v_mfma_f32_16x16x32_bf16 v[58:61], v[86:89], v[166:169], v[58:61]
	v_mfma_f32_16x16x32_bf16 v[46:49], v[70:73], v[188:191], v[46:49]
	v_mfma_f32_16x16x32_bf16 v[42:45], v[86:89], v[188:191], v[42:45]
	v_mfma_f32_16x16x32_bf16 v[30:33], v[70:73], v[202:205], v[30:33]
	v_mfma_f32_16x16x32_bf16 v[26:29], v[86:89], v[202:205], v[26:29]
	v_mfma_f32_16x16x32_bf16 v[14:17], v[70:73], v[210:213], v[14:17]
	v_mfma_f32_16x16x32_bf16 v[10:13], v[86:89], v[210:213], v[10:13]
	v_mfma_f32_16x16x32_bf16 v[54:57], v[146:149], v[162:165], v[54:57]
	v_mfma_f32_16x16x32_bf16 v[50:53], v[154:157], v[162:165], v[50:53]
	v_mfma_f32_16x16x32_bf16 v[38:41], v[146:149], v[184:187], v[38:41]
	v_mfma_f32_16x16x32_bf16 v[34:37], v[154:157], v[184:187], v[34:37]
	v_mfma_f32_16x16x32_bf16 v[22:25], v[146:149], v[192:195], v[22:25]
	v_mfma_f32_16x16x32_bf16 v[18:21], v[154:157], v[192:195], v[18:21]
	v_mfma_f32_16x16x32_bf16 v[6:9], v[146:149], v[206:209], v[6:9]
	v_mfma_f32_16x16x32_bf16 v[2:5], v[154:157], v[206:209], v[2:5]
	v_mfma_f32_16x16x32_bf16 v[54:57], v[150:153], v[166:169], v[54:57]
	v_mfma_f32_16x16x32_bf16 v[50:53], v[158:161], v[166:169], v[50:53]
	v_mfma_f32_16x16x32_bf16 v[38:41], v[150:153], v[188:191], v[38:41]
	v_mfma_f32_16x16x32_bf16 v[34:37], v[158:161], v[188:191], v[34:37]
	v_mfma_f32_16x16x32_bf16 v[22:25], v[150:153], v[202:205], v[22:25]
	v_mfma_f32_16x16x32_bf16 v[18:21], v[158:161], v[202:205], v[18:21]
	v_mfma_f32_16x16x32_bf16 v[6:9], v[150:153], v[210:213], v[6:9]
	v_mfma_f32_16x16x32_bf16 v[2:5], v[158:161], v[210:213], v[2:5]
	s_barrier
	s_add_i32 s73, s73, 2
	s_add_u32 s71, s71, 0x10000
	s_addc_u32 s72, s72, 0
	s_add_u32 s56, s56, 0x100
	s_addc_u32 s57, s57, 0
	s_cmp_gt_u32 s73, 13
	s_cbranch_scc0 .LBB0_1192
	s_setprio 0
	s_and_b64 vcc, exec, s[36:37]
	s_cbranch_vccz .LBB0_1195
	s_barrier

.LBB0_1270:
	s_ashr_i32 s51, s50, 31
	s_lshl_b64 s[26:27], s[50:51], 20
	v_readlane_b32 s52, v254, 58
	v_readlane_b32 s53, v254, 59
	s_add_u32 s52, s52, s26
	s_addc_u32 s53, s53, s27
	s_and_b64 s[26:27], s[0:1], exec
	s_cselect_b32 s51, s53, s61
	s_cselect_b32 s57, s52, s60
	s_ashr_i32 s45, s44, 31
	s_lshl_b64 s[26:27], s[44:45], 20
	s_add_u32 s54, s3, s26
	s_addc_u32 s55, s33, s27
	s_and_b64 s[26:27], s[0:1], exec
	s_cselect_b32 s45, s55, s59
	s_cselect_b32 s73, s54, s58
	s_add_u32 s74, s58, 0x10000
	s_addc_u32 s75, s59, 0
	s_add_u32 s58, s60, 0x80080
	v_mov_b32_e32 v2, 0
	s_addc_u32 s59, s61, 0
	s_mov_b32 s80, -2
	v_mov_b32_e32 v3, v2
	v_mov_b32_e32 v4, v2
	v_mov_b32_e32 v5, v2
	v_mov_b32_e32 v6, v2
	v_mov_b32_e32 v7, v2
	v_mov_b32_e32 v8, v2
	v_mov_b32_e32 v9, v2
	v_mov_b32_e32 v10, v2
	v_mov_b32_e32 v11, v2
	v_mov_b32_e32 v12, v2
	v_mov_b32_e32 v13, v2
	v_mov_b32_e32 v18, v2
	v_mov_b32_e32 v19, v2
	v_mov_b32_e32 v20, v2
	v_mov_b32_e32 v21, v2
	v_mov_b32_e32 v26, v2
	v_mov_b32_e32 v27, v2
	v_mov_b32_e32 v28, v2
	v_mov_b32_e32 v29, v2
	v_mov_b32_e32 v34, v2
	v_mov_b32_e32 v35, v2
	v_mov_b32_e32 v36, v2
	v_mov_b32_e32 v37, v2
	v_mov_b32_e32 v42, v2
	v_mov_b32_e32 v43, v2
	v_mov_b32_e32 v44, v2
	v_mov_b32_e32 v45, v2
	v_mov_b32_e32 v50, v2
	v_mov_b32_e32 v51, v2
	v_mov_b32_e32 v52, v2
	v_mov_b32_e32 v53, v2
	v_mov_b32_e32 v14, v2
	v_mov_b32_e32 v15, v2
	v_mov_b32_e32 v16, v2
	v_mov_b32_e32 v17, v2
	v_mov_b32_e32 v22, v2
	v_mov_b32_e32 v23, v2
	v_mov_b32_e32 v24, v2
	v_mov_b32_e32 v25, v2
	v_mov_b32_e32 v30, v2
	v_mov_b32_e32 v31, v2
	v_mov_b32_e32 v32, v2
	v_mov_b32_e32 v33, v2
	v_mov_b32_e32 v38, v2
	v_mov_b32_e32 v39, v2
	v_mov_b32_e32 v40, v2
	v_mov_b32_e32 v41, v2
	v_mov_b32_e32 v46, v2
	v_mov_b32_e32 v47, v2
	v_mov_b32_e32 v48, v2
	v_mov_b32_e32 v49, v2
	v_mov_b32_e32 v54, v2
	v_mov_b32_e32 v55, v2
	v_mov_b32_e32 v56, v2
	v_mov_b32_e32 v57, v2
	v_mov_b32_e32 v58, v2
	v_mov_b32_e32 v59, v2
	v_mov_b32_e32 v60, v2
	v_mov_b32_e32 v61, v2
	v_mov_b32_e32 v62, v2
	v_mov_b32_e32 v63, v2
	v_mov_b32_e32 v64, v2
	v_mov_b32_e32 v65, v2
	v_mov_b32_e32 v66, v2
	v_mov_b32_e32 v67, v2
	v_mov_b32_e32 v68, v2
	v_mov_b32_e32 v69, v2
	v_mov_b32_e32 v70, v2
	v_mov_b32_e32 v71, v2
	v_mov_b32_e32 v72, v2
	v_mov_b32_e32 v73, v2
	v_mov_b32_e32 v74, v2
	v_mov_b32_e32 v75, v2
	v_mov_b32_e32 v76, v2
	v_mov_b32_e32 v77, v2
	v_mov_b32_e32 v78, v2
	v_mov_b32_e32 v79, v2
	v_mov_b32_e32 v80, v2
	v_mov_b32_e32 v81, v2
	v_mov_b32_e32 v86, v2
	v_mov_b32_e32 v87, v2
	v_mov_b32_e32 v88, v2
	v_mov_b32_e32 v89, v2
	v_mov_b32_e32 v94, v2
	v_mov_b32_e32 v95, v2
	v_mov_b32_e32 v96, v2
	v_mov_b32_e32 v97, v2
	v_mov_b32_e32 v102, v2
	v_mov_b32_e32 v103, v2
	v_mov_b32_e32 v104, v2
	v_mov_b32_e32 v105, v2
	v_mov_b32_e32 v110, v2
	v_mov_b32_e32 v111, v2
	v_mov_b32_e32 v112, v2
	v_mov_b32_e32 v113, v2
	v_mov_b32_e32 v82, v2
	v_mov_b32_e32 v83, v2
	v_mov_b32_e32 v84, v2
	v_mov_b32_e32 v85, v2
	v_mov_b32_e32 v90, v2
	v_mov_b32_e32 v91, v2
	v_mov_b32_e32 v92, v2
	v_mov_b32_e32 v93, v2
	v_mov_b32_e32 v98, v2
	v_mov_b32_e32 v99, v2
	v_mov_b32_e32 v100, v2
	v_mov_b32_e32 v101, v2
	v_mov_b32_e32 v106, v2
	v_mov_b32_e32 v107, v2
	v_mov_b32_e32 v108, v2
	v_mov_b32_e32 v109, v2
	v_mov_b32_e32 v114, v2
	v_mov_b32_e32 v115, v2
	v_mov_b32_e32 v116, v2
	v_mov_b32_e32 v117, v2
	v_mov_b32_e32 v118, v2
	v_mov_b32_e32 v119, v2
	v_mov_b32_e32 v120, v2
	v_mov_b32_e32 v121, v2
	v_mov_b32_e32 v122, v2
	v_mov_b32_e32 v123, v2
	v_mov_b32_e32 v124, v2
	v_mov_b32_e32 v125, v2
	v_mov_b32_e32 v126, v2
	v_mov_b32_e32 v127, v2
	v_mov_b32_e32 v128, v2
	v_mov_b32_e32 v129, v2
	v_readfirstlane_b32 s98, v0
	s_lshr_b32 s98, s98, 8
	s_cmp_eq_u32 s98, 1
	s_cbranch_scc0 .Lprio_skip2
	s_setprio 1
.Lprio_skip2:
.LBB0_1271:
	ds_read_b128 v[144:147], v158
	ds_read_b128 v[148:151], v158 offset:1024
	ds_read_b128 v[152:155], v158 offset:2048
	ds_read_b128 v[162:165], v158 offset:3072
	ds_read_b128 v[166:169], v159
	ds_read_b128 v[170:173], v159 offset:1024
	ds_read_b128 v[174:177], v159 offset:2048
	ds_read_b128 v[178:181], v159 offset:3072
	s_add_u32 s26, s58, 0xfff80080
	s_addc_u32 s27, s59, -1
	s_cmp_eq_u32 s80, 28
	s_cselect_b32 s61, s51, s27
	s_cselect_b32 s60, s57, s26
	s_cselect_b32 s27, s45, s75
	s_cselect_b32 s26, s73, s74
	v_lshl_add_u64 v[214:215], s[58:59], 0, v[136:137]
	s_add_i32 m0, s63, 0xc000
	ds_read_b128 v[182:185], v160
	ds_read_b128 v[186:189], v160 offset:1024
	ds_read_b128 v[190:193], v160 offset:2048
	ds_read_b128 v[194:197], v160 offset:3072
	ds_read_b128 v[198:201], v160 offset:4096
	ds_read_b128 v[202:205], v160 offset:5120
	ds_read_b128 v[206:209], v160 offset:6144
	ds_read_b128 v[210:213], v160 offset:7168
	global_load_lds_dwordx4 v[214:215], off
	v_lshl_add_u64 v[214:215], s[58:59], 0, v[138:139]
	s_add_i32 m0, s63, 0xe000
	s_nop 0
	global_load_lds_dwordx4 v[214:215], off
	s_waitcnt vmcnt(8)
	s_waitcnt lgkmcnt(0)
	s_barrier
	s_waitcnt lgkmcnt(0)
	v_mfma_f32_16x16x32_bf16 v[126:129], v[144:147], v[182:185], v[126:129]
	v_mfma_f32_16x16x32_bf16 v[122:125], v[152:155], v[182:185], v[122:125]
	v_mfma_f32_16x16x32_bf16 v[118:121], v[144:147], v[190:193], v[118:121]
	v_mfma_f32_16x16x32_bf16 v[114:117], v[152:155], v[190:193], v[114:117]
	v_mfma_f32_16x16x32_bf16 v[106:109], v[144:147], v[198:201], v[106:109]
	v_mfma_f32_16x16x32_bf16 v[98:101], v[152:155], v[198:201], v[98:101]
	v_mfma_f32_16x16x32_bf16 v[90:93], v[144:147], v[206:209], v[90:93]
	v_mfma_f32_16x16x32_bf16 v[82:85], v[152:155], v[206:209], v[82:85]
	v_mfma_f32_16x16x32_bf16 v[126:129], v[148:151], v[186:189], v[126:129]
	v_mfma_f32_16x16x32_bf16 v[122:125], v[162:165], v[186:189], v[122:125]
	v_mfma_f32_16x16x32_bf16 v[118:121], v[148:151], v[194:197], v[118:121]
	v_mfma_f32_16x16x32_bf16 v[114:117], v[162:165], v[194:197], v[114:117]
	v_mfma_f32_16x16x32_bf16 v[106:109], v[148:151], v[202:205], v[106:109]
	v_mfma_f32_16x16x32_bf16 v[98:101], v[162:165], v[202:205], v[98:101]
	v_mfma_f32_16x16x32_bf16 v[90:93], v[148:151], v[210:213], v[90:93]
	v_mfma_f32_16x16x32_bf16 v[82:85], v[162:165], v[210:213], v[82:85]
	v_mfma_f32_16x16x32_bf16 v[110:113], v[166:169], v[182:185], v[110:113]
	v_mfma_f32_16x16x32_bf16 v[102:105], v[174:177], v[182:185], v[102:105]
	v_mfma_f32_16x16x32_bf16 v[94:97], v[166:169], v[190:193], v[94:97]
	v_mfma_f32_16x16x32_bf16 v[86:89], v[174:177], v[190:193], v[86:89]
	v_mfma_f32_16x16x32_bf16 v[78:81], v[166:169], v[198:201], v[78:81]
	v_mfma_f32_16x16x32_bf16 v[74:77], v[174:177], v[198:201], v[74:77]
	v_mfma_f32_16x16x32_bf16 v[70:73], v[166:169], v[206:209], v[70:73]
	v_mfma_f32_16x16x32_bf16 v[66:69], v[174:177], v[206:209], v[66:69]
	v_mfma_f32_16x16x32_bf16 v[110:113], v[170:173], v[186:189], v[110:113]
	v_mfma_f32_16x16x32_bf16 v[102:105], v[178:181], v[186:189], v[102:105]
	v_mfma_f32_16x16x32_bf16 v[94:97], v[170:173], v[194:197], v[94:97]
	v_mfma_f32_16x16x32_bf16 v[86:89], v[178:181], v[194:197], v[86:89]
	v_mfma_f32_16x16x32_bf16 v[78:81], v[170:173], v[202:205], v[78:81]
	v_mfma_f32_16x16x32_bf16 v[74:77], v[178:181], v[202:205], v[74:77]
	v_mfma_f32_16x16x32_bf16 v[70:73], v[170:173], v[210:213], v[70:73]
	v_mfma_f32_16x16x32_bf16 v[66:69], v[178:181], v[210:213], v[66:69]
	s_barrier
	v_lshl_add_u64 v[214:215], s[26:27], 0, v[130:131]
	s_add_i32 s26, s71, s35
	s_mov_b32 m0, s26
	ds_read_b128 v[182:185], v160 offset:16384
	ds_read_b128 v[186:189], v160 offset:17408
	ds_read_b128 v[190:193], v160 offset:18432
	ds_read_b128 v[194:197], v160 offset:19456
	ds_read_b128 v[198:201], v160 offset:20480
	ds_read_b128 v[202:205], v160 offset:21504
	ds_read_b128 v[206:209], v160 offset:22528
	ds_read_b128 v[210:213], v160 offset:23552
	global_load_lds_dwordx4 v[214:215], off
	v_lshl_add_u64 v[216:217], v[214:215], 0, s[6:7]
	s_add_i32 m0, s26, 0x2000
	s_add_i32 s26, s72, s35
	global_load_lds_dwordx4 v[216:217], off
	v_lshl_add_u64 v[216:217], v[214:215], 0, s[8:9]
	s_mov_b32 m0, s26
	v_lshl_add_u64 v[220:221], s[60:61], 0, v[134:135]
	global_load_lds_dwordx4 v[216:217], off
	v_lshl_add_u64 v[216:217], v[214:215], 0, s[10:11]
	s_add_i32 m0, s26, 0x2000
	s_nop 0
	global_load_lds_dwordx4 v[216:217], off
	v_lshl_add_u64 v[216:217], s[60:61], 0, v[132:133]
	s_mov_b32 m0, s63
	s_nop 0
	global_load_lds_dwordx4 v[216:217], off
	s_mov_b32 m0, s64
	s_nop 0
	global_load_lds_dwordx4 v[220:221], off
	s_waitcnt vmcnt(8)
	s_waitcnt lgkmcnt(0)
	s_barrier
	s_waitcnt lgkmcnt(0)
	v_mfma_f32_16x16x32_bf16 v[62:65], v[144:147], v[182:185], v[62:65]
	v_mfma_f32_16x16x32_bf16 v[58:61], v[152:155], v[182:185], v[58:61]
	v_mfma_f32_16x16x32_bf16 v[54:57], v[144:147], v[190:193], v[54:57]
	v_mfma_f32_16x16x32_bf16 v[46:49], v[152:155], v[190:193], v[46:49]
	v_mfma_f32_16x16x32_bf16 v[38:41], v[144:147], v[198:201], v[38:41]
	v_mfma_f32_16x16x32_bf16 v[30:33], v[152:155], v[198:201], v[30:33]
	v_mfma_f32_16x16x32_bf16 v[22:25], v[144:147], v[206:209], v[22:25]
	v_mfma_f32_16x16x32_bf16 v[14:17], v[152:155], v[206:209], v[14:17]
	v_mfma_f32_16x16x32_bf16 v[62:65], v[148:151], v[186:189], v[62:65]
	v_mfma_f32_16x16x32_bf16 v[58:61], v[162:165], v[186:189], v[58:61]
	v_mfma_f32_16x16x32_bf16 v[54:57], v[148:151], v[194:197], v[54:57]
	v_mfma_f32_16x16x32_bf16 v[46:49], v[162:165], v[194:197], v[46:49]
	v_mfma_f32_16x16x32_bf16 v[38:41], v[148:151], v[202:205], v[38:41]
	v_mfma_f32_16x16x32_bf16 v[30:33], v[162:165], v[202:205], v[30:33]
	v_mfma_f32_16x16x32_bf16 v[22:25], v[148:151], v[210:213], v[22:25]
	v_mfma_f32_16x16x32_bf16 v[14:17], v[162:165], v[210:213], v[14:17]
	v_mfma_f32_16x16x32_bf16 v[50:53], v[166:169], v[182:185], v[50:53]
	v_mfma_f32_16x16x32_bf16 v[42:45], v[174:177], v[182:185], v[42:45]
	v_mfma_f32_16x16x32_bf16 v[34:37], v[166:169], v[190:193], v[34:37]
	v_mfma_f32_16x16x32_bf16 v[26:29], v[174:177], v[190:193], v[26:29]
	v_mfma_f32_16x16x32_bf16 v[18:21], v[166:169], v[198:201], v[18:21]
	v_mfma_f32_16x16x32_bf16 v[10:13], v[174:177], v[198:201], v[10:13]
	v_mfma_f32_16x16x32_bf16 v[6:9], v[166:169], v[206:209], v[6:9]
	v_mfma_f32_16x16x32_bf16 v[2:5], v[174:177], v[206:209], v[2:5]
	v_mfma_f32_16x16x32_bf16 v[50:53], v[170:173], v[186:189], v[50:53]
	v_mfma_f32_16x16x32_bf16 v[42:45], v[178:181], v[186:189], v[42:45]
	v_mfma_f32_16x16x32_bf16 v[34:37], v[170:173], v[194:197], v[34:37]
	v_mfma_f32_16x16x32_bf16 v[26:29], v[178:181], v[194:197], v[26:29]
	v_mfma_f32_16x16x32_bf16 v[18:21], v[170:173], v[202:205], v[18:21]
	v_mfma_f32_16x16x32_bf16 v[10:13], v[178:181], v[202:205], v[10:13]
	v_mfma_f32_16x16x32_bf16 v[6:9], v[170:173], v[210:213], v[6:9]
	v_mfma_f32_16x16x32_bf16 v[2:5], v[178:181], v[210:213], v[2:5]
	s_barrier
	s_add_i32 s81, 0, 0x18000
	v_add_u32_e32 v161, s81, v156
	s_add_i32 s82, 0, 0x1c000
	ds_read_b128 v[144:147], v161
	ds_read_b128 v[148:151], v161 offset:1024
	ds_read_b128 v[152:155], v161 offset:2048
	ds_read_b128 v[162:165], v161 offset:3072
	v_add_u32_e32 v161, s82, v156
	ds_read_b128 v[166:169], v161
	ds_read_b128 v[170:173], v161 offset:1024
	ds_read_b128 v[174:177], v161 offset:2048
	ds_read_b128 v[178:181], v161 offset:3072
	s_add_u32 s26, s60, 0x80000
	s_addc_u32 s27, s61, 0
	s_mov_b32 m0, s65
	v_lshl_add_u64 v[222:223], s[26:27], 0, v[132:133]
	ds_read_b128 v[182:185], v160 offset:32768
	ds_read_b128 v[186:189], v160 offset:33792
	ds_read_b128 v[190:193], v160 offset:34816
	ds_read_b128 v[194:197], v160 offset:35840
	ds_read_b128 v[198:201], v160 offset:36864
	ds_read_b128 v[202:205], v160 offset:37888
	ds_read_b128 v[206:209], v160 offset:38912
	ds_read_b128 v[210:213], v160 offset:39936
	global_load_lds_dwordx4 v[222:223], off
	v_lshl_add_u64 v[222:223], s[26:27], 0, v[134:135]
	s_mov_b32 m0, s66
	s_nop 0
	global_load_lds_dwordx4 v[222:223], off
	s_waitcnt vmcnt(8)
	s_waitcnt lgkmcnt(0)
	s_barrier
	s_waitcnt lgkmcnt(0)
	v_mfma_f32_16x16x32_bf16 v[126:129], v[144:147], v[182:185], v[126:129]
	v_mfma_f32_16x16x32_bf16 v[122:125], v[152:155], v[182:185], v[122:125]
	v_mfma_f32_16x16x32_bf16 v[118:121], v[144:147], v[190:193], v[118:121]
	v_mfma_f32_16x16x32_bf16 v[114:117], v[152:155], v[190:193], v[114:117]
	v_mfma_f32_16x16x32_bf16 v[106:109], v[144:147], v[198:201], v[106:109]
	v_mfma_f32_16x16x32_bf16 v[98:101], v[152:155], v[198:201], v[98:101]
	v_mfma_f32_16x16x32_bf16 v[90:93], v[144:147], v[206:209], v[90:93]
	v_mfma_f32_16x16x32_bf16 v[82:85], v[152:155], v[206:209], v[82:85]
	v_mfma_f32_16x16x32_bf16 v[126:129], v[148:151], v[186:189], v[126:129]
	v_mfma_f32_16x16x32_bf16 v[122:125], v[162:165], v[186:189], v[122:125]
	v_mfma_f32_16x16x32_bf16 v[118:121], v[148:151], v[194:197], v[118:121]
	v_mfma_f32_16x16x32_bf16 v[114:117], v[162:165], v[194:197], v[114:117]
	v_mfma_f32_16x16x32_bf16 v[106:109], v[148:151], v[202:205], v[106:109]
	v_mfma_f32_16x16x32_bf16 v[98:101], v[162:165], v[202:205], v[98:101]
	v_mfma_f32_16x16x32_bf16 v[90:93], v[148:151], v[210:213], v[90:93]
	v_mfma_f32_16x16x32_bf16 v[82:85], v[162:165], v[210:213], v[82:85]
	v_mfma_f32_16x16x32_bf16 v[110:113], v[166:169], v[182:185], v[110:113]
	v_mfma_f32_16x16x32_bf16 v[102:105], v[174:177], v[182:185], v[102:105]
	v_mfma_f32_16x16x32_bf16 v[94:97], v[166:169], v[190:193], v[94:97]
	v_mfma_f32_16x16x32_bf16 v[86:89], v[174:177], v[190:193], v[86:89]
	v_mfma_f32_16x16x32_bf16 v[78:81], v[166:169], v[198:201], v[78:81]
	v_mfma_f32_16x16x32_bf16 v[74:77], v[174:177], v[198:201], v[74:77]
	v_mfma_f32_16x16x32_bf16 v[70:73], v[166:169], v[206:209], v[70:73]
	v_mfma_f32_16x16x32_bf16 v[66:69], v[174:177], v[206:209], v[66:69]
	v_mfma_f32_16x16x32_bf16 v[110:113], v[170:173], v[186:189], v[110:113]
	v_mfma_f32_16x16x32_bf16 v[102:105], v[178:181], v[186:189], v[102:105]
	v_mfma_f32_16x16x32_bf16 v[94:97], v[170:173], v[194:197], v[94:97]
	v_mfma_f32_16x16x32_bf16 v[86:89], v[178:181], v[194:197], v[86:89]
	v_mfma_f32_16x16x32_bf16 v[78:81], v[170:173], v[202:205], v[78:81]
	v_mfma_f32_16x16x32_bf16 v[74:77], v[178:181], v[202:205], v[74:77]
	v_mfma_f32_16x16x32_bf16 v[70:73], v[170:173], v[210:213], v[70:73]
	v_mfma_f32_16x16x32_bf16 v[66:69], v[178:181], v[210:213], v[66:69]
	s_barrier
	s_add_i32 s26, s81, s35
	v_lshl_add_u64 v[222:223], v[214:215], 0, s[14:15]
	s_mov_b32 m0, s26
	ds_read_b128 v[182:185], v160 offset:49152
	ds_read_b128 v[186:189], v160 offset:50176
	ds_read_b128 v[190:193], v160 offset:51200
	ds_read_b128 v[194:197], v160 offset:52224
	ds_read_b128 v[198:201], v160 offset:53248
	ds_read_b128 v[202:205], v160 offset:54272
	ds_read_b128 v[206:209], v160 offset:55296
	ds_read_b128 v[210:213], v160 offset:56320
	global_load_lds_dwordx4 v[222:223], off
	v_lshl_add_u64 v[222:223], v[214:215], 0, s[16:17]
	s_add_i32 m0, s26, 0x2000
	s_add_i32 s26, s82, s35
	global_load_lds_dwordx4 v[222:223], off
	v_lshl_add_u64 v[222:223], v[214:215], 0, s[20:21]
	s_mov_b32 m0, s26
	v_lshl_add_u64 v[214:215], v[214:215], 0, s[22:23]
	global_load_lds_dwordx4 v[222:223], off
	s_add_i32 m0, s26, 0x2000
	s_nop 0
	global_load_lds_dwordx4 v[214:215], off
	v_lshl_add_u64 v[214:215], v[216:217], 0, s[18:19]
	s_mov_b32 m0, s68
	s_nop 0
	global_load_lds_dwordx4 v[214:215], off
	v_lshl_add_u64 v[214:215], v[220:221], 0, s[18:19]
	s_mov_b32 m0, s69
	s_nop 0
	global_load_lds_dwordx4 v[214:215], off
	s_waitcnt vmcnt(8)
	s_waitcnt lgkmcnt(0)
	s_barrier
	s_waitcnt lgkmcnt(0)
	v_mfma_f32_16x16x32_bf16 v[62:65], v[144:147], v[182:185], v[62:65]
	v_mfma_f32_16x16x32_bf16 v[58:61], v[152:155], v[182:185], v[58:61]
	v_mfma_f32_16x16x32_bf16 v[54:57], v[144:147], v[190:193], v[54:57]
	v_mfma_f32_16x16x32_bf16 v[46:49], v[152:155], v[190:193], v[46:49]
	v_mfma_f32_16x16x32_bf16 v[38:41], v[144:147], v[198:201], v[38:41]
	v_mfma_f32_16x16x32_bf16 v[30:33], v[152:155], v[198:201], v[30:33]
	v_mfma_f32_16x16x32_bf16 v[22:25], v[144:147], v[206:209], v[22:25]
	v_mfma_f32_16x16x32_bf16 v[14:17], v[152:155], v[206:209], v[14:17]
	v_mfma_f32_16x16x32_bf16 v[62:65], v[148:151], v[186:189], v[62:65]
	v_mfma_f32_16x16x32_bf16 v[58:61], v[162:165], v[186:189], v[58:61]
	v_mfma_f32_16x16x32_bf16 v[54:57], v[148:151], v[194:197], v[54:57]
	v_mfma_f32_16x16x32_bf16 v[46:49], v[162:165], v[194:197], v[46:49]
	v_mfma_f32_16x16x32_bf16 v[38:41], v[148:151], v[202:205], v[38:41]
	v_mfma_f32_16x16x32_bf16 v[30:33], v[162:165], v[202:205], v[30:33]
	v_mfma_f32_16x16x32_bf16 v[22:25], v[148:151], v[210:213], v[22:25]
	v_mfma_f32_16x16x32_bf16 v[14:17], v[162:165], v[210:213], v[14:17]
	v_mfma_f32_16x16x32_bf16 v[50:53], v[166:169], v[182:185], v[50:53]
	v_mfma_f32_16x16x32_bf16 v[42:45], v[174:177], v[182:185], v[42:45]
	v_mfma_f32_16x16x32_bf16 v[34:37], v[166:169], v[190:193], v[34:37]
	v_mfma_f32_16x16x32_bf16 v[26:29], v[174:177], v[190:193], v[26:29]
	v_mfma_f32_16x16x32_bf16 v[18:21], v[166:169], v[198:201], v[18:21]
	v_mfma_f32_16x16x32_bf16 v[10:13], v[174:177], v[198:201], v[10:13]
	v_mfma_f32_16x16x32_bf16 v[6:9], v[166:169], v[206:209], v[6:9]
	v_mfma_f32_16x16x32_bf16 v[2:5], v[174:177], v[206:209], v[2:5]
	v_mfma_f32_16x16x32_bf16 v[50:53], v[170:173], v[186:189], v[50:53]
	v_mfma_f32_16x16x32_bf16 v[42:45], v[178:181], v[186:189], v[42:45]
	v_mfma_f32_16x16x32_bf16 v[34:37], v[170:173], v[194:197], v[34:37]
	v_mfma_f32_16x16x32_bf16 v[26:29], v[178:181], v[194:197], v[26:29]
	v_mfma_f32_16x16x32_bf16 v[18:21], v[170:173], v[202:205], v[18:21]
	v_mfma_f32_16x16x32_bf16 v[10:13], v[178:181], v[202:205], v[10:13]
	v_mfma_f32_16x16x32_bf16 v[6:9], v[170:173], v[210:213], v[6:9]
	v_mfma_f32_16x16x32_bf16 v[2:5], v[178:181], v[210:213], v[2:5]
	s_barrier
	s_add_i32 s80, s80, 2
	s_add_u32 s74, s74, 0x10000
	s_addc_u32 s75, s75, 0
	s_add_u32 s58, s58, 0x100
	s_addc_u32 s59, s59, 0
	s_cmp_gt_u32 s80, 29
	s_cbranch_scc0 .LBB0_1271
	s_setprio 0
	s_and_b64 vcc, exec, s[24:25]
	s_cbranch_vccz .LBB0_1274
	s_barrier

.LBB0_1496:
	s_lshl_b64 s[50:51], s[48:49], 19
	s_add_u32 s50, s59, s50
	s_addc_u32 s51, s60, s51
	s_and_b64 s[4:5], s[4:5], exec
	s_cselect_b32 s2, s51, s57
	s_cselect_b32 s47, s50, s56
	s_add_u32 s4, s56, 0x40080
	v_mov_b32_e32 v34, 0
	v_lshl_add_u64 v[176:177], v[2:3], 0, s[40:41]
	s_addc_u32 s5, s57, 0
	s_mov_b32 s49, -2
	v_mov_b32_e32 v35, v34
	v_mov_b32_e32 v36, v34
	v_mov_b32_e32 v37, v34
	v_mov_b32_e32 v42, v34
	v_mov_b32_e32 v43, v34
	v_mov_b32_e32 v44, v34
	v_mov_b32_e32 v45, v34
	v_mov_b32_e32 v50, v34
	v_mov_b32_e32 v51, v34
	v_mov_b32_e32 v52, v34
	v_mov_b32_e32 v53, v34
	v_mov_b32_e32 v58, v34
	v_mov_b32_e32 v59, v34
	v_mov_b32_e32 v60, v34
	v_mov_b32_e32 v61, v34
	v_mov_b32_e32 v66, v34
	v_mov_b32_e32 v67, v34
	v_mov_b32_e32 v68, v34
	v_mov_b32_e32 v69, v34
	v_mov_b32_e32 v74, v34
	v_mov_b32_e32 v75, v34
	v_mov_b32_e32 v76, v34
	v_mov_b32_e32 v77, v34
	v_mov_b32_e32 v82, v34
	v_mov_b32_e32 v83, v34
	v_mov_b32_e32 v84, v34
	v_mov_b32_e32 v85, v34
	v_mov_b32_e32 v90, v34
	v_mov_b32_e32 v91, v34
	v_mov_b32_e32 v92, v34
	v_mov_b32_e32 v93, v34
	v_mov_b32_e32 v38, v34
	v_mov_b32_e32 v39, v34
	v_mov_b32_e32 v40, v34
	v_mov_b32_e32 v41, v34
	v_mov_b32_e32 v46, v34
	v_mov_b32_e32 v47, v34
	v_mov_b32_e32 v48, v34
	v_mov_b32_e32 v49, v34
	v_mov_b32_e32 v54, v34
	v_mov_b32_e32 v55, v34
	v_mov_b32_e32 v56, v34
	v_mov_b32_e32 v57, v34
	v_mov_b32_e32 v62, v34
	v_mov_b32_e32 v63, v34
	v_mov_b32_e32 v64, v34
	v_mov_b32_e32 v65, v34
	v_mov_b32_e32 v70, v34
	v_mov_b32_e32 v71, v34
	v_mov_b32_e32 v72, v34
	v_mov_b32_e32 v73, v34
	v_mov_b32_e32 v78, v34
	v_mov_b32_e32 v79, v34
	v_mov_b32_e32 v80, v34
	v_mov_b32_e32 v81, v34
	v_mov_b32_e32 v86, v34
	v_mov_b32_e32 v87, v34
	v_mov_b32_e32 v88, v34
	v_mov_b32_e32 v89, v34
	v_mov_b32_e32 v94, v34
	v_mov_b32_e32 v95, v34
	v_mov_b32_e32 v96, v34
	v_mov_b32_e32 v97, v34
	v_mov_b32_e32 v98, v34
	v_mov_b32_e32 v99, v34
	v_mov_b32_e32 v100, v34
	v_mov_b32_e32 v101, v34
	v_mov_b32_e32 v106, v34
	v_mov_b32_e32 v107, v34
	v_mov_b32_e32 v108, v34
	v_mov_b32_e32 v109, v34
	v_mov_b32_e32 v114, v34
	v_mov_b32_e32 v115, v34
	v_mov_b32_e32 v116, v34
	v_mov_b32_e32 v117, v34
	v_mov_b32_e32 v122, v34
	v_mov_b32_e32 v123, v34
	v_mov_b32_e32 v124, v34
	v_mov_b32_e32 v125, v34
	v_mov_b32_e32 v130, v34
	v_mov_b32_e32 v131, v34
	v_mov_b32_e32 v132, v34
	v_mov_b32_e32 v133, v34
	v_mov_b32_e32 v138, v34
	v_mov_b32_e32 v139, v34
	v_mov_b32_e32 v140, v34
	v_mov_b32_e32 v141, v34
	v_mov_b32_e32 v146, v34
	v_mov_b32_e32 v147, v34
	v_mov_b32_e32 v148, v34
	v_mov_b32_e32 v149, v34
	v_mov_b32_e32 v154, v34
	v_mov_b32_e32 v155, v34
	v_mov_b32_e32 v156, v34
	v_mov_b32_e32 v157, v34
	v_mov_b32_e32 v102, v34
	v_mov_b32_e32 v103, v34
	v_mov_b32_e32 v104, v34
	v_mov_b32_e32 v105, v34
	v_mov_b32_e32 v110, v34
	v_mov_b32_e32 v111, v34
	v_mov_b32_e32 v112, v34
	v_mov_b32_e32 v113, v34
	v_mov_b32_e32 v118, v34
	v_mov_b32_e32 v119, v34
	v_mov_b32_e32 v120, v34
	v_mov_b32_e32 v121, v34
	v_mov_b32_e32 v126, v34
	v_mov_b32_e32 v127, v34
	v_mov_b32_e32 v128, v34
	v_mov_b32_e32 v129, v34
	v_mov_b32_e32 v134, v34
	v_mov_b32_e32 v135, v34
	v_mov_b32_e32 v136, v34
	v_mov_b32_e32 v137, v34
	v_mov_b32_e32 v142, v34
	v_mov_b32_e32 v143, v34
	v_mov_b32_e32 v144, v34
	v_mov_b32_e32 v145, v34
	v_mov_b32_e32 v150, v34
	v_mov_b32_e32 v151, v34
	v_mov_b32_e32 v152, v34
	v_mov_b32_e32 v153, v34
	v_mov_b32_e32 v158, v34
	v_mov_b32_e32 v159, v34
	v_mov_b32_e32 v160, v34
	v_mov_b32_e32 v161, v34
	v_readfirstlane_b32 s98, v0
	s_lshr_b32 s98, s98, 8
	s_cmp_eq_u32 s98, 1
	s_cbranch_scc0 .Lprio_skip1
	s_setprio 1
.Lprio_skip1:
.LBB0_1497:
	ds_read_b128 v[26:29], v186
	ds_read_b128 v[30:33], v186 offset:1024
	ds_read_b128 v[18:21], v186 offset:2048
	ds_read_b128 v[22:25], v186 offset:3072
	ds_read_b128 v[10:13], v187
	ds_read_b128 v[14:17], v187 offset:1024
	ds_read_b128 v[2:5], v187 offset:2048
	ds_read_b128 v[6:9], v187 offset:3072
	s_add_u32 s56, s4, 0xfffc0080
	s_addc_u32 s57, s5, -1
	s_cmp_eq_u32 s49, 12
	s_cselect_b64 vcc, -1, 0
	s_cselect_b32 s57, s2, s57
	s_cselect_b32 s56, s47, s56
	v_cndmask_b32_e32 v179, v177, v175, vcc
	v_cndmask_b32_e32 v178, v176, v174, vcc
	v_lshl_add_u64 v[180:181], s[4:5], 0, v[168:169]
	s_add_i32 m0, s62, 0xc000
	ds_read_b128 v[192:195], v188
	ds_read_b128 v[196:199], v188 offset:1024
	ds_read_b128 v[200:203], v188 offset:2048
	ds_read_b128 v[204:207], v188 offset:3072
	ds_read_b128 v[208:211], v188 offset:4096
	ds_read_b128 v[212:215], v188 offset:5120
	ds_read_b128 v[220:223], v188 offset:6144
	ds_read_b128 v[224:227], v188 offset:7168
	global_load_lds_dwordx4 v[180:181], off
	v_lshl_add_u64 v[180:181], s[4:5], 0, v[170:171]
	s_add_i32 m0, s62, 0xe000
	s_nop 0
	global_load_lds_dwordx4 v[180:181], off
	s_waitcnt vmcnt(8)
	s_waitcnt lgkmcnt(0)
	s_barrier
	s_waitcnt lgkmcnt(0)
	v_mfma_scale_f32_16x16x128_f8f6f4 v[158:161], v[26:33], v[192:199], v[158:161], v189, v190 op_sel_hi:[0,0,0]
	v_mfma_scale_f32_16x16x128_f8f6f4 v[150:153], v[18:25], v[192:199], v[150:153], v189, v190 op_sel_hi:[0,0,0]
	v_mfma_scale_f32_16x16x128_f8f6f4 v[142:145], v[26:33], v[200:207], v[142:145], v189, v190 op_sel_hi:[0,0,0]
	v_mfma_scale_f32_16x16x128_f8f6f4 v[134:137], v[18:25], v[200:207], v[134:137], v189, v190 op_sel_hi:[0,0,0]
	v_mfma_scale_f32_16x16x128_f8f6f4 v[126:129], v[26:33], v[208:215], v[126:129], v189, v190 op_sel_hi:[0,0,0]
	v_mfma_scale_f32_16x16x128_f8f6f4 v[118:121], v[18:25], v[208:215], v[118:121], v189, v190 op_sel_hi:[0,0,0]
	v_mfma_scale_f32_16x16x128_f8f6f4 v[110:113], v[26:33], v[220:227], v[110:113], v189, v190 op_sel_hi:[0,0,0]
	v_mfma_scale_f32_16x16x128_f8f6f4 v[102:105], v[18:25], v[220:227], v[102:105], v189, v190 op_sel_hi:[0,0,0]
	v_mfma_scale_f32_16x16x128_f8f6f4 v[154:157], v[10:17], v[192:199], v[154:157], v189, v190 op_sel_hi:[0,0,0]
	v_mfma_scale_f32_16x16x128_f8f6f4 v[146:149], v[2:9], v[192:199], v[146:149], v189, v190 op_sel_hi:[0,0,0]
	v_mfma_scale_f32_16x16x128_f8f6f4 v[138:141], v[10:17], v[200:207], v[138:141], v189, v190 op_sel_hi:[0,0,0]
	v_mfma_scale_f32_16x16x128_f8f6f4 v[130:133], v[2:9], v[200:207], v[130:133], v189, v190 op_sel_hi:[0,0,0]
	v_mfma_scale_f32_16x16x128_f8f6f4 v[122:125], v[10:17], v[208:215], v[122:125], v189, v190 op_sel_hi:[0,0,0]
	v_mfma_scale_f32_16x16x128_f8f6f4 v[114:117], v[2:9], v[208:215], v[114:117], v189, v190 op_sel_hi:[0,0,0]
	v_mfma_scale_f32_16x16x128_f8f6f4 v[106:109], v[10:17], v[220:227], v[106:109], v189, v190 op_sel_hi:[0,0,0]
	v_mfma_scale_f32_16x16x128_f8f6f4 v[98:101], v[2:9], v[220:227], v[98:101], v189, v190 op_sel_hi:[0,0,0]
	s_barrier
	s_add_i32 s73, s69, s61
	v_lshl_add_u64 v[178:179], v[178:179], 0, v[162:163]
	s_mov_b32 m0, s73
	ds_read_b128 v[192:195], v188 offset:16384
	ds_read_b128 v[196:199], v188 offset:17408
	ds_read_b128 v[200:203], v188 offset:18432
	ds_read_b128 v[204:207], v188 offset:19456
	ds_read_b128 v[208:211], v188 offset:20480
	ds_read_b128 v[212:215], v188 offset:21504
	ds_read_b128 v[220:223], v188 offset:22528
	ds_read_b128 v[224:227], v188 offset:23552
	global_load_lds_dwordx4 v[178:179], off
	v_lshl_add_u64 v[180:181], v[178:179], 0, s[10:11]
	s_add_i32 m0, s73, 0x2000
	s_add_i32 s73, s70, s61
	global_load_lds_dwordx4 v[180:181], off
	v_lshl_add_u64 v[180:181], v[178:179], 0, s[12:13]
	s_mov_b32 m0, s73
	v_lshl_add_u64 v[182:183], s[56:57], 0, v[166:167]
	global_load_lds_dwordx4 v[180:181], off
	v_lshl_add_u64 v[180:181], v[178:179], 0, s[14:15]
	s_add_i32 m0, s73, 0x2000
	s_nop 0
	global_load_lds_dwordx4 v[180:181], off
	v_lshl_add_u64 v[180:181], s[56:57], 0, v[164:165]
	s_mov_b32 m0, s62
	s_nop 0
	global_load_lds_dwordx4 v[180:181], off
	s_mov_b32 m0, s53
	s_nop 0
	global_load_lds_dwordx4 v[182:183], off
	s_waitcnt vmcnt(8)
	s_waitcnt lgkmcnt(0)
	s_barrier
	s_waitcnt lgkmcnt(0)
	v_mfma_scale_f32_16x16x128_f8f6f4 v[94:97], v[26:33], v[192:199], v[94:97], v189, v190 op_sel_hi:[0,0,0]
	v_mfma_scale_f32_16x16x128_f8f6f4 v[86:89], v[18:25], v[192:199], v[86:89], v189, v190 op_sel_hi:[0,0,0]
	v_mfma_scale_f32_16x16x128_f8f6f4 v[78:81], v[26:33], v[200:207], v[78:81], v189, v190 op_sel_hi:[0,0,0]
	v_mfma_scale_f32_16x16x128_f8f6f4 v[70:73], v[18:25], v[200:207], v[70:73], v189, v190 op_sel_hi:[0,0,0]
	v_mfma_scale_f32_16x16x128_f8f6f4 v[62:65], v[26:33], v[208:215], v[62:65], v189, v190 op_sel_hi:[0,0,0]
	v_mfma_scale_f32_16x16x128_f8f6f4 v[54:57], v[18:25], v[208:215], v[54:57], v189, v190 op_sel_hi:[0,0,0]
	v_mfma_scale_f32_16x16x128_f8f6f4 v[46:49], v[26:33], v[220:227], v[46:49], v189, v190 op_sel_hi:[0,0,0]
	v_mfma_scale_f32_16x16x128_f8f6f4 v[38:41], v[18:25], v[220:227], v[38:41], v189, v190 op_sel_hi:[0,0,0]
	v_mfma_scale_f32_16x16x128_f8f6f4 v[90:93], v[10:17], v[192:199], v[90:93], v189, v190 op_sel_hi:[0,0,0]
	v_mfma_scale_f32_16x16x128_f8f6f4 v[82:85], v[2:9], v[192:199], v[82:85], v189, v190 op_sel_hi:[0,0,0]
	v_mfma_scale_f32_16x16x128_f8f6f4 v[74:77], v[10:17], v[200:207], v[74:77], v189, v190 op_sel_hi:[0,0,0]
	v_mfma_scale_f32_16x16x128_f8f6f4 v[66:69], v[2:9], v[200:207], v[66:69], v189, v190 op_sel_hi:[0,0,0]
	v_mfma_scale_f32_16x16x128_f8f6f4 v[58:61], v[10:17], v[208:215], v[58:61], v189, v190 op_sel_hi:[0,0,0]
	v_mfma_scale_f32_16x16x128_f8f6f4 v[50:53], v[2:9], v[208:215], v[50:53], v189, v190 op_sel_hi:[0,0,0]
	v_mfma_scale_f32_16x16x128_f8f6f4 v[42:45], v[10:17], v[220:227], v[42:45], v189, v190 op_sel_hi:[0,0,0]
	v_mfma_scale_f32_16x16x128_f8f6f4 v[34:37], v[2:9], v[220:227], v[34:37], v189, v190 op_sel_hi:[0,0,0]
	s_barrier
	s_add_i32 s73, 0, 0x18000
	s_add_i32 s74, 0, 0x1c000
	v_add_u32_e32 v14, s73, v184
	v_add_u32_e32 v30, s74, v184
	ds_read_b128 v[2:5], v14
	ds_read_b128 v[6:9], v14 offset:1024
	ds_read_b128 v[10:13], v14 offset:2048
	ds_read_b128 v[14:17], v14 offset:3072
	ds_read_b128 v[18:21], v30
	ds_read_b128 v[22:25], v30 offset:1024
	ds_read_b128 v[26:29], v30 offset:2048
	ds_read_b128 v[30:33], v30 offset:3072
	s_add_u32 s56, s56, 0x40000
	s_addc_u32 s57, s57, 0
	s_mov_b32 m0, s63
	v_lshl_add_u64 v[216:217], s[56:57], 0, v[164:165]
	ds_read_b128 v[192:195], v188 offset:32768
	ds_read_b128 v[196:199], v188 offset:33792
	ds_read_b128 v[200:203], v188 offset:34816
	ds_read_b128 v[204:207], v188 offset:35840
	ds_read_b128 v[208:211], v188 offset:36864
	ds_read_b128 v[212:215], v188 offset:37888
	ds_read_b128 v[220:223], v188 offset:38912
	ds_read_b128 v[224:227], v188 offset:39936
	global_load_lds_dwordx4 v[216:217], off
	v_lshl_add_u64 v[216:217], s[56:57], 0, v[166:167]
	s_mov_b32 m0, s64
	s_nop 0
	global_load_lds_dwordx4 v[216:217], off
	s_waitcnt vmcnt(8)
	s_waitcnt lgkmcnt(0)
	s_barrier
	s_waitcnt lgkmcnt(0)
	v_mfma_scale_f32_16x16x128_f8f6f4 v[158:161], v[2:9], v[192:199], v[158:161], v189, v190 op_sel_hi:[0,0,0]
	v_mfma_scale_f32_16x16x128_f8f6f4 v[150:153], v[10:17], v[192:199], v[150:153], v189, v190 op_sel_hi:[0,0,0]
	v_mfma_scale_f32_16x16x128_f8f6f4 v[142:145], v[2:9], v[200:207], v[142:145], v189, v190 op_sel_hi:[0,0,0]
	v_mfma_scale_f32_16x16x128_f8f6f4 v[134:137], v[10:17], v[200:207], v[134:137], v189, v190 op_sel_hi:[0,0,0]
	v_mfma_scale_f32_16x16x128_f8f6f4 v[126:129], v[2:9], v[208:215], v[126:129], v189, v190 op_sel_hi:[0,0,0]
	v_mfma_scale_f32_16x16x128_f8f6f4 v[118:121], v[10:17], v[208:215], v[118:121], v189, v190 op_sel_hi:[0,0,0]
	v_mfma_scale_f32_16x16x128_f8f6f4 v[110:113], v[2:9], v[220:227], v[110:113], v189, v190 op_sel_hi:[0,0,0]
	v_mfma_scale_f32_16x16x128_f8f6f4 v[102:105], v[10:17], v[220:227], v[102:105], v189, v190 op_sel_hi:[0,0,0]
	v_mfma_scale_f32_16x16x128_f8f6f4 v[154:157], v[18:25], v[192:199], v[154:157], v189, v190 op_sel_hi:[0,0,0]
	v_mfma_scale_f32_16x16x128_f8f6f4 v[146:149], v[26:33], v[192:199], v[146:149], v189, v190 op_sel_hi:[0,0,0]
	v_mfma_scale_f32_16x16x128_f8f6f4 v[138:141], v[18:25], v[200:207], v[138:141], v189, v190 op_sel_hi:[0,0,0]
	v_mfma_scale_f32_16x16x128_f8f6f4 v[130:133], v[26:33], v[200:207], v[130:133], v189, v190 op_sel_hi:[0,0,0]
	v_mfma_scale_f32_16x16x128_f8f6f4 v[122:125], v[18:25], v[208:215], v[122:125], v189, v190 op_sel_hi:[0,0,0]
	v_mfma_scale_f32_16x16x128_f8f6f4 v[114:117], v[26:33], v[208:215], v[114:117], v189, v190 op_sel_hi:[0,0,0]
	v_mfma_scale_f32_16x16x128_f8f6f4 v[106:109], v[18:25], v[220:227], v[106:109], v189, v190 op_sel_hi:[0,0,0]
	v_mfma_scale_f32_16x16x128_f8f6f4 v[98:101], v[26:33], v[220:227], v[98:101], v189, v190 op_sel_hi:[0,0,0]
	s_barrier
	s_add_i32 s56, s73, s61
	v_lshl_add_u64 v[216:217], v[178:179], 0, s[20:21]
	s_mov_b32 m0, s56
	ds_read_b128 v[192:195], v188 offset:49152
	ds_read_b128 v[196:199], v188 offset:50176
	ds_read_b128 v[200:203], v188 offset:51200
	ds_read_b128 v[204:207], v188 offset:52224
	ds_read_b128 v[208:211], v188 offset:53248
	ds_read_b128 v[212:215], v188 offset:54272
	ds_read_b128 v[220:223], v188 offset:55296
	ds_read_b128 v[224:227], v188 offset:56320
	global_load_lds_dwordx4 v[216:217], off
	v_lshl_add_u64 v[216:217], v[178:179], 0, s[22:23]
	s_add_i32 m0, s56, 0x2000
	s_add_i32 s56, s74, s61
	global_load_lds_dwordx4 v[216:217], off
	v_lshl_add_u64 v[216:217], v[178:179], 0, s[26:27]
	s_mov_b32 m0, s56
	v_lshl_add_u64 v[178:179], v[178:179], 0, s[36:37]
	global_load_lds_dwordx4 v[216:217], off
	s_add_i32 m0, s56, 0x2000
	s_nop 0
	global_load_lds_dwordx4 v[178:179], off
	v_lshl_add_u64 v[178:179], v[180:181], 0, s[24:25]
	s_mov_b32 m0, s66
	s_nop 0
	global_load_lds_dwordx4 v[178:179], off
	v_lshl_add_u64 v[178:179], v[182:183], 0, s[24:25]
	s_mov_b32 m0, s67
	s_nop 0
	global_load_lds_dwordx4 v[178:179], off
	s_waitcnt vmcnt(8)
	s_waitcnt lgkmcnt(0)
	s_barrier
	s_waitcnt lgkmcnt(0)
	v_mfma_scale_f32_16x16x128_f8f6f4 v[94:97], v[2:9], v[192:199], v[94:97], v189, v190 op_sel_hi:[0,0,0]
	v_mfma_scale_f32_16x16x128_f8f6f4 v[86:89], v[10:17], v[192:199], v[86:89], v189, v190 op_sel_hi:[0,0,0]
	v_mfma_scale_f32_16x16x128_f8f6f4 v[78:81], v[2:9], v[200:207], v[78:81], v189, v190 op_sel_hi:[0,0,0]
	v_mfma_scale_f32_16x16x128_f8f6f4 v[70:73], v[10:17], v[200:207], v[70:73], v189, v190 op_sel_hi:[0,0,0]
	v_mfma_scale_f32_16x16x128_f8f6f4 v[62:65], v[2:9], v[208:215], v[62:65], v189, v190 op_sel_hi:[0,0,0]
	v_mfma_scale_f32_16x16x128_f8f6f4 v[54:57], v[10:17], v[208:215], v[54:57], v189, v190 op_sel_hi:[0,0,0]
	v_mfma_scale_f32_16x16x128_f8f6f4 v[46:49], v[2:9], v[220:227], v[46:49], v189, v190 op_sel_hi:[0,0,0]
	v_mfma_scale_f32_16x16x128_f8f6f4 v[38:41], v[10:17], v[220:227], v[38:41], v189, v190 op_sel_hi:[0,0,0]
	v_mfma_scale_f32_16x16x128_f8f6f4 v[90:93], v[18:25], v[192:199], v[90:93], v189, v190 op_sel_hi:[0,0,0]
	v_mfma_scale_f32_16x16x128_f8f6f4 v[82:85], v[26:33], v[192:199], v[82:85], v189, v190 op_sel_hi:[0,0,0]
	v_mfma_scale_f32_16x16x128_f8f6f4 v[74:77], v[18:25], v[200:207], v[74:77], v189, v190 op_sel_hi:[0,0,0]
	v_mfma_scale_f32_16x16x128_f8f6f4 v[66:69], v[26:33], v[200:207], v[66:69], v189, v190 op_sel_hi:[0,0,0]
	v_mfma_scale_f32_16x16x128_f8f6f4 v[58:61], v[18:25], v[208:215], v[58:61], v189, v190 op_sel_hi:[0,0,0]
	v_mfma_scale_f32_16x16x128_f8f6f4 v[50:53], v[26:33], v[208:215], v[50:53], v189, v190 op_sel_hi:[0,0,0]
	v_mfma_scale_f32_16x16x128_f8f6f4 v[42:45], v[18:25], v[220:227], v[42:45], v189, v190 op_sel_hi:[0,0,0]
	v_mfma_scale_f32_16x16x128_f8f6f4 v[34:37], v[26:33], v[220:227], v[34:37], v189, v190 op_sel_hi:[0,0,0]
	s_barrier
	s_add_i32 s49, s49, 2
	s_add_u32 s4, s4, 0x100
	s_addc_u32 s5, s5, 0
	s_cmp_gt_u32 s49, 13
	v_lshl_add_u64 v[176:177], v[176:177], 0, s[40:41]
	s_cbranch_scc0 .LBB0_1497
	s_setprio 0
	s_and_b64 vcc, exec, s[38:39]
	s_cbranch_vccz .LBB0_1500
	s_barrier

.LBB0_1567:
	s_add_u32 s56, s56, 0xb0080
	v_mov_b32_e32 v34, 0
	v_lshl_add_u64 v[176:177], v[2:3], 0, s[44:45]
	s_addc_u32 s57, s57, 0
	s_mov_b32 s53, -2
	v_mov_b32_e32 v35, v34
	v_mov_b32_e32 v36, v34
	v_mov_b32_e32 v37, v34
	v_mov_b32_e32 v38, v34
	v_mov_b32_e32 v39, v34
	v_mov_b32_e32 v40, v34
	v_mov_b32_e32 v41, v34
	v_mov_b32_e32 v42, v34
	v_mov_b32_e32 v43, v34
	v_mov_b32_e32 v44, v34
	v_mov_b32_e32 v45, v34
	v_mov_b32_e32 v50, v34
	v_mov_b32_e32 v51, v34
	v_mov_b32_e32 v52, v34
	v_mov_b32_e32 v53, v34
	v_mov_b32_e32 v58, v34
	v_mov_b32_e32 v59, v34
	v_mov_b32_e32 v60, v34
	v_mov_b32_e32 v61, v34
	v_mov_b32_e32 v66, v34
	v_mov_b32_e32 v67, v34
	v_mov_b32_e32 v68, v34
	v_mov_b32_e32 v69, v34
	v_mov_b32_e32 v74, v34
	v_mov_b32_e32 v75, v34
	v_mov_b32_e32 v76, v34
	v_mov_b32_e32 v77, v34
	v_mov_b32_e32 v82, v34
	v_mov_b32_e32 v83, v34
	v_mov_b32_e32 v84, v34
	v_mov_b32_e32 v85, v34
	v_mov_b32_e32 v46, v34
	v_mov_b32_e32 v47, v34
	v_mov_b32_e32 v48, v34
	v_mov_b32_e32 v49, v34
	v_mov_b32_e32 v54, v34
	v_mov_b32_e32 v55, v34
	v_mov_b32_e32 v56, v34
	v_mov_b32_e32 v57, v34
	v_mov_b32_e32 v62, v34
	v_mov_b32_e32 v63, v34
	v_mov_b32_e32 v64, v34
	v_mov_b32_e32 v65, v34
	v_mov_b32_e32 v70, v34
	v_mov_b32_e32 v71, v34
	v_mov_b32_e32 v72, v34
	v_mov_b32_e32 v73, v34
	v_mov_b32_e32 v78, v34
	v_mov_b32_e32 v79, v34
	v_mov_b32_e32 v80, v34
	v_mov_b32_e32 v81, v34
	v_mov_b32_e32 v86, v34
	v_mov_b32_e32 v87, v34
	v_mov_b32_e32 v88, v34
	v_mov_b32_e32 v89, v34
	v_mov_b32_e32 v90, v34
	v_mov_b32_e32 v91, v34
	v_mov_b32_e32 v92, v34
	v_mov_b32_e32 v93, v34
	v_mov_b32_e32 v94, v34
	v_mov_b32_e32 v95, v34
	v_mov_b32_e32 v96, v34
	v_mov_b32_e32 v97, v34
	v_mov_b32_e32 v98, v34
	v_mov_b32_e32 v99, v34
	v_mov_b32_e32 v100, v34
	v_mov_b32_e32 v101, v34
	v_mov_b32_e32 v102, v34
	v_mov_b32_e32 v103, v34
	v_mov_b32_e32 v104, v34
	v_mov_b32_e32 v105, v34
	v_mov_b32_e32 v106, v34
	v_mov_b32_e32 v107, v34
	v_mov_b32_e32 v108, v34
	v_mov_b32_e32 v109, v34
	v_mov_b32_e32 v114, v34
	v_mov_b32_e32 v115, v34
	v_mov_b32_e32 v116, v34
	v_mov_b32_e32 v117, v34
	v_mov_b32_e32 v122, v34
	v_mov_b32_e32 v123, v34
	v_mov_b32_e32 v124, v34
	v_mov_b32_e32 v125, v34
	v_mov_b32_e32 v130, v34
	v_mov_b32_e32 v131, v34
	v_mov_b32_e32 v132, v34
	v_mov_b32_e32 v133, v34
	v_mov_b32_e32 v138, v34
	v_mov_b32_e32 v139, v34
	v_mov_b32_e32 v140, v34
	v_mov_b32_e32 v141, v34
	v_mov_b32_e32 v146, v34
	v_mov_b32_e32 v147, v34
	v_mov_b32_e32 v148, v34
	v_mov_b32_e32 v149, v34
	v_mov_b32_e32 v110, v34
	v_mov_b32_e32 v111, v34
	v_mov_b32_e32 v112, v34
	v_mov_b32_e32 v113, v34
	v_mov_b32_e32 v118, v34
	v_mov_b32_e32 v119, v34
	v_mov_b32_e32 v120, v34
	v_mov_b32_e32 v121, v34
	v_mov_b32_e32 v126, v34
	v_mov_b32_e32 v127, v34
	v_mov_b32_e32 v128, v34
	v_mov_b32_e32 v129, v34
	v_mov_b32_e32 v134, v34
	v_mov_b32_e32 v135, v34
	v_mov_b32_e32 v136, v34
	v_mov_b32_e32 v137, v34
	v_mov_b32_e32 v142, v34
	v_mov_b32_e32 v143, v34
	v_mov_b32_e32 v144, v34
	v_mov_b32_e32 v145, v34
	v_mov_b32_e32 v150, v34
	v_mov_b32_e32 v151, v34
	v_mov_b32_e32 v152, v34
	v_mov_b32_e32 v153, v34
	v_mov_b32_e32 v154, v34
	v_mov_b32_e32 v155, v34
	v_mov_b32_e32 v156, v34
	v_mov_b32_e32 v157, v34
	v_mov_b32_e32 v158, v34
	v_mov_b32_e32 v159, v34
	v_mov_b32_e32 v160, v34
	v_mov_b32_e32 v161, v34
	v_readfirstlane_b32 s98, v0
	s_lshr_b32 s98, s98, 8
	s_cmp_eq_u32 s98, 1
	s_cbranch_scc0 .Lprio_skip0
	s_setprio 1
.Lprio_skip0:
.LBB0_1568:
	ds_read_b128 v[26:29], v186
	ds_read_b128 v[30:33], v186 offset:1024
	ds_read_b128 v[18:21], v186 offset:2048
	ds_read_b128 v[22:25], v186 offset:3072
	ds_read_b128 v[10:13], v187
	ds_read_b128 v[14:17], v187 offset:1024
	ds_read_b128 v[2:5], v187 offset:2048
	ds_read_b128 v[6:9], v187 offset:3072
	s_add_u32 s58, s56, 0xfff50080
	s_addc_u32 s59, s57, -1
	s_cmp_eq_u32 s53, 40
	s_cselect_b64 vcc, -1, 0
	s_cselect_b32 s59, s5, s59
	s_cselect_b32 s58, s4, s58
	v_cndmask_b32_e32 v179, v177, v175, vcc
	v_cndmask_b32_e32 v178, v176, v174, vcc
	v_lshl_add_u64 v[180:181], s[56:57], 0, v[170:171]
	s_add_i32 m0, s61, 0xc000
	ds_read_b128 v[192:195], v188
	ds_read_b128 v[196:199], v188 offset:1024
	ds_read_b128 v[200:203], v188 offset:2048
	ds_read_b128 v[204:207], v188 offset:3072
	ds_read_b128 v[208:211], v188 offset:4096
	ds_read_b128 v[212:215], v188 offset:5120
	ds_read_b128 v[220:223], v188 offset:6144
	ds_read_b128 v[224:227], v188 offset:7168
	global_load_lds_dwordx4 v[180:181], off
	v_lshl_add_u64 v[180:181], s[56:57], 0, v[172:173]
	s_add_i32 m0, s61, 0xe000
	s_nop 0
	global_load_lds_dwordx4 v[180:181], off
	s_waitcnt vmcnt(8)
	s_waitcnt lgkmcnt(0)
	s_barrier
	s_waitcnt lgkmcnt(0)
	v_mfma_scale_f32_16x16x128_f8f6f4 v[158:161], v[26:33], v[192:199], v[158:161], v189, v190 op_sel_hi:[0,0,0]
	v_mfma_scale_f32_16x16x128_f8f6f4 v[154:157], v[18:25], v[192:199], v[154:157], v189, v190 op_sel_hi:[0,0,0]
	v_mfma_scale_f32_16x16x128_f8f6f4 v[150:153], v[26:33], v[200:207], v[150:153], v189, v190 op_sel_hi:[0,0,0]
	v_mfma_scale_f32_16x16x128_f8f6f4 v[142:145], v[18:25], v[200:207], v[142:145], v189, v190 op_sel_hi:[0,0,0]
	v_mfma_scale_f32_16x16x128_f8f6f4 v[134:137], v[26:33], v[208:215], v[134:137], v189, v190 op_sel_hi:[0,0,0]
	v_mfma_scale_f32_16x16x128_f8f6f4 v[126:129], v[18:25], v[208:215], v[126:129], v189, v190 op_sel_hi:[0,0,0]
	v_mfma_scale_f32_16x16x128_f8f6f4 v[118:121], v[26:33], v[220:227], v[118:121], v189, v190 op_sel_hi:[0,0,0]
	v_mfma_scale_f32_16x16x128_f8f6f4 v[110:113], v[18:25], v[220:227], v[110:113], v189, v190 op_sel_hi:[0,0,0]
	v_mfma_scale_f32_16x16x128_f8f6f4 v[146:149], v[10:17], v[192:199], v[146:149], v189, v190 op_sel_hi:[0,0,0]
	v_mfma_scale_f32_16x16x128_f8f6f4 v[138:141], v[2:9], v[192:199], v[138:141], v189, v190 op_sel_hi:[0,0,0]
	v_mfma_scale_f32_16x16x128_f8f6f4 v[130:133], v[10:17], v[200:207], v[130:133], v189, v190 op_sel_hi:[0,0,0]
	v_mfma_scale_f32_16x16x128_f8f6f4 v[122:125], v[2:9], v[200:207], v[122:125], v189, v190 op_sel_hi:[0,0,0]
	v_mfma_scale_f32_16x16x128_f8f6f4 v[114:117], v[10:17], v[208:215], v[114:117], v189, v190 op_sel_hi:[0,0,0]
	v_mfma_scale_f32_16x16x128_f8f6f4 v[106:109], v[2:9], v[208:215], v[106:109], v189, v190 op_sel_hi:[0,0,0]
	v_mfma_scale_f32_16x16x128_f8f6f4 v[102:105], v[10:17], v[220:227], v[102:105], v189, v190 op_sel_hi:[0,0,0]
	v_mfma_scale_f32_16x16x128_f8f6f4 v[98:101], v[2:9], v[220:227], v[98:101], v189, v190 op_sel_hi:[0,0,0]
	s_barrier
	s_add_i32 s80, s69, s33
	v_lshl_add_u64 v[178:179], v[178:179], 0, v[164:165]
	s_mov_b32 m0, s80
	ds_read_b128 v[192:195], v188 offset:16384
	ds_read_b128 v[196:199], v188 offset:17408
	ds_read_b128 v[200:203], v188 offset:18432
	ds_read_b128 v[204:207], v188 offset:19456
	ds_read_b128 v[208:211], v188 offset:20480
	ds_read_b128 v[212:215], v188 offset:21504
	ds_read_b128 v[220:223], v188 offset:22528
	ds_read_b128 v[224:227], v188 offset:23552
	global_load_lds_dwordx4 v[178:179], off
	v_lshl_add_u64 v[180:181], v[178:179], 0, s[10:11]
	s_add_i32 m0, s80, 0x2000
	s_add_i32 s80, s70, s33
	global_load_lds_dwordx4 v[180:181], off
	v_lshl_add_u64 v[180:181], v[178:179], 0, s[12:13]
	s_mov_b32 m0, s80
	v_lshl_add_u64 v[182:183], s[58:59], 0, v[168:169]
	global_load_lds_dwordx4 v[180:181], off
	v_lshl_add_u64 v[180:181], v[178:179], 0, s[14:15]
	s_add_i32 m0, s80, 0x2000
	s_nop 0
	global_load_lds_dwordx4 v[180:181], off
	v_lshl_add_u64 v[180:181], s[58:59], 0, v[166:167]
	s_mov_b32 m0, s61
	s_nop 0
	global_load_lds_dwordx4 v[180:181], off
	s_mov_b32 m0, s62
	s_nop 0
	global_load_lds_dwordx4 v[182:183], off
	s_waitcnt vmcnt(8)
	s_waitcnt lgkmcnt(0)
	s_barrier
	s_waitcnt lgkmcnt(0)
	v_mfma_scale_f32_16x16x128_f8f6f4 v[94:97], v[26:33], v[192:199], v[94:97], v189, v190 op_sel_hi:[0,0,0]
	v_mfma_scale_f32_16x16x128_f8f6f4 v[90:93], v[18:25], v[192:199], v[90:93], v189, v190 op_sel_hi:[0,0,0]
	v_mfma_scale_f32_16x16x128_f8f6f4 v[86:89], v[26:33], v[200:207], v[86:89], v189, v190 op_sel_hi:[0,0,0]
	v_mfma_scale_f32_16x16x128_f8f6f4 v[78:81], v[18:25], v[200:207], v[78:81], v189, v190 op_sel_hi:[0,0,0]
	v_mfma_scale_f32_16x16x128_f8f6f4 v[70:73], v[26:33], v[208:215], v[70:73], v189, v190 op_sel_hi:[0,0,0]
	v_mfma_scale_f32_16x16x128_f8f6f4 v[62:65], v[18:25], v[208:215], v[62:65], v189, v190 op_sel_hi:[0,0,0]
	v_mfma_scale_f32_16x16x128_f8f6f4 v[54:57], v[26:33], v[220:227], v[54:57], v189, v190 op_sel_hi:[0,0,0]
	v_mfma_scale_f32_16x16x128_f8f6f4 v[46:49], v[18:25], v[220:227], v[46:49], v189, v190 op_sel_hi:[0,0,0]
	v_mfma_scale_f32_16x16x128_f8f6f4 v[82:85], v[10:17], v[192:199], v[82:85], v189, v190 op_sel_hi:[0,0,0]
	v_mfma_scale_f32_16x16x128_f8f6f4 v[74:77], v[2:9], v[192:199], v[74:77], v189, v190 op_sel_hi:[0,0,0]
	v_mfma_scale_f32_16x16x128_f8f6f4 v[66:69], v[10:17], v[200:207], v[66:69], v189, v190 op_sel_hi:[0,0,0]
	v_mfma_scale_f32_16x16x128_f8f6f4 v[58:61], v[2:9], v[200:207], v[58:61], v189, v190 op_sel_hi:[0,0,0]
	v_mfma_scale_f32_16x16x128_f8f6f4 v[50:53], v[10:17], v[208:215], v[50:53], v189, v190 op_sel_hi:[0,0,0]
	v_mfma_scale_f32_16x16x128_f8f6f4 v[42:45], v[2:9], v[208:215], v[42:45], v189, v190 op_sel_hi:[0,0,0]
	v_mfma_scale_f32_16x16x128_f8f6f4 v[38:41], v[10:17], v[220:227], v[38:41], v189, v190 op_sel_hi:[0,0,0]
	v_mfma_scale_f32_16x16x128_f8f6f4 v[34:37], v[2:9], v[220:227], v[34:37], v189, v190 op_sel_hi:[0,0,0]
	s_barrier
	s_add_i32 s80, 0, 0x18000
	s_add_i32 s81, 0, 0x1c000
	v_add_u32_e32 v14, s80, v184
	v_add_u32_e32 v30, s81, v184
	ds_read_b128 v[2:5], v14
	ds_read_b128 v[6:9], v14 offset:1024
	ds_read_b128 v[10:13], v14 offset:2048
	ds_read_b128 v[14:17], v14 offset:3072
	ds_read_b128 v[18:21], v30
	ds_read_b128 v[22:25], v30 offset:1024
	ds_read_b128 v[26:29], v30 offset:2048
	ds_read_b128 v[30:33], v30 offset:3072
	s_add_u32 s58, s58, 0xb0000
	s_addc_u32 s59, s59, 0
	s_mov_b32 m0, s63
	v_lshl_add_u64 v[216:217], s[58:59], 0, v[166:167]
	ds_read_b128 v[192:195], v188 offset:32768
	ds_read_b128 v[196:199], v188 offset:33792
	ds_read_b128 v[200:203], v188 offset:34816
	ds_read_b128 v[204:207], v188 offset:35840
	ds_read_b128 v[208:211], v188 offset:36864
	ds_read_b128 v[212:215], v188 offset:37888
	ds_read_b128 v[220:223], v188 offset:38912
	ds_read_b128 v[224:227], v188 offset:39936
	global_load_lds_dwordx4 v[216:217], off
	v_lshl_add_u64 v[216:217], s[58:59], 0, v[168:169]
	s_mov_b32 m0, s64
	s_nop 0
	global_load_lds_dwordx4 v[216:217], off
	s_waitcnt vmcnt(8)
	s_waitcnt lgkmcnt(0)
	s_barrier
	s_waitcnt lgkmcnt(0)
	v_mfma_scale_f32_16x16x128_f8f6f4 v[158:161], v[2:9], v[192:199], v[158:161], v189, v190 op_sel_hi:[0,0,0]
	v_mfma_scale_f32_16x16x128_f8f6f4 v[154:157], v[10:17], v[192:199], v[154:157], v189, v190 op_sel_hi:[0,0,0]
	v_mfma_scale_f32_16x16x128_f8f6f4 v[150:153], v[2:9], v[200:207], v[150:153], v189, v190 op_sel_hi:[0,0,0]
	v_mfma_scale_f32_16x16x128_f8f6f4 v[142:145], v[10:17], v[200:207], v[142:145], v189, v190 op_sel_hi:[0,0,0]
	v_mfma_scale_f32_16x16x128_f8f6f4 v[134:137], v[2:9], v[208:215], v[134:137], v189, v190 op_sel_hi:[0,0,0]
	v_mfma_scale_f32_16x16x128_f8f6f4 v[126:129], v[10:17], v[208:215], v[126:129], v189, v190 op_sel_hi:[0,0,0]
	v_mfma_scale_f32_16x16x128_f8f6f4 v[118:121], v[2:9], v[220:227], v[118:121], v189, v190 op_sel_hi:[0,0,0]
	v_mfma_scale_f32_16x16x128_f8f6f4 v[110:113], v[10:17], v[220:227], v[110:113], v189, v190 op_sel_hi:[0,0,0]
	v_mfma_scale_f32_16x16x128_f8f6f4 v[146:149], v[18:25], v[192:199], v[146:149], v189, v190 op_sel_hi:[0,0,0]
	v_mfma_scale_f32_16x16x128_f8f6f4 v[138:141], v[26:33], v[192:199], v[138:141], v189, v190 op_sel_hi:[0,0,0]
	v_mfma_scale_f32_16x16x128_f8f6f4 v[130:133], v[18:25], v[200:207], v[130:133], v189, v190 op_sel_hi:[0,0,0]
	v_mfma_scale_f32_16x16x128_f8f6f4 v[122:125], v[26:33], v[200:207], v[122:125], v189, v190 op_sel_hi:[0,0,0]
	v_mfma_scale_f32_16x16x128_f8f6f4 v[114:117], v[18:25], v[208:215], v[114:117], v189, v190 op_sel_hi:[0,0,0]
	v_mfma_scale_f32_16x16x128_f8f6f4 v[106:109], v[26:33], v[208:215], v[106:109], v189, v190 op_sel_hi:[0,0,0]
	v_mfma_scale_f32_16x16x128_f8f6f4 v[102:105], v[18:25], v[220:227], v[102:105], v189, v190 op_sel_hi:[0,0,0]
	v_mfma_scale_f32_16x16x128_f8f6f4 v[98:101], v[26:33], v[220:227], v[98:101], v189, v190 op_sel_hi:[0,0,0]
	s_barrier
	s_add_i32 s58, s80, s33
	v_lshl_add_u64 v[216:217], v[178:179], 0, s[24:25]
	s_mov_b32 m0, s58
	ds_read_b128 v[192:195], v188 offset:49152
	ds_read_b128 v[196:199], v188 offset:50176
	ds_read_b128 v[200:203], v188 offset:51200
	ds_read_b128 v[204:207], v188 offset:52224
	ds_read_b128 v[208:211], v188 offset:53248
	ds_read_b128 v[212:215], v188 offset:54272
	ds_read_b128 v[220:223], v188 offset:55296
	ds_read_b128 v[224:227], v188 offset:56320
	global_load_lds_dwordx4 v[216:217], off
	v_lshl_add_u64 v[216:217], v[178:179], 0, s[26:27]
	s_add_i32 m0, s58, 0x2000
	s_add_i32 s58, s81, s33
	global_load_lds_dwordx4 v[216:217], off
	v_lshl_add_u64 v[216:217], v[178:179], 0, s[38:39]
	s_mov_b32 m0, s58
	v_lshl_add_u64 v[178:179], v[178:179], 0, s[40:41]
	global_load_lds_dwordx4 v[216:217], off
	s_add_i32 m0, s58, 0x2000
	s_nop 0
	global_load_lds_dwordx4 v[178:179], off
	v_lshl_add_u64 v[178:179], v[180:181], 0, s[36:37]
	s_mov_b32 m0, s66
	s_nop 0
	global_load_lds_dwordx4 v[178:179], off
	v_lshl_add_u64 v[178:179], v[182:183], 0, s[36:37]
	s_mov_b32 m0, s67
	s_nop 0
	global_load_lds_dwordx4 v[178:179], off
	s_waitcnt vmcnt(8)
	s_waitcnt lgkmcnt(0)
	s_barrier
	s_waitcnt lgkmcnt(0)
	v_mfma_scale_f32_16x16x128_f8f6f4 v[94:97], v[2:9], v[192:199], v[94:97], v189, v190 op_sel_hi:[0,0,0]
	v_mfma_scale_f32_16x16x128_f8f6f4 v[90:93], v[10:17], v[192:199], v[90:93], v189, v190 op_sel_hi:[0,0,0]
	v_mfma_scale_f32_16x16x128_f8f6f4 v[86:89], v[2:9], v[200:207], v[86:89], v189, v190 op_sel_hi:[0,0,0]
	v_mfma_scale_f32_16x16x128_f8f6f4 v[78:81], v[10:17], v[200:207], v[78:81], v189, v190 op_sel_hi:[0,0,0]
	v_mfma_scale_f32_16x16x128_f8f6f4 v[70:73], v[2:9], v[208:215], v[70:73], v189, v190 op_sel_hi:[0,0,0]
	v_mfma_scale_f32_16x16x128_f8f6f4 v[62:65], v[10:17], v[208:215], v[62:65], v189, v190 op_sel_hi:[0,0,0]
	v_mfma_scale_f32_16x16x128_f8f6f4 v[54:57], v[2:9], v[220:227], v[54:57], v189, v190 op_sel_hi:[0,0,0]
	v_mfma_scale_f32_16x16x128_f8f6f4 v[46:49], v[10:17], v[220:227], v[46:49], v189, v190 op_sel_hi:[0,0,0]
	v_mfma_scale_f32_16x16x128_f8f6f4 v[82:85], v[18:25], v[192:199], v[82:85], v189, v190 op_sel_hi:[0,0,0]
	v_mfma_scale_f32_16x16x128_f8f6f4 v[74:77], v[26:33], v[192:199], v[74:77], v189, v190 op_sel_hi:[0,0,0]
	v_mfma_scale_f32_16x16x128_f8f6f4 v[66:69], v[18:25], v[200:207], v[66:69], v189, v190 op_sel_hi:[0,0,0]
	v_mfma_scale_f32_16x16x128_f8f6f4 v[58:61], v[26:33], v[200:207], v[58:61], v189, v190 op_sel_hi:[0,0,0]
	v_mfma_scale_f32_16x16x128_f8f6f4 v[50:53], v[18:25], v[208:215], v[50:53], v189, v190 op_sel_hi:[0,0,0]
	v_mfma_scale_f32_16x16x128_f8f6f4 v[42:45], v[26:33], v[208:215], v[42:45], v189, v190 op_sel_hi:[0,0,0]
	v_mfma_scale_f32_16x16x128_f8f6f4 v[38:41], v[18:25], v[220:227], v[38:41], v189, v190 op_sel_hi:[0,0,0]
	v_mfma_scale_f32_16x16x128_f8f6f4 v[34:37], v[26:33], v[220:227], v[34:37], v189, v190 op_sel_hi:[0,0,0]
	s_barrier
	s_add_i32 s53, s53, 2
	s_add_u32 s56, s56, 0x100
	s_addc_u32 s57, s57, 0
	s_cmp_gt_u32 s53, 41
	v_lshl_add_u64 v[176:177], v[176:177], 0, s[44:45]
	s_cbranch_scc0 .LBB0_1568
	s_setprio 0
	s_and_b64 vcc, exec, s[42:43]
	s_cbranch_vccz .LBB0_1571
	s_barrier
